# batch: P9/P10 bias loads hoisted above the epilogue barrier, expert search by ballot, moe tables built once, sc1 on bf16 GEMM epilogue stores (on top of P5 wait + P9 gather DMA)
# baseline (speedup 1.0000x reference)
.LBB0_184:
	v_add_u32_e32 v136, s29, v231
	v_ashrrev_i32_e32 v137, 31, v136
	v_ashrrev_i32_e32 v5, 31, v4
	v_lshl_add_u64 v[136:137], v[136:137], 1, s[38:39]
	v_mul_lo_u32 v7, s37, v4
	v_mul_lo_u32 v5, s36, v5
	v_mad_u64_u32 v[138:139], s[38:39], s36, v4, 0
	v_add3_u32 v139, v139, v5, v7
	v_lshl_add_u64 v[142:143], v[138:139], 1, v[136:137]
	v_or_b32_e32 v7, 16, v4
	v_cvt_pk_bf16_f32 v138, v72, v73
	v_cvt_pk_bf16_f32 v139, v74, v75
	v_cvt_pk_bf16_f32 v140, v68, v69
	v_cvt_pk_bf16_f32 v141, v70, v71
	global_store_dwordx4 v[142:143], v[138:141], off sc1
	v_cvt_pk_bf16_f32 v132, v132, v133
	v_cvt_pk_bf16_f32 v133, v134, v135
	v_cvt_pk_bf16_f32 v134, v128, v129
	v_cvt_pk_bf16_f32 v135, v130, v131
	v_mul_lo_u32 v130, s37, v7
	v_mad_u64_u32 v[128:129], s[38:39], s36, v7, 0
	v_add3_u32 v129, v129, v5, v130
	global_store_dwordx4 v[142:143], v[132:135], off offset:256 sc1
	v_or_b32_e32 v7, 32, v4
	s_nop 0
	v_lshl_add_u64 v[132:133], v[128:129], 1, v[136:137]
	v_cvt_pk_bf16_f32 v128, v60, v61
	v_cvt_pk_bf16_f32 v129, v62, v63
	v_cvt_pk_bf16_f32 v130, v56, v57
	v_cvt_pk_bf16_f32 v131, v58, v59
	global_store_dwordx4 v[132:133], v[128:131], off sc1
	v_cvt_pk_bf16_f32 v124, v124, v125
	v_cvt_pk_bf16_f32 v125, v126, v127
	v_cvt_pk_bf16_f32 v126, v120, v121
	v_cvt_pk_bf16_f32 v127, v122, v123
	v_mul_lo_u32 v122, s37, v7
	v_mad_u64_u32 v[120:121], s[38:39], s36, v7, 0
	v_add3_u32 v121, v121, v5, v122
	global_store_dwordx4 v[132:133], v[124:127], off offset:256 sc1
	v_or_b32_e32 v7, 48, v4
	s_nop 0
	v_lshl_add_u64 v[124:125], v[120:121], 1, v[136:137]
	v_cvt_pk_bf16_f32 v120, v52, v53
	v_cvt_pk_bf16_f32 v121, v54, v55
	v_cvt_pk_bf16_f32 v122, v48, v49
	v_cvt_pk_bf16_f32 v123, v50, v51
	global_store_dwordx4 v[124:125], v[120:123], off sc1
	v_cvt_pk_bf16_f32 v116, v116, v117
	v_cvt_pk_bf16_f32 v117, v118, v119
	v_cvt_pk_bf16_f32 v118, v112, v113
	v_cvt_pk_bf16_f32 v119, v114, v115
	v_mul_lo_u32 v114, s37, v7
	v_mad_u64_u32 v[112:113], s[38:39], s36, v7, 0
	v_add3_u32 v113, v113, v5, v114
	v_add_u32_e32 v5, 0x80, v4
	global_store_dwordx4 v[124:125], v[116:119], off offset:256 sc1
	v_ashrrev_i32_e32 v7, 31, v5
	v_mul_lo_u32 v7, s36, v7
	v_lshl_add_u64 v[116:117], v[112:113], 1, v[136:137]
	v_cvt_pk_bf16_f32 v112, v44, v45
	v_cvt_pk_bf16_f32 v113, v46, v47
	v_cvt_pk_bf16_f32 v114, v40, v41
	v_cvt_pk_bf16_f32 v115, v42, v43
	global_store_dwordx4 v[116:117], v[112:115], off sc1
	v_cvt_pk_bf16_f32 v108, v108, v109
	v_cvt_pk_bf16_f32 v109, v110, v111
	v_cvt_pk_bf16_f32 v110, v104, v105
	v_cvt_pk_bf16_f32 v111, v106, v107
	v_mul_lo_u32 v106, s37, v5
	v_mad_u64_u32 v[104:105], s[38:39], s36, v5, 0
	v_add3_u32 v105, v105, v7, v106
	v_add_u32_e32 v5, 0x90, v4
	global_store_dwordx4 v[116:117], v[108:111], off offset:256 sc1
	v_ashrrev_i32_e32 v7, 31, v5
	v_mul_lo_u32 v7, s36, v7
	v_lshl_add_u64 v[108:109], v[104:105], 1, v[136:137]
	v_cvt_pk_bf16_f32 v104, v36, v37
	v_cvt_pk_bf16_f32 v105, v38, v39
	v_cvt_pk_bf16_f32 v106, v32, v33
	v_cvt_pk_bf16_f32 v107, v34, v35
	global_store_dwordx4 v[108:109], v[104:107], off sc1
	v_cvt_pk_bf16_f32 v92, v92, v93
	v_cvt_pk_bf16_f32 v93, v94, v95
	v_cvt_pk_bf16_f32 v94, v88, v89
	v_cvt_pk_bf16_f32 v95, v90, v91
	v_mul_lo_u32 v90, s37, v5
	v_mad_u64_u32 v[88:89], s[38:39], s36, v5, 0
	v_add3_u32 v89, v89, v7, v90
	v_add_u32_e32 v5, 0xa0, v4
	global_store_dwordx4 v[108:109], v[92:95], off offset:256 sc1
	v_ashrrev_i32_e32 v7, 31, v5
	v_mul_lo_u32 v7, s36, v7
	v_lshl_add_u64 v[92:93], v[88:89], 1, v[136:137]
	v_cvt_pk_bf16_f32 v88, v28, v29
	v_cvt_pk_bf16_f32 v89, v30, v31
	v_cvt_pk_bf16_f32 v90, v24, v25
	v_cvt_pk_bf16_f32 v91, v26, v27
	global_store_dwordx4 v[92:93], v[88:91], off sc1
	v_cvt_pk_bf16_f32 v76, v76, v77
	v_cvt_pk_bf16_f32 v77, v78, v79
	v_cvt_pk_bf16_f32 v78, v64, v65
	v_cvt_pk_bf16_f32 v79, v66, v67
	v_mul_lo_u32 v66, s37, v5
	v_mad_u64_u32 v[64:65], s[38:39], s36, v5, 0
	v_add3_u32 v65, v65, v7, v66
	global_store_dwordx4 v[92:93], v[76:79], off offset:256 sc1
	v_add_u32_e32 v5, 0xb0, v4
	v_ashrrev_i32_e32 v7, 31, v5
	v_lshl_add_u64 v[76:77], v[64:65], 1, v[136:137]
	v_cvt_pk_bf16_f32 v64, v20, v21
	v_cvt_pk_bf16_f32 v65, v22, v23
	v_cvt_pk_bf16_f32 v66, v16, v17
	v_cvt_pk_bf16_f32 v67, v18, v19
	global_store_dwordx4 v[76:77], v[64:67], off sc1
	v_mul_lo_u32 v7, s36, v7
	s_nop 0
	v_cvt_pk_bf16_f32 v64, v100, v101
	v_cvt_pk_bf16_f32 v65, v102, v103
	v_cvt_pk_bf16_f32 v66, v96, v97
	v_cvt_pk_bf16_f32 v67, v98, v99
	global_store_dwordx4 v[76:77], v[64:67], off offset:256 sc1
	s_nop 1
	v_mul_lo_u32 v66, s37, v5
	v_mad_u64_u32 v[64:65], s[36:37], s36, v5, 0
	v_add3_u32 v65, v65, v7, v66
	v_lshl_add_u64 v[76:77], v[64:65], 1, v[136:137]
	v_cvt_pk_bf16_f32 v64, v12, v13
	v_cvt_pk_bf16_f32 v65, v14, v15
	v_cvt_pk_bf16_f32 v66, v8, v9
	v_cvt_pk_bf16_f32 v67, v10, v11
	global_store_dwordx4 v[76:77], v[64:67], off sc1
	s_nop 1
	v_cvt_pk_bf16_f32 v64, v84, v85
	v_cvt_pk_bf16_f32 v65, v86, v87
	v_cvt_pk_bf16_f32 v66, v80, v81
	v_cvt_pk_bf16_f32 v67, v82, v83
	global_store_dwordx4 v[76:77], v[64:67], off offset:256 sc1
	s_branch .LBB0_187
.LBB0_185:
	s_andn2_b64 vcc, exec, s[26:27]
	s_cbranch_vccnz .LBB0_187
	v_or_b32_e32 v66, 16, v4
	v_ashrrev_i32_e32 v5, 31, v4
	v_ashrrev_i32_e32 v67, 31, v66
	v_lshlrev_b64 v[64:65], 8, v[4:5]
	v_lshlrev_b64 v[66:67], 8, v[66:67]
	v_lshl_add_u64 v[64:65], v[208:209], 0, v[64:65]
	v_lshl_add_u64 v[66:67], v[208:209], 0, v[66:67]
	global_store_dwordx4 v[64:65], v[72:75], off sc1
	global_store_dwordx4 v[64:65], v[68:71], off offset:16 sc1
	global_store_dwordx4 v[66:67], v[60:63], off sc1
	global_store_dwordx4 v[66:67], v[56:59], off offset:16 sc1
	s_mov_b32 s29, 0x8000
	s_mov_b64 s[36:37], 0x8000
	v_or_b32_e32 v56, 32, v4
	v_or_b32_e32 v4, 48, v4
	v_ashrrev_i32_e32 v57, 31, v56
	v_ashrrev_i32_e32 v5, 31, v4
	v_lshlrev_b64 v[56:57], 8, v[56:57]
	v_lshlrev_b64 v[4:5], 8, v[4:5]
	v_lshl_add_u64 v[56:57], v[208:209], 0, v[56:57]
	v_lshl_add_u64 v[4:5], v[208:209], 0, v[4:5]
	global_store_dwordx4 v[56:57], v[52:55], off sc1
	global_store_dwordx4 v[56:57], v[48:51], off offset:16 sc1
	global_store_dwordx4 v[4:5], v[44:47], off sc1
	global_store_dwordx4 v[4:5], v[40:43], off offset:16 sc1
	v_lshl_add_u64 v[4:5], v[64:65], 0, s[36:37]
	s_mov_b64 s[36:37], 0x9000
	v_add_co_u32_e32 v40, vcc, s29, v64
	s_nop 1
	v_addc_co_u32_e32 v41, vcc, 0, v65, vcc
	global_store_dwordx4 v[40:41], v[36:39], off sc1
	global_store_dwordx4 v[4:5], v[32:35], off offset:16 sc1
	v_lshl_add_u64 v[4:5], v[64:65], 0, s[36:37]
	s_mov_b64 s[36:37], 0xa000
	v_add_co_u32_e32 v32, vcc, 0x9000, v64
	s_nop 1
	v_addc_co_u32_e32 v33, vcc, 0, v65, vcc
	global_store_dwordx4 v[32:33], v[28:31], off sc1
	global_store_dwordx4 v[4:5], v[24:27], off offset:16 sc1
	v_lshl_add_u64 v[4:5], v[64:65], 0, s[36:37]
	s_mov_b64 s[36:37], 0xb000
	v_add_co_u32_e32 v24, vcc, 0xa000, v64
	s_nop 1
	v_addc_co_u32_e32 v25, vcc, 0, v65, vcc
	global_store_dwordx4 v[24:25], v[20:23], off sc1
	global_store_dwordx4 v[4:5], v[16:19], off offset:16 sc1
	v_lshl_add_u64 v[4:5], v[64:65], 0, s[36:37]
	s_nop 0
	v_add_co_u32_e32 v16, vcc, 0xb000, v64
	s_nop 1
	v_addc_co_u32_e32 v17, vcc, 0, v65, vcc
	global_store_dwordx4 v[16:17], v[12:15], off sc1
	global_store_dwordx4 v[4:5], v[8:11], off offset:16 sc1

.LBB0_238:
	v_add_u32_e32 v4, s31, v220
	v_ashrrev_i32_e32 v5, 31, v4
	v_ashrrev_i32_e32 v3, 31, v2
	v_lshl_add_u64 v[4:5], v[4:5], 1, s[40:41]
	v_mul_lo_u32 v8, s39, v2
	v_mul_lo_u32 v3, s38, v3
	v_mad_u64_u32 v[6:7], s[40:41], s38, v2, 0
	v_add3_u32 v7, v7, v3, v8
	v_lshl_add_u64 v[10:11], v[6:7], 1, v[4:5]
	v_pk_mul_f32 v[6:7], v[132:133], s[16:17] op_sel_hi:[1,0]
	v_pk_mul_f32 v[8:9], v[134:135], s[16:17] op_sel_hi:[1,0]
	v_cvt_pk_bf16_f32 v6, v6, v7
	v_pk_mul_f32 v[12:13], v[130:131], s[16:17] op_sel_hi:[1,0]
	v_cvt_pk_bf16_f32 v7, v8, v9
	v_pk_mul_f32 v[14:15], v[128:129], s[16:17] op_sel_hi:[1,0]
	s_nop 0
	v_cvt_pk_bf16_f32 v8, v14, v15
	v_cvt_pk_bf16_f32 v9, v12, v13
	global_store_dwordx4 v[10:11], v[6:9], off sc1
	v_pk_mul_f32 v[12:13], v[194:195], s[16:17] op_sel_hi:[1,0]
	v_pk_mul_f32 v[14:15], v[192:193], s[16:17] op_sel_hi:[1,0]
	v_pk_mul_f32 v[6:7], v[196:197], s[16:17] op_sel_hi:[1,0]
	v_pk_mul_f32 v[8:9], v[198:199], s[16:17] op_sel_hi:[1,0]
	v_cvt_pk_bf16_f32 v6, v6, v7
	s_nop 0
	v_cvt_pk_bf16_f32 v7, v8, v9
	v_cvt_pk_bf16_f32 v8, v14, v15
	v_cvt_pk_bf16_f32 v9, v12, v13
	global_store_dwordx4 v[10:11], v[6:9], off offset:256 sc1
	v_pk_mul_f32 v[12:13], v[122:123], s[16:17] op_sel_hi:[1,0]
	v_pk_mul_f32 v[14:15], v[120:121], s[16:17] op_sel_hi:[1,0]
	v_or_b32_e32 v6, 16, v2
	v_mul_lo_u32 v8, s39, v6
	v_mad_u64_u32 v[6:7], s[40:41], s38, v6, 0
	v_add3_u32 v7, v7, v3, v8
	v_lshl_add_u64 v[10:11], v[6:7], 1, v[4:5]
	v_pk_mul_f32 v[6:7], v[124:125], s[16:17] op_sel_hi:[1,0]
	v_pk_mul_f32 v[8:9], v[126:127], s[16:17] op_sel_hi:[1,0]
	v_cvt_pk_bf16_f32 v6, v6, v7
	s_nop 0
	v_cvt_pk_bf16_f32 v7, v8, v9
	v_cvt_pk_bf16_f32 v8, v14, v15
	v_cvt_pk_bf16_f32 v9, v12, v13
	global_store_dwordx4 v[10:11], v[6:9], off sc1
	v_pk_mul_f32 v[12:13], v[186:187], s[16:17] op_sel_hi:[1,0]
	v_pk_mul_f32 v[14:15], v[184:185], s[16:17] op_sel_hi:[1,0]
	v_pk_mul_f32 v[6:7], v[188:189], s[16:17] op_sel_hi:[1,0]
	v_pk_mul_f32 v[8:9], v[190:191], s[16:17] op_sel_hi:[1,0]
	v_cvt_pk_bf16_f32 v6, v6, v7
	s_nop 0
	v_cvt_pk_bf16_f32 v7, v8, v9
	v_cvt_pk_bf16_f32 v8, v14, v15
	v_cvt_pk_bf16_f32 v9, v12, v13
	global_store_dwordx4 v[10:11], v[6:9], off offset:256 sc1
	v_pk_mul_f32 v[12:13], v[114:115], s[16:17] op_sel_hi:[1,0]
	v_pk_mul_f32 v[14:15], v[112:113], s[16:17] op_sel_hi:[1,0]
	v_or_b32_e32 v6, 32, v2
	v_mul_lo_u32 v8, s39, v6
	v_mad_u64_u32 v[6:7], s[40:41], s38, v6, 0
	v_add3_u32 v7, v7, v3, v8
	v_lshl_add_u64 v[10:11], v[6:7], 1, v[4:5]
	v_pk_mul_f32 v[6:7], v[116:117], s[16:17] op_sel_hi:[1,0]
	v_pk_mul_f32 v[8:9], v[118:119], s[16:17] op_sel_hi:[1,0]
	v_cvt_pk_bf16_f32 v6, v6, v7
	s_nop 0
	v_cvt_pk_bf16_f32 v7, v8, v9
	v_cvt_pk_bf16_f32 v8, v14, v15
	v_cvt_pk_bf16_f32 v9, v12, v13
	global_store_dwordx4 v[10:11], v[6:9], off sc1
	v_pk_mul_f32 v[12:13], v[178:179], s[16:17] op_sel_hi:[1,0]
	v_pk_mul_f32 v[14:15], v[176:177], s[16:17] op_sel_hi:[1,0]
	v_pk_mul_f32 v[6:7], v[180:181], s[16:17] op_sel_hi:[1,0]
	v_pk_mul_f32 v[8:9], v[182:183], s[16:17] op_sel_hi:[1,0]
	v_cvt_pk_bf16_f32 v6, v6, v7
	s_nop 0
	v_cvt_pk_bf16_f32 v7, v8, v9
	v_cvt_pk_bf16_f32 v8, v14, v15
	v_cvt_pk_bf16_f32 v9, v12, v13
	global_store_dwordx4 v[10:11], v[6:9], off offset:256 sc1
	v_pk_mul_f32 v[12:13], v[106:107], s[16:17] op_sel_hi:[1,0]
	v_pk_mul_f32 v[14:15], v[104:105], s[16:17] op_sel_hi:[1,0]
	v_or_b32_e32 v6, 48, v2
	v_mul_lo_u32 v8, s39, v6
	v_mad_u64_u32 v[6:7], s[40:41], s38, v6, 0
	v_add3_u32 v7, v7, v3, v8
	v_lshl_add_u64 v[10:11], v[6:7], 1, v[4:5]
	v_pk_mul_f32 v[6:7], v[108:109], s[16:17] op_sel_hi:[1,0]
	v_pk_mul_f32 v[8:9], v[110:111], s[16:17] op_sel_hi:[1,0]
	v_cvt_pk_bf16_f32 v6, v6, v7
	v_add_u32_e32 v3, 0x80, v2
	v_cvt_pk_bf16_f32 v7, v8, v9
	v_cvt_pk_bf16_f32 v8, v14, v15
	v_cvt_pk_bf16_f32 v9, v12, v13
	global_store_dwordx4 v[10:11], v[6:9], off sc1
	v_pk_mul_f32 v[12:13], v[170:171], s[16:17] op_sel_hi:[1,0]
	v_pk_mul_f32 v[14:15], v[168:169], s[16:17] op_sel_hi:[1,0]
	v_pk_mul_f32 v[6:7], v[172:173], s[16:17] op_sel_hi:[1,0]
	v_pk_mul_f32 v[8:9], v[174:175], s[16:17] op_sel_hi:[1,0]
	v_cvt_pk_bf16_f32 v6, v6, v7
	s_nop 0
	v_cvt_pk_bf16_f32 v7, v8, v9
	v_cvt_pk_bf16_f32 v8, v14, v15
	v_cvt_pk_bf16_f32 v9, v12, v13
	global_store_dwordx4 v[10:11], v[6:9], off offset:256 sc1
	v_pk_mul_f32 v[12:13], v[98:99], s[16:17] op_sel_hi:[1,0]
	v_pk_mul_f32 v[14:15], v[96:97], s[16:17] op_sel_hi:[1,0]
	v_ashrrev_i32_e32 v6, 31, v3
	v_mul_lo_u32 v8, s38, v6
	v_mul_lo_u32 v9, s39, v3
	v_mad_u64_u32 v[6:7], s[40:41], s38, v3, 0
	v_add3_u32 v7, v7, v8, v9
	v_lshl_add_u64 v[10:11], v[6:7], 1, v[4:5]
	v_pk_mul_f32 v[6:7], v[100:101], s[16:17] op_sel_hi:[1,0]
	v_pk_mul_f32 v[8:9], v[102:103], s[16:17] op_sel_hi:[1,0]
	v_cvt_pk_bf16_f32 v6, v6, v7
	v_add_u32_e32 v3, 0x90, v2
	v_cvt_pk_bf16_f32 v7, v8, v9
	v_cvt_pk_bf16_f32 v8, v14, v15
	v_cvt_pk_bf16_f32 v9, v12, v13
	global_store_dwordx4 v[10:11], v[6:9], off sc1
	v_pk_mul_f32 v[12:13], v[162:163], s[16:17] op_sel_hi:[1,0]
	v_pk_mul_f32 v[14:15], v[160:161], s[16:17] op_sel_hi:[1,0]
	v_pk_mul_f32 v[6:7], v[164:165], s[16:17] op_sel_hi:[1,0]
	v_pk_mul_f32 v[8:9], v[166:167], s[16:17] op_sel_hi:[1,0]
	v_cvt_pk_bf16_f32 v6, v6, v7
	s_nop 0
	v_cvt_pk_bf16_f32 v7, v8, v9
	v_cvt_pk_bf16_f32 v8, v14, v15
	v_cvt_pk_bf16_f32 v9, v12, v13
	global_store_dwordx4 v[10:11], v[6:9], off offset:256 sc1
	v_pk_mul_f32 v[12:13], v[90:91], s[16:17] op_sel_hi:[1,0]
	v_pk_mul_f32 v[14:15], v[88:89], s[16:17] op_sel_hi:[1,0]
	v_ashrrev_i32_e32 v6, 31, v3
	v_mul_lo_u32 v8, s38, v6
	v_mul_lo_u32 v9, s39, v3
	v_mad_u64_u32 v[6:7], s[40:41], s38, v3, 0
	v_add3_u32 v7, v7, v8, v9
	v_lshl_add_u64 v[10:11], v[6:7], 1, v[4:5]
	v_pk_mul_f32 v[6:7], v[92:93], s[16:17] op_sel_hi:[1,0]
	v_pk_mul_f32 v[8:9], v[94:95], s[16:17] op_sel_hi:[1,0]
	v_cvt_pk_bf16_f32 v6, v6, v7
	v_add_u32_e32 v3, 0xa0, v2
	v_cvt_pk_bf16_f32 v7, v8, v9
	v_cvt_pk_bf16_f32 v8, v14, v15
	v_cvt_pk_bf16_f32 v9, v12, v13
	global_store_dwordx4 v[10:11], v[6:9], off sc1
	v_pk_mul_f32 v[12:13], v[138:139], s[16:17] op_sel_hi:[1,0]
	v_pk_mul_f32 v[14:15], v[136:137], s[16:17] op_sel_hi:[1,0]
	v_pk_mul_f32 v[6:7], v[148:149], s[16:17] op_sel_hi:[1,0]
	v_pk_mul_f32 v[8:9], v[150:151], s[16:17] op_sel_hi:[1,0]
	v_cvt_pk_bf16_f32 v6, v6, v7
	s_nop 0
	v_cvt_pk_bf16_f32 v7, v8, v9
	v_cvt_pk_bf16_f32 v8, v14, v15
	v_cvt_pk_bf16_f32 v9, v12, v13
	global_store_dwordx4 v[10:11], v[6:9], off offset:256 sc1
	v_pk_mul_f32 v[12:13], v[82:83], s[16:17] op_sel_hi:[1,0]
	v_pk_mul_f32 v[14:15], v[80:81], s[16:17] op_sel_hi:[1,0]
	v_ashrrev_i32_e32 v6, 31, v3
	v_mul_lo_u32 v8, s38, v6
	v_mul_lo_u32 v9, s39, v3
	v_mad_u64_u32 v[6:7], s[40:41], s38, v3, 0
	v_add3_u32 v7, v7, v8, v9
	v_lshl_add_u64 v[10:11], v[6:7], 1, v[4:5]
	v_pk_mul_f32 v[6:7], v[84:85], s[16:17] op_sel_hi:[1,0]
	v_pk_mul_f32 v[8:9], v[86:87], s[16:17] op_sel_hi:[1,0]
	v_cvt_pk_bf16_f32 v6, v6, v7
	v_add_u32_e32 v3, 0xb0, v2
	v_cvt_pk_bf16_f32 v7, v8, v9
	v_cvt_pk_bf16_f32 v8, v14, v15
	v_cvt_pk_bf16_f32 v9, v12, v13
	global_store_dwordx4 v[10:11], v[6:9], off sc1
	v_pk_mul_f32 v[12:13], v[154:155], s[16:17] op_sel_hi:[1,0]
	v_pk_mul_f32 v[14:15], v[152:153], s[16:17] op_sel_hi:[1,0]
	v_pk_mul_f32 v[6:7], v[156:157], s[16:17] op_sel_hi:[1,0]
	v_pk_mul_f32 v[8:9], v[158:159], s[16:17] op_sel_hi:[1,0]
	v_cvt_pk_bf16_f32 v6, v6, v7
	s_nop 0
	v_cvt_pk_bf16_f32 v7, v8, v9
	v_cvt_pk_bf16_f32 v8, v14, v15
	v_cvt_pk_bf16_f32 v9, v12, v13
	global_store_dwordx4 v[10:11], v[6:9], off offset:256 sc1
	v_pk_mul_f32 v[10:11], v[74:75], s[16:17] op_sel_hi:[1,0]
	v_pk_mul_f32 v[12:13], v[72:73], s[16:17] op_sel_hi:[1,0]
	v_ashrrev_i32_e32 v6, 31, v3
	v_mul_lo_u32 v8, s38, v6
	v_mul_lo_u32 v9, s39, v3
	v_mad_u64_u32 v[6:7], s[38:39], s38, v3, 0
	v_add3_u32 v7, v7, v8, v9
	v_lshl_add_u64 v[8:9], v[6:7], 1, v[4:5]
	v_pk_mul_f32 v[6:7], v[78:79], s[16:17] op_sel_hi:[1,0]
	v_pk_mul_f32 v[4:5], v[76:77], s[16:17] op_sel_hi:[1,0]
	s_mov_b64 s[38:39], 0
	v_cvt_pk_bf16_f32 v4, v4, v5
	v_cvt_pk_bf16_f32 v5, v6, v7
	v_cvt_pk_bf16_f32 v6, v12, v13
	v_cvt_pk_bf16_f32 v7, v10, v11
	global_store_dwordx4 v[8:9], v[4:7], off sc1
	v_pk_mul_f32 v[10:11], v[142:143], s[16:17] op_sel_hi:[1,0]
	v_pk_mul_f32 v[12:13], v[140:141], s[16:17] op_sel_hi:[1,0]
	v_pk_mul_f32 v[6:7], v[146:147], s[16:17] op_sel_hi:[1,0]
	v_pk_mul_f32 v[4:5], v[144:145], s[16:17] op_sel_hi:[1,0]
	s_nop 0
	v_cvt_pk_bf16_f32 v4, v4, v5
	v_cvt_pk_bf16_f32 v5, v6, v7
	v_cvt_pk_bf16_f32 v6, v12, v13
	v_cvt_pk_bf16_f32 v7, v10, v11
	global_store_dwordx4 v[8:9], v[4:7], off offset:256 sc1
.LBB0_239:
	s_and_b64 vcc, exec, s[38:39]
	s_cbranch_vccz .LBB0_242
	s_andn2_b64 vcc, exec, s[28:29]
	s_cbranch_vccnz .LBB0_242
	v_or_b32_e32 v6, 16, v2
	v_ashrrev_i32_e32 v3, 31, v2
	v_ashrrev_i32_e32 v7, 31, v6
	v_lshlrev_b64 v[4:5], 8, v[2:3]
	v_lshlrev_b64 v[6:7], 8, v[6:7]
	v_lshl_add_u64 v[4:5], v[208:209], 0, v[4:5]
	v_lshl_add_u64 v[6:7], v[208:209], 0, v[6:7]
	global_store_dwordx4 v[4:5], v[132:135], off sc1
	global_store_dwordx4 v[4:5], v[128:131], off offset:16 sc1
	global_store_dwordx4 v[6:7], v[124:127], off sc1
	global_store_dwordx4 v[6:7], v[120:123], off offset:16 sc1
	v_or_b32_e32 v6, 32, v2
	v_ashrrev_i32_e32 v7, 31, v6
	v_lshlrev_b64 v[6:7], 8, v[6:7]
	v_or_b32_e32 v2, 48, v2
	v_lshl_add_u64 v[6:7], v[208:209], 0, v[6:7]
	v_ashrrev_i32_e32 v3, 31, v2
	s_mov_b32 s31, 0x8000
	global_store_dwordx4 v[6:7], v[116:119], off sc1
	global_store_dwordx4 v[6:7], v[112:115], off offset:16 sc1
	v_lshlrev_b64 v[2:3], 8, v[2:3]
	v_add_co_u32_e32 v6, vcc, s31, v4
	v_lshl_add_u64 v[2:3], v[208:209], 0, v[2:3]
	s_mov_b64 s[38:39], 0x8000
	v_addc_co_u32_e32 v7, vcc, 0, v5, vcc
	global_store_dwordx4 v[2:3], v[108:111], off sc1
	global_store_dwordx4 v[2:3], v[104:107], off offset:16 sc1
	v_lshl_add_u64 v[2:3], v[4:5], 0, s[38:39]
	global_store_dwordx4 v[6:7], v[100:103], off sc1
	global_store_dwordx4 v[2:3], v[96:99], off offset:16 sc1
	v_add_co_u32_e32 v6, vcc, 0x9000, v4
	s_mov_b64 s[38:39], 0x9000
	s_nop 0
	v_addc_co_u32_e32 v7, vcc, 0, v5, vcc
	v_lshl_add_u64 v[2:3], v[4:5], 0, s[38:39]
	global_store_dwordx4 v[6:7], v[92:95], off sc1
	global_store_dwordx4 v[2:3], v[88:91], off offset:16 sc1
	s_mov_b64 s[38:39], 0xa000
	v_add_co_u32_e32 v6, vcc, 0xa000, v4
	v_lshl_add_u64 v[2:3], v[4:5], 0, s[38:39]
	s_nop 0
	v_addc_co_u32_e32 v7, vcc, 0, v5, vcc
	s_mov_b64 s[38:39], 0xb000
	global_store_dwordx4 v[6:7], v[84:87], off sc1
	global_store_dwordx4 v[2:3], v[80:83], off offset:16 sc1
	v_lshl_add_u64 v[2:3], v[4:5], 0, s[38:39]
	v_add_co_u32_e32 v4, vcc, 0xb000, v4
	s_nop 1
	v_addc_co_u32_e32 v5, vcc, 0, v5, vcc
	global_store_dwordx4 v[4:5], v[76:79], off sc1
	global_store_dwordx4 v[2:3], v[72:75], off offset:16 sc1

.LBB0_477:
	s_lshl_b32 s20, s46, 9
	s_lshl_b32 s21, s45, 8
	s_or_b32 s20, s20, s21
	v_or_b32_e32 v4, s20, v219
	v_readlane_b32 s52, v253, 18
	v_ashrrev_i32_e32 v5, 31, v4
	v_readlane_b32 s60, v253, 26
	v_readlane_b32 s61, v253, 27
	v_lshl_add_u32 v174, s44, 8, v217
	v_mov_b32_e32 v175, v3
	v_lshl_add_u64 v[92:93], v[4:5], 2, s[60:61]
	v_lshlrev_b64 v[4:5], 1, v[4:5]
	v_lshl_add_u64 v[172:173], s[8:9], 0, v[4:5]
	v_lshlrev_b64 v[152:153], 12, v[174:175]
	v_lshl_add_u64 v[154:155], v[172:173], 0, v[152:153]
	global_load_dwordx4 v[104:107], v[92:93], off offset:16
	global_load_dwordx4 v[108:111], v[92:93], off
	global_load_dwordx4 v[88:91], v[92:93], off offset:528
	s_nop 0
	global_load_dwordx4 v[92:95], v[92:93], off offset:512
	s_nop 0
	global_load_dwordx4 v[182:185], v[154:155], off
	global_load_dwordx4 v[186:189], v[154:155], off offset:256
	v_mov_b32_e32 v155, v3
	v_mov_b32_e32 v157, v3
	v_or_b32_e32 v154, 16, v174
	v_or_b32_e32 v156, 32, v174
	v_mov_b32_e32 v159, v3
	v_or_b32_e32 v158, 48, v174
	v_lshlrev_b64 v[180:181], 12, v[154:155]
	v_lshlrev_b64 v[178:179], 12, v[156:157]
	v_lshl_add_u64 v[152:153], s[6:7], 0, v[152:153]
	v_lshlrev_b64 v[176:177], 12, v[158:159]
	v_lshl_add_u64 v[194:195], v[152:153], 0, v[4:5]
	v_lshl_add_u64 v[152:153], v[172:173], 0, v[180:181]
	v_lshl_add_u64 v[154:155], v[172:173], 0, v[178:179]
	v_lshl_add_u64 v[196:197], v[172:173], 0, v[176:177]
	global_load_dwordx4 v[190:193], v[152:153], off
	global_load_dwordx4 v[168:171], v[152:153], off offset:256
	global_load_dwordx4 v[164:167], v[154:155], off
	global_load_dwordx4 v[160:163], v[154:155], off offset:256
	global_load_dwordx4 v[156:159], v[196:197], off
	s_nop 0
	global_load_dwordx4 v[152:155], v[196:197], off offset:256
	s_andn2_b64 vcc, exec, s[16:17]
	s_mov_b64 s[16:17], -1
	v_readlane_b32 s53, v253, 19
	v_readlane_b32 s54, v253, 20
	v_readlane_b32 s55, v253, 21
	v_readlane_b32 s56, v253, 22
	v_readlane_b32 s57, v253, 23
	v_readlane_b32 s58, v253, 24
	v_readlane_b32 s59, v253, 25
	v_readlane_b32 s62, v253, 28
	v_readlane_b32 s63, v253, 29
	v_readlane_b32 s64, v253, 30
	v_readlane_b32 s65, v253, 31
	v_readlane_b32 s66, v253, 32
	v_readlane_b32 s67, v253, 33
	s_waitcnt vmcnt(0)
	v_pk_mul_f32 v[144:145], v[144:145], v[104:105]
	v_pk_mul_f32 v[148:149], v[148:149], v[108:109]
	v_pk_mul_f32 v[198:199], v[138:139], v[90:91]
	v_lshlrev_b32_e32 v7, 16, v182
	v_and_b32_e32 v138, 0xffff0000, v182
	v_mul_f32_e32 v7, 0xbfb8aa3b, v7
	v_mul_f32_e32 v138, 0xbfb8aa3b, v138
	v_exp_f32_e32 v7, v7
	v_exp_f32_e32 v138, v138
	v_lshlrev_b32_e32 v139, 16, v183
	v_pk_mul_f32 v[196:197], v[140:141], v[92:93]
	v_and_b32_e32 v140, 0xffff0000, v183
	v_lshlrev_b32_e32 v141, 16, v184
	v_mul_f32_e32 v139, 0xbfb8aa3b, v139
	v_add_f32_e32 v7, 1.0, v7
	v_add_f32_e32 v138, 1.0, v138
	v_and_b32_e32 v175, 0xffff0000, v184
	v_lshlrev_b32_e32 v182, 16, v185
	v_and_b32_e32 v183, 0xffff0000, v185
	v_mul_f32_e32 v140, 0xbfb8aa3b, v140
	v_mul_f32_e32 v141, 0xbfb8aa3b, v141
	v_exp_f32_e32 v139, v139
	v_rcp_f32_e32 v7, v7
	v_rcp_f32_e32 v138, v138
	v_mul_f32_e32 v175, 0xbfb8aa3b, v175
	v_mul_f32_e32 v182, 0xbfb8aa3b, v182
	v_mul_f32_e32 v183, 0xbfb8aa3b, v183
	v_exp_f32_e32 v140, v140
	v_exp_f32_e32 v141, v141
	v_exp_f32_e32 v175, v175
	v_exp_f32_e32 v182, v182
	v_exp_f32_e32 v183, v183
	v_add_f32_e32 v139, 1.0, v139
	v_mul_f32_e32 v7, v148, v7
	v_mul_f32_e32 v138, v149, v138
	v_lshlrev_b32_e32 v184, 16, v186
	v_add_f32_e32 v140, 1.0, v140
	v_add_f32_e32 v141, 1.0, v141
	v_rcp_f32_e32 v139, v139
	v_cvt_pk_bf16_f32 v138, v7, v138
	v_and_b32_e32 v7, 0xffff0000, v186
	v_mul_f32_e32 v184, 0xbfb8aa3b, v184
	v_add_f32_e32 v175, 1.0, v175
	v_add_f32_e32 v182, 1.0, v182
	v_add_f32_e32 v183, 1.0, v183
	v_rcp_f32_e32 v140, v140
	v_rcp_f32_e32 v141, v141
	v_mul_f32_e32 v7, 0xbfb8aa3b, v7
	v_exp_f32_e32 v184, v184
	v_rcp_f32_e32 v175, v175
	v_rcp_f32_e32 v182, v182
	v_rcp_f32_e32 v183, v183
	v_exp_f32_e32 v7, v7
	v_pk_mul_f32 v[150:151], v[150:151], v[110:111]
	v_pk_mul_f32 v[146:147], v[146:147], v[106:107]
	v_mul_f32_e32 v139, v150, v139
	v_mul_f32_e32 v140, v151, v140
	v_mul_f32_e32 v141, v144, v141
	v_cvt_pk_bf16_f32 v139, v139, v140
	v_mul_f32_e32 v144, v145, v175
	v_mul_f32_e32 v145, v146, v182
	v_mul_f32_e32 v146, v147, v183
	v_cvt_pk_bf16_f32 v140, v141, v144
	v_cvt_pk_bf16_f32 v141, v145, v146
	global_store_dwordx4 v[194:195], v[138:141], off sc1
	v_add_f32_e32 v7, 1.0, v7
	v_rcp_f32_e32 v7, v7
	v_pk_mul_f32 v[138:139], v[136:137], v[88:89]
	v_add_f32_e32 v136, 1.0, v184
	v_lshlrev_b32_e32 v137, 16, v187
	v_rcp_f32_e32 v136, v136
	v_mul_f32_e32 v137, 0xbfb8aa3b, v137
	v_exp_f32_e32 v137, v137
	v_mul_f32_e32 v7, v197, v7
	v_mul_f32_e32 v136, v196, v136
	v_cvt_pk_bf16_f32 v136, v136, v7
	v_add_f32_e32 v7, 1.0, v137
	v_and_b32_e32 v137, 0xffff0000, v187
	v_mul_f32_e32 v137, 0xbfb8aa3b, v137
	v_lshlrev_b32_e32 v140, 16, v188
	v_exp_f32_e32 v137, v137
	v_mul_f32_e32 v140, 0xbfb8aa3b, v140
	v_exp_f32_e32 v140, v140
	v_and_b32_e32 v141, 0xffff0000, v188
	v_add_f32_e32 v137, 1.0, v137
	v_rcp_f32_e32 v7, v7
	v_rcp_f32_e32 v137, v137
	v_add_f32_e32 v140, 1.0, v140
	v_mul_f32_e32 v141, 0xbfb8aa3b, v141
	v_rcp_f32_e32 v140, v140
	v_exp_f32_e32 v141, v141
	v_pk_mul_f32 v[142:143], v[142:143], v[94:95]
	v_pk_mul_f32 v[132:133], v[132:133], v[108:109]
	v_mul_f32_e32 v7, v142, v7
	v_mul_f32_e32 v137, v143, v137
	v_cvt_pk_bf16_f32 v137, v7, v137
	v_mul_f32_e32 v7, v138, v140
	v_add_f32_e32 v138, 1.0, v141
	v_lshlrev_b32_e32 v140, 16, v189
	v_and_b32_e32 v141, 0xffff0000, v189
	v_mul_f32_e32 v140, 0xbfb8aa3b, v140
	v_mul_f32_e32 v141, 0xbfb8aa3b, v141
	v_exp_f32_e32 v140, v140
	v_exp_f32_e32 v141, v141
	v_rcp_f32_e32 v138, v138
	v_pk_mul_f32 v[134:135], v[134:135], v[110:111]
	v_add_f32_e32 v140, 1.0, v140
	v_add_f32_e32 v141, 1.0, v141
	v_rcp_f32_e32 v140, v140
	v_rcp_f32_e32 v141, v141
	v_mul_f32_e32 v138, v139, v138
	v_cvt_pk_bf16_f32 v138, v7, v138
	v_mul_f32_e32 v7, v198, v140
	v_mul_f32_e32 v139, v199, v141
	v_cvt_pk_bf16_f32 v139, v7, v139
	global_store_dwordx4 v[194:195], v[136:139], off offset:256 sc1
	v_lshlrev_b32_e32 v7, 16, v190
	v_mul_f32_e32 v7, 0xbfb8aa3b, v7
	v_pk_mul_f32 v[136:137], v[130:131], v[106:107]
	v_and_b32_e32 v130, 0xffff0000, v190
	v_mul_f32_e32 v130, 0xbfb8aa3b, v130
	v_exp_f32_e32 v7, v7
	v_exp_f32_e32 v138, v130
	v_pk_mul_f32 v[130:131], v[128:129], v[104:105]
	v_lshlrev_b32_e32 v129, 16, v191
	v_add_f32_e32 v7, 1.0, v7
	v_add_f32_e32 v128, 1.0, v138
	v_rcp_f32_e32 v7, v7
	v_rcp_f32_e32 v128, v128
	v_mul_f32_e32 v129, 0xbfb8aa3b, v129
	v_exp_f32_e32 v129, v129
	v_mul_f32_e32 v7, v132, v7
	v_mul_f32_e32 v128, v133, v128
	v_cvt_pk_bf16_f32 v128, v7, v128
	v_add_f32_e32 v7, 1.0, v129
	v_and_b32_e32 v129, 0xffff0000, v191
	v_mul_f32_e32 v129, 0xbfb8aa3b, v129
	v_lshlrev_b32_e32 v132, 16, v192
	v_exp_f32_e32 v129, v129
	v_mul_f32_e32 v132, 0xbfb8aa3b, v132
	v_exp_f32_e32 v132, v132
	v_and_b32_e32 v133, 0xffff0000, v192
	v_add_f32_e32 v129, 1.0, v129
	v_rcp_f32_e32 v7, v7
	v_rcp_f32_e32 v129, v129
	v_add_f32_e32 v132, 1.0, v132
	v_mul_f32_e32 v133, 0xbfb8aa3b, v133
	v_rcp_f32_e32 v132, v132
	v_exp_f32_e32 v133, v133
	v_mul_f32_e32 v7, v134, v7
	v_mul_f32_e32 v129, v135, v129
	v_cvt_pk_bf16_f32 v129, v7, v129
	v_mul_f32_e32 v7, v130, v132
	v_add_f32_e32 v130, 1.0, v133
	v_lshlrev_b32_e32 v132, 16, v193
	v_and_b32_e32 v133, 0xffff0000, v193
	v_mul_f32_e32 v132, 0xbfb8aa3b, v132
	v_mul_f32_e32 v133, 0xbfb8aa3b, v133
	v_exp_f32_e32 v132, v132
	v_exp_f32_e32 v133, v133
	v_rcp_f32_e32 v130, v130
	v_pk_mul_f32 v[124:125], v[124:125], v[92:93]
	v_add_f32_e32 v132, 1.0, v132
	v_add_f32_e32 v133, 1.0, v133
	v_rcp_f32_e32 v132, v132
	v_rcp_f32_e32 v133, v133
	v_mul_f32_e32 v130, v131, v130
	v_cvt_pk_bf16_f32 v130, v7, v130
	v_mul_f32_e32 v7, v136, v132
	v_mul_f32_e32 v131, v137, v133
	v_lshl_add_u64 v[132:133], s[6:7], 0, v[180:181]
	v_lshl_add_u64 v[132:133], v[132:133], 0, v[4:5]
	v_cvt_pk_bf16_f32 v131, v7, v131
	global_store_dwordx4 v[132:133], v[128:131], off sc1
	v_lshlrev_b32_e32 v7, 16, v168
	v_mul_f32_e32 v7, 0xbfb8aa3b, v7
	v_pk_mul_f32 v[128:129], v[122:123], v[90:91]
	v_and_b32_e32 v122, 0xffff0000, v168
	v_mul_f32_e32 v122, 0xbfb8aa3b, v122
	v_exp_f32_e32 v7, v7
	v_exp_f32_e32 v130, v122
	v_pk_mul_f32 v[122:123], v[120:121], v[88:89]
	v_lshlrev_b32_e32 v121, 16, v169
	v_add_f32_e32 v7, 1.0, v7
	v_add_f32_e32 v120, 1.0, v130
	v_rcp_f32_e32 v7, v7
	v_rcp_f32_e32 v120, v120
	v_mul_f32_e32 v121, 0xbfb8aa3b, v121
	v_exp_f32_e32 v121, v121
	v_mul_f32_e32 v7, v124, v7
	v_mul_f32_e32 v120, v125, v120
	v_cvt_pk_bf16_f32 v120, v7, v120
	v_add_f32_e32 v7, 1.0, v121
	v_and_b32_e32 v121, 0xffff0000, v169
	v_mul_f32_e32 v121, 0xbfb8aa3b, v121
	v_lshlrev_b32_e32 v124, 16, v170
	v_exp_f32_e32 v121, v121
	v_mul_f32_e32 v124, 0xbfb8aa3b, v124
	v_exp_f32_e32 v124, v124
	v_and_b32_e32 v125, 0xffff0000, v170
	v_add_f32_e32 v121, 1.0, v121
	v_rcp_f32_e32 v7, v7
	v_rcp_f32_e32 v121, v121
	v_add_f32_e32 v124, 1.0, v124
	v_mul_f32_e32 v125, 0xbfb8aa3b, v125
	v_rcp_f32_e32 v124, v124
	v_exp_f32_e32 v125, v125
	v_pk_mul_f32 v[126:127], v[126:127], v[94:95]
	v_pk_mul_f32 v[116:117], v[116:117], v[108:109]
	v_mul_f32_e32 v7, v126, v7
	v_mul_f32_e32 v121, v127, v121
	v_cvt_pk_bf16_f32 v121, v7, v121
	v_mul_f32_e32 v7, v122, v124
	v_add_f32_e32 v122, 1.0, v125
	v_lshlrev_b32_e32 v124, 16, v171
	v_and_b32_e32 v125, 0xffff0000, v171
	v_mul_f32_e32 v124, 0xbfb8aa3b, v124
	v_mul_f32_e32 v125, 0xbfb8aa3b, v125
	v_exp_f32_e32 v124, v124
	v_exp_f32_e32 v125, v125
	v_rcp_f32_e32 v122, v122
	v_pk_mul_f32 v[118:119], v[118:119], v[110:111]
	v_add_f32_e32 v124, 1.0, v124
	v_add_f32_e32 v125, 1.0, v125
	v_rcp_f32_e32 v124, v124
	v_rcp_f32_e32 v125, v125
	v_mul_f32_e32 v122, v123, v122
	v_cvt_pk_bf16_f32 v122, v7, v122
	v_mul_f32_e32 v7, v128, v124
	v_mul_f32_e32 v123, v129, v125
	v_cvt_pk_bf16_f32 v123, v7, v123
	global_store_dwordx4 v[132:133], v[120:123], off offset:256 sc1
	v_lshlrev_b32_e32 v7, 16, v164
	v_mul_f32_e32 v7, 0xbfb8aa3b, v7
	v_pk_mul_f32 v[120:121], v[114:115], v[106:107]
	v_and_b32_e32 v114, 0xffff0000, v164
	v_mul_f32_e32 v114, 0xbfb8aa3b, v114
	v_exp_f32_e32 v7, v7
	v_exp_f32_e32 v122, v114
	v_pk_mul_f32 v[114:115], v[112:113], v[104:105]
	v_lshlrev_b32_e32 v113, 16, v165
	v_add_f32_e32 v7, 1.0, v7
	v_add_f32_e32 v112, 1.0, v122
	v_rcp_f32_e32 v7, v7
	v_rcp_f32_e32 v112, v112
	v_mul_f32_e32 v113, 0xbfb8aa3b, v113
	v_exp_f32_e32 v113, v113
	v_mul_f32_e32 v7, v116, v7
	v_mul_f32_e32 v112, v117, v112
	v_cvt_pk_bf16_f32 v112, v7, v112
	v_add_f32_e32 v7, 1.0, v113
	v_and_b32_e32 v113, 0xffff0000, v165
	v_mul_f32_e32 v113, 0xbfb8aa3b, v113
	v_lshlrev_b32_e32 v116, 16, v166
	v_exp_f32_e32 v113, v113
	v_mul_f32_e32 v116, 0xbfb8aa3b, v116
	v_exp_f32_e32 v116, v116
	v_and_b32_e32 v117, 0xffff0000, v166
	v_add_f32_e32 v113, 1.0, v113
	v_rcp_f32_e32 v7, v7
	v_rcp_f32_e32 v113, v113
	v_add_f32_e32 v116, 1.0, v116
	v_mul_f32_e32 v117, 0xbfb8aa3b, v117
	v_rcp_f32_e32 v116, v116
	v_exp_f32_e32 v117, v117
	v_mul_f32_e32 v7, v118, v7
	v_mul_f32_e32 v113, v119, v113
	v_cvt_pk_bf16_f32 v113, v7, v113
	v_mul_f32_e32 v7, v114, v116
	v_add_f32_e32 v114, 1.0, v117
	v_lshlrev_b32_e32 v116, 16, v167
	v_and_b32_e32 v117, 0xffff0000, v167
	v_mul_f32_e32 v116, 0xbfb8aa3b, v116
	v_mul_f32_e32 v117, 0xbfb8aa3b, v117
	v_exp_f32_e32 v116, v116
	v_exp_f32_e32 v117, v117
	v_rcp_f32_e32 v114, v114
	v_pk_mul_f32 v[100:101], v[100:101], v[92:93]
	v_add_f32_e32 v116, 1.0, v116
	v_add_f32_e32 v117, 1.0, v117
	v_rcp_f32_e32 v116, v116
	v_rcp_f32_e32 v117, v117
	v_mul_f32_e32 v114, v115, v114
	v_cvt_pk_bf16_f32 v114, v7, v114
	v_mul_f32_e32 v7, v120, v116
	v_mul_f32_e32 v115, v121, v117
	v_lshl_add_u64 v[116:117], s[6:7], 0, v[178:179]
	v_lshl_add_u64 v[116:117], v[116:117], 0, v[4:5]
	v_cvt_pk_bf16_f32 v115, v7, v115
	global_store_dwordx4 v[116:117], v[112:115], off sc1
	v_lshlrev_b32_e32 v7, 16, v160
	v_mul_f32_e32 v7, 0xbfb8aa3b, v7
	v_pk_mul_f32 v[112:113], v[98:99], v[90:91]
	v_and_b32_e32 v98, 0xffff0000, v160
	v_mul_f32_e32 v98, 0xbfb8aa3b, v98
	v_exp_f32_e32 v7, v7
	v_exp_f32_e32 v114, v98
	v_pk_mul_f32 v[98:99], v[96:97], v[88:89]
	v_lshlrev_b32_e32 v97, 16, v161
	v_add_f32_e32 v7, 1.0, v7
	v_add_f32_e32 v96, 1.0, v114
	v_rcp_f32_e32 v7, v7
	v_rcp_f32_e32 v96, v96
	v_mul_f32_e32 v97, 0xbfb8aa3b, v97
	v_exp_f32_e32 v97, v97
	v_mul_f32_e32 v7, v100, v7
	v_mul_f32_e32 v96, v101, v96
	v_cvt_pk_bf16_f32 v96, v7, v96
	v_add_f32_e32 v7, 1.0, v97
	v_and_b32_e32 v97, 0xffff0000, v161
	v_mul_f32_e32 v97, 0xbfb8aa3b, v97
	v_lshlrev_b32_e32 v100, 16, v162
	v_exp_f32_e32 v97, v97
	v_mul_f32_e32 v100, 0xbfb8aa3b, v100
	v_exp_f32_e32 v100, v100
	v_and_b32_e32 v101, 0xffff0000, v162
	v_add_f32_e32 v97, 1.0, v97
	v_rcp_f32_e32 v7, v7
	v_rcp_f32_e32 v97, v97
	v_add_f32_e32 v100, 1.0, v100
	v_mul_f32_e32 v101, 0xbfb8aa3b, v101
	v_rcp_f32_e32 v100, v100
	v_exp_f32_e32 v101, v101
	v_pk_mul_f32 v[102:103], v[102:103], v[94:95]
	v_pk_mul_f32 v[84:85], v[84:85], v[108:109]
	v_mul_f32_e32 v7, v102, v7
	v_mul_f32_e32 v97, v103, v97
	v_cvt_pk_bf16_f32 v97, v7, v97
	v_mul_f32_e32 v7, v98, v100
	v_add_f32_e32 v98, 1.0, v101
	v_lshlrev_b32_e32 v100, 16, v163
	v_and_b32_e32 v101, 0xffff0000, v163
	v_mul_f32_e32 v100, 0xbfb8aa3b, v100
	v_mul_f32_e32 v101, 0xbfb8aa3b, v101
	v_exp_f32_e32 v100, v100
	v_exp_f32_e32 v101, v101
	v_rcp_f32_e32 v98, v98
	v_pk_mul_f32 v[86:87], v[86:87], v[110:111]
	v_add_f32_e32 v100, 1.0, v100
	v_add_f32_e32 v101, 1.0, v101
	v_rcp_f32_e32 v100, v100
	v_rcp_f32_e32 v101, v101
	v_mul_f32_e32 v98, v99, v98
	v_cvt_pk_bf16_f32 v98, v7, v98
	v_mul_f32_e32 v7, v112, v100
	v_mul_f32_e32 v99, v113, v101
	v_cvt_pk_bf16_f32 v99, v7, v99
	global_store_dwordx4 v[116:117], v[96:99], off offset:256 sc1
	v_lshlrev_b32_e32 v7, 16, v156
	v_mul_f32_e32 v7, 0xbfb8aa3b, v7
	v_pk_mul_f32 v[96:97], v[82:83], v[106:107]
	v_and_b32_e32 v82, 0xffff0000, v156
	v_mul_f32_e32 v82, 0xbfb8aa3b, v82
	v_exp_f32_e32 v7, v7
	v_exp_f32_e32 v98, v82
	v_pk_mul_f32 v[82:83], v[80:81], v[104:105]
	v_lshlrev_b32_e32 v81, 16, v157
	v_add_f32_e32 v7, 1.0, v7
	v_add_f32_e32 v80, 1.0, v98
	v_rcp_f32_e32 v7, v7
	v_rcp_f32_e32 v80, v80
	v_mul_f32_e32 v81, 0xbfb8aa3b, v81
	v_exp_f32_e32 v81, v81
	v_mul_f32_e32 v7, v84, v7
	v_mul_f32_e32 v80, v85, v80
	v_cvt_pk_bf16_f32 v80, v7, v80
	v_add_f32_e32 v7, 1.0, v81
	v_and_b32_e32 v81, 0xffff0000, v157
	v_mul_f32_e32 v81, 0xbfb8aa3b, v81
	v_lshlrev_b32_e32 v84, 16, v158
	v_exp_f32_e32 v81, v81
	v_mul_f32_e32 v84, 0xbfb8aa3b, v84
	v_exp_f32_e32 v84, v84
	v_and_b32_e32 v85, 0xffff0000, v158
	v_add_f32_e32 v81, 1.0, v81
	v_rcp_f32_e32 v7, v7
	v_rcp_f32_e32 v81, v81
	v_add_f32_e32 v84, 1.0, v84
	v_mul_f32_e32 v85, 0xbfb8aa3b, v85
	v_rcp_f32_e32 v84, v84
	v_exp_f32_e32 v85, v85
	v_mul_f32_e32 v7, v86, v7
	v_mul_f32_e32 v81, v87, v81
	v_cvt_pk_bf16_f32 v81, v7, v81
	v_mul_f32_e32 v7, v82, v84
	v_add_f32_e32 v82, 1.0, v85
	v_lshlrev_b32_e32 v84, 16, v159
	v_and_b32_e32 v85, 0xffff0000, v159
	v_mul_f32_e32 v84, 0xbfb8aa3b, v84
	v_mul_f32_e32 v85, 0xbfb8aa3b, v85
	v_exp_f32_e32 v84, v84
	v_exp_f32_e32 v85, v85
	v_rcp_f32_e32 v82, v82
	v_pk_mul_f32 v[76:77], v[76:77], v[92:93]
	v_add_f32_e32 v84, 1.0, v84
	v_add_f32_e32 v85, 1.0, v85
	v_rcp_f32_e32 v84, v84
	v_rcp_f32_e32 v85, v85
	v_mul_f32_e32 v82, v83, v82
	v_cvt_pk_bf16_f32 v82, v7, v82
	v_mul_f32_e32 v7, v96, v84
	v_mul_f32_e32 v83, v97, v85
	v_lshl_add_u64 v[84:85], s[6:7], 0, v[176:177]
	v_lshl_add_u64 v[84:85], v[84:85], 0, v[4:5]
	v_cvt_pk_bf16_f32 v83, v7, v83
	global_store_dwordx4 v[84:85], v[80:83], off sc1
	v_lshlrev_b32_e32 v7, 16, v152
	v_mul_f32_e32 v7, 0xbfb8aa3b, v7
	v_pk_mul_f32 v[80:81], v[74:75], v[90:91]
	v_and_b32_e32 v74, 0xffff0000, v152
	v_mul_f32_e32 v74, 0xbfb8aa3b, v74
	v_exp_f32_e32 v7, v7
	v_exp_f32_e32 v82, v74
	v_pk_mul_f32 v[74:75], v[72:73], v[88:89]
	v_lshlrev_b32_e32 v73, 16, v153
	v_add_f32_e32 v7, 1.0, v7
	v_add_f32_e32 v72, 1.0, v82
	v_rcp_f32_e32 v7, v7
	v_rcp_f32_e32 v72, v72
	v_mul_f32_e32 v73, 0xbfb8aa3b, v73
	v_exp_f32_e32 v73, v73
	v_mul_f32_e32 v7, v76, v7
	v_mul_f32_e32 v72, v77, v72
	v_cvt_pk_bf16_f32 v72, v7, v72
	v_add_f32_e32 v7, 1.0, v73
	v_and_b32_e32 v73, 0xffff0000, v153
	v_mul_f32_e32 v73, 0xbfb8aa3b, v73
	v_lshlrev_b32_e32 v76, 16, v154
	v_exp_f32_e32 v73, v73
	v_mul_f32_e32 v76, 0xbfb8aa3b, v76
	v_exp_f32_e32 v76, v76
	v_and_b32_e32 v77, 0xffff0000, v154
	v_add_f32_e32 v73, 1.0, v73
	v_rcp_f32_e32 v7, v7
	v_rcp_f32_e32 v73, v73
	v_add_f32_e32 v76, 1.0, v76
	v_mul_f32_e32 v77, 0xbfb8aa3b, v77
	v_rcp_f32_e32 v76, v76
	v_exp_f32_e32 v77, v77
	v_pk_mul_f32 v[78:79], v[78:79], v[94:95]
	v_pk_mul_f32 v[128:129], v[66:67], v[106:107]
	v_mul_f32_e32 v7, v78, v7
	v_mul_f32_e32 v73, v79, v73
	v_cvt_pk_bf16_f32 v73, v7, v73
	v_mul_f32_e32 v7, v74, v76
	v_add_f32_e32 v74, 1.0, v77
	v_lshlrev_b32_e32 v76, 16, v155
	v_and_b32_e32 v77, 0xffff0000, v155
	v_mul_f32_e32 v76, 0xbfb8aa3b, v76
	v_mul_f32_e32 v77, 0xbfb8aa3b, v77
	v_exp_f32_e32 v76, v76
	v_exp_f32_e32 v77, v77
	v_rcp_f32_e32 v74, v74
	v_pk_mul_f32 v[68:69], v[68:69], v[108:109]
	v_add_f32_e32 v76, 1.0, v76
	v_add_f32_e32 v77, 1.0, v77
	v_rcp_f32_e32 v76, v76
	v_rcp_f32_e32 v77, v77
	v_mul_f32_e32 v74, v75, v74
	v_cvt_pk_bf16_f32 v74, v7, v74
	v_mul_f32_e32 v7, v80, v76
	v_mul_f32_e32 v75, v81, v77
	v_add_u32_e32 v76, 0x80, v174
	v_mov_b32_e32 v77, v3
	v_lshlrev_b64 v[126:127], 12, v[76:77]
	v_lshl_add_u64 v[76:77], v[172:173], 0, v[126:127]
	v_cvt_pk_bf16_f32 v75, v7, v75
	global_load_dwordx4 v[114:117], v[76:77], off
	global_load_dwordx4 v[118:121], v[76:77], off offset:256
	v_pk_mul_f32 v[70:71], v[70:71], v[110:111]
	global_store_dwordx4 v[84:85], v[72:75], off offset:256 sc1
	v_pk_mul_f32 v[60:61], v[60:61], v[92:93]
	v_pk_mul_f32 v[62:63], v[62:63], v[94:95]
	v_add_u32_e32 v72, 0x90, v174
	v_mov_b32_e32 v73, v3
	v_lshlrev_b64 v[112:113], 12, v[72:73]
	v_lshl_add_u64 v[72:73], v[172:173], 0, v[112:113]
	global_load_dwordx4 v[122:125], v[72:73], off
	global_load_dwordx4 v[96:99], v[72:73], off offset:256
	v_add_u32_e32 v72, 0xa0, v174
	v_mov_b32_e32 v73, v3
	v_lshlrev_b64 v[102:103], 12, v[72:73]
	v_lshl_add_u64 v[72:73], v[172:173], 0, v[102:103]
	global_load_dwordx4 v[84:87], v[72:73], off
	global_load_dwordx4 v[80:83], v[72:73], off offset:256
	v_add_u32_e32 v72, 0xb0, v174
	v_mov_b32_e32 v73, v3
	v_lshlrev_b64 v[100:101], 12, v[72:73]
	v_lshl_add_u64 v[72:73], v[172:173], 0, v[100:101]
	global_load_dwordx4 v[76:79], v[72:73], off
	s_nop 0
	global_load_dwordx4 v[72:75], v[72:73], off offset:256
	v_pk_mul_f32 v[52:53], v[52:53], v[108:109]
	v_pk_mul_f32 v[54:55], v[54:55], v[110:111]
	v_pk_mul_f32 v[44:45], v[44:45], v[92:93]
	v_pk_mul_f32 v[46:47], v[46:47], v[94:95]
	v_pk_mul_f32 v[36:37], v[36:37], v[108:109]
	v_pk_mul_f32 v[38:39], v[38:39], v[110:111]
	v_pk_mul_f32 v[28:29], v[28:29], v[88:89]
	v_pk_mul_f32 v[30:31], v[30:31], v[90:91]
	v_pk_mul_f32 v[12:13], v[12:13], v[108:109]
	v_pk_mul_f32 v[14:15], v[14:15], v[110:111]
	s_waitcnt vmcnt(8)
	v_lshlrev_b32_e32 v7, 16, v114
	v_and_b32_e32 v66, 0xffff0000, v114
	v_mul_f32_e32 v7, 0xbfb8aa3b, v7
	v_mul_f32_e32 v66, 0xbfb8aa3b, v66
	v_exp_f32_e32 v7, v7
	v_exp_f32_e32 v114, v66
	v_pk_mul_f32 v[66:67], v[64:65], v[104:105]
	v_lshlrev_b32_e32 v65, 16, v115
	v_add_f32_e32 v7, 1.0, v7
	v_add_f32_e32 v64, 1.0, v114
	v_rcp_f32_e32 v7, v7
	v_rcp_f32_e32 v64, v64
	v_mul_f32_e32 v65, 0xbfb8aa3b, v65
	v_exp_f32_e32 v65, v65
	v_mul_f32_e32 v7, v68, v7
	v_mul_f32_e32 v64, v69, v64
	v_cvt_pk_bf16_f32 v64, v7, v64
	v_add_f32_e32 v7, 1.0, v65
	v_and_b32_e32 v65, 0xffff0000, v115
	v_mul_f32_e32 v65, 0xbfb8aa3b, v65
	v_lshlrev_b32_e32 v68, 16, v116
	v_exp_f32_e32 v65, v65
	v_mul_f32_e32 v68, 0xbfb8aa3b, v68
	v_exp_f32_e32 v68, v68
	v_and_b32_e32 v69, 0xffff0000, v116
	v_add_f32_e32 v65, 1.0, v65
	v_rcp_f32_e32 v7, v7
	v_rcp_f32_e32 v65, v65
	v_add_f32_e32 v68, 1.0, v68
	v_mul_f32_e32 v69, 0xbfb8aa3b, v69
	v_rcp_f32_e32 v68, v68
	v_exp_f32_e32 v69, v69
	v_mul_f32_e32 v7, v70, v7
	v_mul_f32_e32 v65, v71, v65
	v_cvt_pk_bf16_f32 v65, v7, v65
	v_mul_f32_e32 v7, v66, v68
	v_add_f32_e32 v66, 1.0, v69
	v_lshlrev_b32_e32 v68, 16, v117
	v_and_b32_e32 v69, 0xffff0000, v117
	v_mul_f32_e32 v68, 0xbfb8aa3b, v68
	v_mul_f32_e32 v69, 0xbfb8aa3b, v69
	v_exp_f32_e32 v68, v68
	v_exp_f32_e32 v69, v69
	v_rcp_f32_e32 v66, v66
	v_add_f32_e32 v68, 1.0, v68
	v_add_f32_e32 v69, 1.0, v69
	v_rcp_f32_e32 v68, v68
	v_rcp_f32_e32 v69, v69
	v_mul_f32_e32 v66, v67, v66
	v_cvt_pk_bf16_f32 v66, v7, v66
	v_mul_f32_e32 v7, v128, v68
	v_mul_f32_e32 v67, v129, v69
	v_lshl_add_u64 v[68:69], s[6:7], 0, v[126:127]
	v_lshl_add_u64 v[68:69], v[68:69], 0, v[4:5]
	v_cvt_pk_bf16_f32 v67, v7, v67
	global_store_dwordx4 v[68:69], v[64:67], off sc1
	s_waitcnt vmcnt(8)
	v_lshlrev_b32_e32 v7, 16, v118
	v_mul_f32_e32 v7, 0xbfb8aa3b, v7
	v_pk_mul_f32 v[64:65], v[58:59], v[90:91]
	v_and_b32_e32 v58, 0xffff0000, v118
	v_mul_f32_e32 v58, 0xbfb8aa3b, v58
	v_exp_f32_e32 v7, v7
	v_exp_f32_e32 v66, v58
	v_pk_mul_f32 v[58:59], v[56:57], v[88:89]
	v_lshlrev_b32_e32 v57, 16, v119
	v_add_f32_e32 v7, 1.0, v7
	v_add_f32_e32 v56, 1.0, v66
	v_rcp_f32_e32 v7, v7
	v_rcp_f32_e32 v56, v56
	v_mul_f32_e32 v57, 0xbfb8aa3b, v57
	v_exp_f32_e32 v57, v57
	v_mul_f32_e32 v7, v60, v7
	v_mul_f32_e32 v56, v61, v56
	v_cvt_pk_bf16_f32 v56, v7, v56
	v_add_f32_e32 v7, 1.0, v57
	v_and_b32_e32 v57, 0xffff0000, v119
	v_mul_f32_e32 v57, 0xbfb8aa3b, v57
	v_lshlrev_b32_e32 v60, 16, v120
	v_exp_f32_e32 v57, v57
	v_mul_f32_e32 v60, 0xbfb8aa3b, v60
	v_exp_f32_e32 v60, v60
	v_and_b32_e32 v61, 0xffff0000, v120
	v_add_f32_e32 v57, 1.0, v57
	v_rcp_f32_e32 v7, v7
	v_rcp_f32_e32 v57, v57
	v_add_f32_e32 v60, 1.0, v60
	v_mul_f32_e32 v61, 0xbfb8aa3b, v61
	v_rcp_f32_e32 v60, v60
	v_exp_f32_e32 v61, v61
	v_mul_f32_e32 v7, v62, v7
	v_mul_f32_e32 v57, v63, v57
	v_cvt_pk_bf16_f32 v57, v7, v57
	v_mul_f32_e32 v7, v58, v60
	v_add_f32_e32 v58, 1.0, v61
	v_lshlrev_b32_e32 v60, 16, v121
	v_and_b32_e32 v61, 0xffff0000, v121
	v_mul_f32_e32 v60, 0xbfb8aa3b, v60
	v_mul_f32_e32 v61, 0xbfb8aa3b, v61
	v_exp_f32_e32 v60, v60
	v_exp_f32_e32 v61, v61
	v_rcp_f32_e32 v58, v58
	v_add_f32_e32 v60, 1.0, v60
	v_add_f32_e32 v61, 1.0, v61
	v_rcp_f32_e32 v60, v60
	v_rcp_f32_e32 v61, v61
	v_mul_f32_e32 v58, v59, v58
	v_cvt_pk_bf16_f32 v58, v7, v58
	v_mul_f32_e32 v7, v64, v60
	v_mul_f32_e32 v59, v65, v61
	v_cvt_pk_bf16_f32 v59, v7, v59
	global_store_dwordx4 v[68:69], v[56:59], off offset:256 sc1
	s_waitcnt vmcnt(7)
	v_lshlrev_b32_e32 v7, 16, v122
	v_mul_f32_e32 v7, 0xbfb8aa3b, v7
	v_pk_mul_f32 v[56:57], v[50:51], v[106:107]
	v_and_b32_e32 v50, 0xffff0000, v122
	v_mul_f32_e32 v50, 0xbfb8aa3b, v50
	v_exp_f32_e32 v7, v7
	v_exp_f32_e32 v58, v50
	v_pk_mul_f32 v[50:51], v[48:49], v[104:105]
	v_lshlrev_b32_e32 v49, 16, v123
	v_add_f32_e32 v7, 1.0, v7
	v_add_f32_e32 v48, 1.0, v58
	v_rcp_f32_e32 v7, v7
	v_rcp_f32_e32 v48, v48
	v_mul_f32_e32 v49, 0xbfb8aa3b, v49
	v_exp_f32_e32 v49, v49
	v_mul_f32_e32 v7, v52, v7
	v_mul_f32_e32 v48, v53, v48
	v_cvt_pk_bf16_f32 v48, v7, v48
	v_add_f32_e32 v7, 1.0, v49
	v_and_b32_e32 v49, 0xffff0000, v123
	v_mul_f32_e32 v49, 0xbfb8aa3b, v49
	v_lshlrev_b32_e32 v52, 16, v124
	v_exp_f32_e32 v49, v49
	v_mul_f32_e32 v52, 0xbfb8aa3b, v52
	v_exp_f32_e32 v52, v52
	v_and_b32_e32 v53, 0xffff0000, v124
	v_add_f32_e32 v49, 1.0, v49
	v_rcp_f32_e32 v7, v7
	v_rcp_f32_e32 v49, v49
	v_add_f32_e32 v52, 1.0, v52
	v_mul_f32_e32 v53, 0xbfb8aa3b, v53
	v_rcp_f32_e32 v52, v52
	v_exp_f32_e32 v53, v53
	v_mul_f32_e32 v7, v54, v7
	v_mul_f32_e32 v49, v55, v49
	v_cvt_pk_bf16_f32 v49, v7, v49
	v_mul_f32_e32 v7, v50, v52
	v_add_f32_e32 v50, 1.0, v53
	v_lshlrev_b32_e32 v52, 16, v125
	v_and_b32_e32 v53, 0xffff0000, v125
	v_mul_f32_e32 v52, 0xbfb8aa3b, v52
	v_mul_f32_e32 v53, 0xbfb8aa3b, v53
	v_exp_f32_e32 v52, v52
	v_exp_f32_e32 v53, v53
	v_rcp_f32_e32 v50, v50
	v_add_f32_e32 v52, 1.0, v52
	v_add_f32_e32 v53, 1.0, v53
	v_rcp_f32_e32 v52, v52
	v_rcp_f32_e32 v53, v53
	v_mul_f32_e32 v50, v51, v50
	v_cvt_pk_bf16_f32 v50, v7, v50
	v_mul_f32_e32 v7, v56, v52
	v_mul_f32_e32 v51, v57, v53
	v_lshl_add_u64 v[52:53], s[6:7], 0, v[112:113]
	v_lshl_add_u64 v[52:53], v[52:53], 0, v[4:5]
	v_cvt_pk_bf16_f32 v51, v7, v51
	global_store_dwordx4 v[52:53], v[48:51], off sc1
	s_waitcnt vmcnt(7)
	v_lshlrev_b32_e32 v7, 16, v96
	v_mul_f32_e32 v7, 0xbfb8aa3b, v7
	v_pk_mul_f32 v[48:49], v[42:43], v[90:91]
	v_and_b32_e32 v42, 0xffff0000, v96
	v_mul_f32_e32 v42, 0xbfb8aa3b, v42
	v_exp_f32_e32 v7, v7
	v_exp_f32_e32 v50, v42
	v_pk_mul_f32 v[42:43], v[40:41], v[88:89]
	v_lshlrev_b32_e32 v41, 16, v97
	v_add_f32_e32 v7, 1.0, v7
	v_add_f32_e32 v40, 1.0, v50
	v_rcp_f32_e32 v7, v7
	v_rcp_f32_e32 v40, v40
	v_mul_f32_e32 v41, 0xbfb8aa3b, v41
	v_exp_f32_e32 v41, v41
	v_mul_f32_e32 v7, v44, v7
	v_mul_f32_e32 v40, v45, v40
	v_cvt_pk_bf16_f32 v40, v7, v40
	v_add_f32_e32 v7, 1.0, v41
	v_and_b32_e32 v41, 0xffff0000, v97
	v_mul_f32_e32 v41, 0xbfb8aa3b, v41
	v_lshlrev_b32_e32 v44, 16, v98
	v_exp_f32_e32 v41, v41
	v_mul_f32_e32 v44, 0xbfb8aa3b, v44
	v_exp_f32_e32 v44, v44
	v_and_b32_e32 v45, 0xffff0000, v98
	v_add_f32_e32 v41, 1.0, v41
	v_rcp_f32_e32 v7, v7
	v_rcp_f32_e32 v41, v41
	v_add_f32_e32 v44, 1.0, v44
	v_mul_f32_e32 v45, 0xbfb8aa3b, v45
	v_rcp_f32_e32 v44, v44
	v_exp_f32_e32 v45, v45
	v_mul_f32_e32 v7, v46, v7
	v_mul_f32_e32 v41, v47, v41
	v_cvt_pk_bf16_f32 v41, v7, v41
	v_mul_f32_e32 v7, v42, v44
	v_add_f32_e32 v42, 1.0, v45
	v_lshlrev_b32_e32 v44, 16, v99
	v_and_b32_e32 v45, 0xffff0000, v99
	v_mul_f32_e32 v44, 0xbfb8aa3b, v44
	v_mul_f32_e32 v45, 0xbfb8aa3b, v45
	v_exp_f32_e32 v44, v44
	v_exp_f32_e32 v45, v45
	v_rcp_f32_e32 v42, v42
	v_add_f32_e32 v44, 1.0, v44
	v_add_f32_e32 v45, 1.0, v45
	v_rcp_f32_e32 v44, v44
	v_rcp_f32_e32 v45, v45
	v_mul_f32_e32 v42, v43, v42
	v_cvt_pk_bf16_f32 v42, v7, v42
	v_mul_f32_e32 v7, v48, v44
	v_mul_f32_e32 v43, v49, v45
	v_cvt_pk_bf16_f32 v43, v7, v43
	global_store_dwordx4 v[52:53], v[40:43], off offset:256 sc1
	s_waitcnt vmcnt(7)
	v_lshlrev_b32_e32 v7, 16, v84
	v_mul_f32_e32 v7, 0xbfb8aa3b, v7
	v_pk_mul_f32 v[40:41], v[26:27], v[106:107]
	v_and_b32_e32 v26, 0xffff0000, v84
	v_mul_f32_e32 v26, 0xbfb8aa3b, v26
	v_exp_f32_e32 v7, v7
	v_exp_f32_e32 v42, v26
	v_pk_mul_f32 v[26:27], v[24:25], v[104:105]
	v_lshlrev_b32_e32 v25, 16, v85
	v_add_f32_e32 v7, 1.0, v7
	v_add_f32_e32 v24, 1.0, v42
	v_rcp_f32_e32 v7, v7
	v_rcp_f32_e32 v24, v24
	v_mul_f32_e32 v25, 0xbfb8aa3b, v25
	v_exp_f32_e32 v25, v25
	v_mul_f32_e32 v7, v36, v7
	v_mul_f32_e32 v24, v37, v24
	v_cvt_pk_bf16_f32 v24, v7, v24
	v_add_f32_e32 v7, 1.0, v25
	v_and_b32_e32 v25, 0xffff0000, v85
	v_mul_f32_e32 v25, 0xbfb8aa3b, v25
	v_lshlrev_b32_e32 v36, 16, v86
	v_exp_f32_e32 v25, v25
	v_mul_f32_e32 v36, 0xbfb8aa3b, v36
	v_exp_f32_e32 v36, v36
	v_and_b32_e32 v37, 0xffff0000, v86
	v_add_f32_e32 v25, 1.0, v25
	v_rcp_f32_e32 v7, v7
	v_rcp_f32_e32 v25, v25
	v_add_f32_e32 v36, 1.0, v36
	v_mul_f32_e32 v37, 0xbfb8aa3b, v37
	v_rcp_f32_e32 v36, v36
	v_exp_f32_e32 v37, v37
	v_mul_f32_e32 v7, v38, v7
	v_mul_f32_e32 v25, v39, v25
	v_cvt_pk_bf16_f32 v25, v7, v25
	v_mul_f32_e32 v7, v26, v36
	v_add_f32_e32 v26, 1.0, v37
	v_lshlrev_b32_e32 v36, 16, v87
	v_and_b32_e32 v37, 0xffff0000, v87
	v_mul_f32_e32 v36, 0xbfb8aa3b, v36
	v_mul_f32_e32 v37, 0xbfb8aa3b, v37
	v_exp_f32_e32 v36, v36
	v_exp_f32_e32 v37, v37
	v_rcp_f32_e32 v26, v26
	v_add_f32_e32 v36, 1.0, v36
	v_add_f32_e32 v37, 1.0, v37
	v_rcp_f32_e32 v36, v36
	v_rcp_f32_e32 v37, v37
	v_mul_f32_e32 v26, v27, v26
	v_cvt_pk_bf16_f32 v26, v7, v26
	v_mul_f32_e32 v7, v40, v36
	v_mul_f32_e32 v27, v41, v37
	v_lshl_add_u64 v[36:37], s[6:7], 0, v[102:103]
	v_lshl_add_u64 v[36:37], v[36:37], 0, v[4:5]
	v_cvt_pk_bf16_f32 v27, v7, v27
	global_store_dwordx4 v[36:37], v[24:27], off sc1
	s_waitcnt vmcnt(7)
	v_lshlrev_b32_e32 v7, 16, v80
	v_mul_f32_e32 v7, 0xbfb8aa3b, v7
	v_pk_mul_f32 v[24:25], v[32:33], v[92:93]
	v_and_b32_e32 v32, 0xffff0000, v80
	v_mul_f32_e32 v32, 0xbfb8aa3b, v32
	v_exp_f32_e32 v7, v7
	v_exp_f32_e32 v32, v32
	v_lshlrev_b32_e32 v33, 16, v81
	v_mul_f32_e32 v33, 0xbfb8aa3b, v33
	v_add_f32_e32 v7, 1.0, v7
	v_add_f32_e32 v32, 1.0, v32
	v_rcp_f32_e32 v7, v7
	v_rcp_f32_e32 v32, v32
	v_exp_f32_e32 v33, v33
	v_pk_mul_f32 v[26:27], v[34:35], v[94:95]
	v_mul_f32_e32 v7, v24, v7
	v_mul_f32_e32 v24, v25, v32
	v_and_b32_e32 v25, 0xffff0000, v81
	v_mul_f32_e32 v25, 0xbfb8aa3b, v25
	v_lshlrev_b32_e32 v32, 16, v82
	v_cvt_pk_bf16_f32 v24, v7, v24
	v_add_f32_e32 v7, 1.0, v33
	v_exp_f32_e32 v25, v25
	v_mul_f32_e32 v32, 0xbfb8aa3b, v32
	v_rcp_f32_e32 v7, v7
	v_exp_f32_e32 v32, v32
	v_add_f32_e32 v25, 1.0, v25
	v_rcp_f32_e32 v25, v25
	v_mul_f32_e32 v7, v26, v7
	v_add_f32_e32 v26, 1.0, v32
	v_rcp_f32_e32 v26, v26
	v_and_b32_e32 v32, 0xffff0000, v82
	v_mul_f32_e32 v25, v27, v25
	v_mul_f32_e32 v32, 0xbfb8aa3b, v32
	v_cvt_pk_bf16_f32 v25, v7, v25
	v_mul_f32_e32 v7, v28, v26
	v_lshlrev_b32_e32 v27, 16, v83
	v_and_b32_e32 v28, 0xffff0000, v83
	v_exp_f32_e32 v32, v32
	v_mul_f32_e32 v27, 0xbfb8aa3b, v27
	v_mul_f32_e32 v28, 0xbfb8aa3b, v28
	v_exp_f32_e32 v27, v27
	v_exp_f32_e32 v28, v28
	v_add_f32_e32 v26, 1.0, v32
	v_rcp_f32_e32 v26, v26
	v_add_f32_e32 v27, 1.0, v27
	v_add_f32_e32 v28, 1.0, v28
	v_rcp_f32_e32 v27, v27
	v_rcp_f32_e32 v28, v28
	v_mul_f32_e32 v26, v29, v26
	v_cvt_pk_bf16_f32 v26, v7, v26
	v_mul_f32_e32 v7, v30, v27
	v_mul_f32_e32 v27, v31, v28
	v_cvt_pk_bf16_f32 v27, v7, v27
	global_store_dwordx4 v[36:37], v[24:27], off offset:256 sc1
	s_waitcnt vmcnt(7)
	v_lshlrev_b32_e32 v7, 16, v76
	v_mul_f32_e32 v7, 0xbfb8aa3b, v7
	v_pk_mul_f32 v[24:25], v[10:11], v[106:107]
	v_and_b32_e32 v10, 0xffff0000, v76
	v_mul_f32_e32 v10, 0xbfb8aa3b, v10
	v_exp_f32_e32 v7, v7
	v_exp_f32_e32 v26, v10
	v_pk_mul_f32 v[10:11], v[8:9], v[104:105]
	v_lshlrev_b32_e32 v9, 16, v77
	v_add_f32_e32 v7, 1.0, v7
	v_add_f32_e32 v8, 1.0, v26
	v_rcp_f32_e32 v7, v7
	v_rcp_f32_e32 v8, v8
	v_mul_f32_e32 v9, 0xbfb8aa3b, v9
	v_exp_f32_e32 v9, v9
	v_mul_f32_e32 v7, v12, v7
	v_mul_f32_e32 v8, v13, v8
	v_cvt_pk_bf16_f32 v8, v7, v8
	v_add_f32_e32 v7, 1.0, v9
	v_and_b32_e32 v9, 0xffff0000, v77
	v_mul_f32_e32 v9, 0xbfb8aa3b, v9
	v_lshlrev_b32_e32 v12, 16, v78
	v_exp_f32_e32 v9, v9
	v_mul_f32_e32 v12, 0xbfb8aa3b, v12
	v_exp_f32_e32 v12, v12
	v_and_b32_e32 v13, 0xffff0000, v78
	v_add_f32_e32 v9, 1.0, v9
	v_rcp_f32_e32 v7, v7
	v_rcp_f32_e32 v9, v9
	v_add_f32_e32 v12, 1.0, v12
	v_mul_f32_e32 v13, 0xbfb8aa3b, v13
	v_rcp_f32_e32 v12, v12
	v_exp_f32_e32 v13, v13
	v_mul_f32_e32 v7, v14, v7
	v_mul_f32_e32 v9, v15, v9
	v_cvt_pk_bf16_f32 v9, v7, v9
	v_mul_f32_e32 v7, v10, v12
	v_add_f32_e32 v10, 1.0, v13
	v_lshlrev_b32_e32 v12, 16, v79
	v_and_b32_e32 v13, 0xffff0000, v79
	v_mul_f32_e32 v12, 0xbfb8aa3b, v12
	v_mul_f32_e32 v13, 0xbfb8aa3b, v13
	v_exp_f32_e32 v12, v12
	v_exp_f32_e32 v13, v13
	v_rcp_f32_e32 v10, v10
	s_waitcnt vmcnt(6)
	v_and_b32_e32 v14, 0xffff0000, v72
	v_add_f32_e32 v12, 1.0, v12
	v_add_f32_e32 v13, 1.0, v13
	v_rcp_f32_e32 v12, v12
	v_rcp_f32_e32 v13, v13
	v_mul_f32_e32 v10, v11, v10
	v_cvt_pk_bf16_f32 v10, v7, v10
	v_mul_f32_e32 v7, v24, v12
	v_mul_f32_e32 v11, v25, v13
	v_cvt_pk_bf16_f32 v11, v7, v11
	v_lshlrev_b32_e32 v7, 16, v72
	v_lshl_add_u64 v[12:13], s[6:7], 0, v[100:101]
	v_mul_f32_e32 v7, 0xbfb8aa3b, v7
	v_mul_f32_e32 v14, 0xbfb8aa3b, v14
	v_lshl_add_u64 v[4:5], v[12:13], 0, v[4:5]
	v_pk_mul_f32 v[12:13], v[18:19], v[90:91]
	v_exp_f32_e32 v7, v7
	v_exp_f32_e32 v18, v14
	v_pk_mul_f32 v[14:15], v[16:17], v[88:89]
	v_lshlrev_b32_e32 v17, 16, v73
	v_add_f32_e32 v7, 1.0, v7
	v_add_f32_e32 v16, 1.0, v18
	v_rcp_f32_e32 v7, v7
	v_rcp_f32_e32 v16, v16
	v_mul_f32_e32 v17, 0xbfb8aa3b, v17
	v_exp_f32_e32 v17, v17
	global_store_dwordx4 v[4:5], v[8:11], off sc1
	s_nop 1
	v_pk_mul_f32 v[8:9], v[20:21], v[92:93]
	v_pk_mul_f32 v[10:11], v[22:23], v[94:95]
	v_mul_f32_e32 v7, v8, v7
	v_mul_f32_e32 v8, v9, v16
	v_and_b32_e32 v9, 0xffff0000, v73
	v_mul_f32_e32 v9, 0xbfb8aa3b, v9
	v_lshlrev_b32_e32 v16, 16, v74
	v_cvt_pk_bf16_f32 v8, v7, v8
	v_add_f32_e32 v7, 1.0, v17
	v_exp_f32_e32 v9, v9
	v_mul_f32_e32 v16, 0xbfb8aa3b, v16
	v_rcp_f32_e32 v7, v7
	v_exp_f32_e32 v16, v16
	v_add_f32_e32 v9, 1.0, v9
	v_rcp_f32_e32 v9, v9
	v_mul_f32_e32 v7, v10, v7
	v_add_f32_e32 v10, 1.0, v16
	v_rcp_f32_e32 v10, v10
	v_and_b32_e32 v16, 0xffff0000, v74
	v_mul_f32_e32 v9, v11, v9
	v_mul_f32_e32 v16, 0xbfb8aa3b, v16
	v_cvt_pk_bf16_f32 v9, v7, v9
	v_mul_f32_e32 v7, v14, v10
	v_lshlrev_b32_e32 v11, 16, v75
	v_and_b32_e32 v14, 0xffff0000, v75
	v_exp_f32_e32 v16, v16
	v_mul_f32_e32 v11, 0xbfb8aa3b, v11
	v_mul_f32_e32 v14, 0xbfb8aa3b, v14
	v_exp_f32_e32 v11, v11
	v_exp_f32_e32 v14, v14
	v_add_f32_e32 v10, 1.0, v16
	v_rcp_f32_e32 v10, v10
	v_add_f32_e32 v11, 1.0, v11
	v_add_f32_e32 v14, 1.0, v14
	v_rcp_f32_e32 v11, v11
	v_rcp_f32_e32 v14, v14
	v_mul_f32_e32 v10, v15, v10
	v_cvt_pk_bf16_f32 v10, v7, v10
	v_mul_f32_e32 v7, v12, v11
	v_mul_f32_e32 v11, v13, v14
	v_cvt_pk_bf16_f32 v11, v7, v11
	global_store_dwordx4 v[4:5], v[8:11], off offset:256 sc1
	s_cbranch_vccnz .LBB0_467
	s_andn2_b64 vcc, exec, s[4:5]
	s_cbranch_vccnz .LBB0_466
	s_barrier
	s_branch .LBB0_466

.LBB0_484:
	v_add_u32_e32 v2, 0xfffffe40, v18
	v_ashrrev_i32_e32 v3, 31, v2
	v_lshl_add_u64 v[2:3], v[2:3], 2, s[4:5]
	global_load_dword v72, v[2:3], off
	v_add_u32_e32 v2, 0xfffffe80, v18
	v_ashrrev_i32_e32 v3, 31, v2
	v_add_co_u32_e32 v70, vcc, 0xff900000, v20
	v_lshl_add_u64 v[2:3], v[2:3], 2, s[4:5]
	s_nop 0
	v_addc_co_u32_e32 v71, vcc, -1, v21, vcc
	global_load_dword v78, v[2:3], off
	v_add_u32_e32 v2, 0xfffffec0, v18
	v_add_co_u32_e32 v74, vcc, 0xffa00000, v20
	v_ashrrev_i32_e32 v3, 31, v2
	global_load_dwordx4 v[50:53], v[70:71], off nt
	v_addc_co_u32_e32 v75, vcc, -1, v21, vcc
	v_lshl_add_u64 v[2:3], v[2:3], 2, s[4:5]
	global_load_dwordx4 v[54:57], v[74:75], off nt
	global_load_dword v36, v[2:3], off
	v_add_u32_e32 v2, 0xffffff00, v18
	v_add_co_u32_e32 v76, vcc, 0xffb00000, v20
	v_ashrrev_i32_e32 v3, 31, v2
	s_nop 0
	v_addc_co_u32_e32 v77, vcc, -1, v21, vcc
	v_lshl_add_u64 v[2:3], v[2:3], 2, s[4:5]
	v_add_co_u32_e32 v24, vcc, 0xffc00000, v20
	global_load_dword v40, v[2:3], off
	v_add_u32_e32 v2, 0xffffff40, v18
	v_addc_co_u32_e32 v25, vcc, -1, v21, vcc
	v_ashrrev_i32_e32 v3, 31, v2
	v_add_co_u32_e32 v26, vcc, 0xffd00000, v20
	v_lshl_add_u64 v[2:3], v[2:3], 2, s[4:5]
	s_nop 0
	v_addc_co_u32_e32 v27, vcc, -1, v21, vcc
	global_load_dword v42, v[2:3], off
	v_add_u32_e32 v2, 0xffffff80, v18
	global_load_dwordx4 v[58:61], v[76:77], off nt
	v_add_co_u32_e32 v28, vcc, 0xffe00000, v20
	v_ashrrev_i32_e32 v3, 31, v2
	global_load_dwordx4 v[62:65], v[24:25], off nt
	global_load_dwordx4 v[6:9], v[26:27], off nt
	v_addc_co_u32_e32 v29, vcc, -1, v21, vcc
	v_lshl_add_u64 v[2:3], v[2:3], 2, s[4:5]
	global_load_dword v44, v[2:3], off
	v_add_co_u32_e32 v30, vcc, 0xfff00000, v20
	v_subrev_u32_e32 v2, 64, v18
	global_load_dwordx4 v[10:13], v[28:29], off nt
	v_addc_co_u32_e32 v31, vcc, -1, v21, vcc
	v_ashrrev_i32_e32 v3, 31, v2
	global_load_dwordx4 v[14:17], v[30:31], off nt
	v_lshl_add_u64 v[2:3], v[2:3], 2, s[4:5]
	v_ashrrev_i32_e32 v19, 31, v18
	global_load_dword v46, v[2:3], off
	s_nop 0
	global_load_dwordx4 v[2:5], v[20:21], off nt
	v_lshl_add_u64 v[66:67], v[18:19], 2, s[4:5]
	global_load_dword v34, v[66:67], off
	v_cvt_pk_bf16_f32 v66, v22, v23
	v_cvt_pk_bf16_f32 v67, v32, v33
	v_cvt_pk_bf16_f32 v68, v38, v39
	v_cvt_pk_bf16_f32 v69, v48, v41
	global_store_dwordx4 v[70:71], v[66:69], off sc1
	s_add_i32 s17, s17, 8
	v_add_u32_e32 v18, 0x200, v18
	s_cmp_gt_u32 s17, 55
	s_waitcnt vmcnt(14)
	v_lshlrev_b32_e32 v66, 16, v50
	v_and_b32_e32 v67, 0xffff0000, v50
	v_pk_fma_f32 v[22:23], v[22:23], v[72:73], v[66:67] op_sel_hi:[1,0,1]
	s_waitcnt vmcnt(13)
	v_lshlrev_b32_e32 v66, 16, v54
	v_and_b32_e32 v67, 0xffff0000, v54
	v_cvt_pk_bf16_f32 v50, v22, v23
	v_pk_fma_f32 v[22:23], v[78:79], v[22:23], v[66:67] op_sel_hi:[0,1,1]
	v_lshlrev_b32_e32 v66, 16, v51
	v_and_b32_e32 v67, 0xffff0000, v51
	v_pk_fma_f32 v[32:33], v[32:33], v[72:73], v[66:67] op_sel_hi:[1,0,1]
	v_lshlrev_b32_e32 v66, 16, v55
	v_and_b32_e32 v67, 0xffff0000, v55
	v_cvt_pk_bf16_f32 v51, v32, v33
	v_pk_fma_f32 v[32:33], v[78:79], v[32:33], v[66:67] op_sel_hi:[0,1,1]
	v_lshlrev_b32_e32 v66, 16, v52
	v_and_b32_e32 v67, 0xffff0000, v52
	v_pk_fma_f32 v[38:39], v[38:39], v[72:73], v[66:67] op_sel_hi:[1,0,1]
	v_lshlrev_b32_e32 v66, 16, v56
	v_and_b32_e32 v67, 0xffff0000, v56
	v_cvt_pk_bf16_f32 v52, v38, v39
	v_pk_fma_f32 v[38:39], v[78:79], v[38:39], v[66:67] op_sel_hi:[0,1,1]
	v_lshlrev_b32_e32 v66, 16, v53
	v_and_b32_e32 v67, 0xffff0000, v53
	v_pk_fma_f32 v[48:49], v[48:49], v[72:73], v[66:67] op_sel_hi:[1,0,1]
	s_waitcnt vmcnt(9)
	v_lshlrev_b32_e32 v68, 16, v58
	v_cvt_pk_bf16_f32 v53, v48, v49
	global_store_dwordx4 v[74:75], v[50:53], off sc1
	v_and_b32_e32 v69, 0xffff0000, v58
	v_lshlrev_b32_e32 v54, 16, v59
	v_lshlrev_b32_e32 v50, 16, v57
	v_and_b32_e32 v51, 0xffff0000, v57
	v_and_b32_e32 v55, 0xffff0000, v59
	v_pk_fma_f32 v[52:53], v[78:79], v[48:49], v[50:51] op_sel_hi:[0,1,1]
	v_cvt_pk_bf16_f32 v48, v22, v23
	v_cvt_pk_bf16_f32 v49, v32, v33
	v_cvt_pk_bf16_f32 v50, v38, v39
	v_cvt_pk_bf16_f32 v51, v52, v53
	v_lshlrev_b32_e32 v58, 16, v60
	v_and_b32_e32 v59, 0xffff0000, v60
	v_lshlrev_b32_e32 v56, 16, v61
	global_store_dwordx4 v[76:77], v[48:51], off sc1
	v_and_b32_e32 v57, 0xffff0000, v61
	s_waitcnt vmcnt(10)
	v_lshlrev_b32_e32 v60, 16, v63
	v_lshlrev_b32_e32 v50, 16, v62
	v_and_b32_e32 v51, 0xffff0000, v62
	v_and_b32_e32 v61, 0xffff0000, v63
	v_pk_fma_f32 v[22:23], v[36:37], v[22:23], v[68:69] op_sel_hi:[0,1,1]
	v_pk_fma_f32 v[32:33], v[36:37], v[32:33], v[54:55] op_sel_hi:[0,1,1]
	v_cvt_pk_bf16_f32 v48, v22, v23
	v_pk_fma_f32 v[66:67], v[40:41], v[22:23], v[50:51] op_sel_hi:[0,1,1]
	s_waitcnt vmcnt(9)
	v_lshlrev_b32_e32 v22, 16, v6
	v_and_b32_e32 v23, 0xffff0000, v6
	v_pk_fma_f32 v[54:55], v[40:41], v[32:33], v[60:61] op_sel_hi:[0,1,1]
	v_lshlrev_b32_e32 v6, 16, v7
	v_and_b32_e32 v7, 0xffff0000, v7
	v_pk_fma_f32 v[68:69], v[42:43], v[66:67], v[22:23] op_sel_hi:[0,1,1]
	s_waitcnt vmcnt(7)
	v_lshlrev_b32_e32 v22, 16, v10
	v_and_b32_e32 v23, 0xffff0000, v10
	v_pk_fma_f32 v[60:61], v[42:43], v[54:55], v[6:7] op_sel_hi:[0,1,1]
	v_lshlrev_b32_e32 v6, 16, v11
	v_and_b32_e32 v7, 0xffff0000, v11
	v_pk_fma_f32 v[70:71], v[44:45], v[68:69], v[22:23] op_sel_hi:[0,1,1]
	s_waitcnt vmcnt(6)
	v_lshlrev_b32_e32 v22, 16, v14
	v_and_b32_e32 v23, 0xffff0000, v14
	v_pk_fma_f32 v[10:11], v[44:45], v[60:61], v[6:7] op_sel_hi:[0,1,1]
	v_lshlrev_b32_e32 v6, 16, v15
	v_and_b32_e32 v7, 0xffff0000, v15
	s_waitcnt vmcnt(5)
	v_pk_fma_f32 v[72:73], v[46:47], v[70:71], v[22:23] op_sel_hi:[0,1,1]
	s_waitcnt vmcnt(4)
	v_lshlrev_b32_e32 v22, 16, v2
	v_and_b32_e32 v23, 0xffff0000, v2
	v_pk_fma_f32 v[14:15], v[46:47], v[10:11], v[6:7] op_sel_hi:[0,1,1]
	v_lshlrev_b32_e32 v2, 16, v3
	v_and_b32_e32 v3, 0xffff0000, v3
	v_lshlrev_b32_e32 v62, 16, v64
	v_and_b32_e32 v63, 0xffff0000, v64
	v_cvt_pk_bf16_f32 v49, v32, v33
	s_waitcnt vmcnt(3)
	v_pk_fma_f32 v[32:33], v[34:35], v[14:15], v[2:3] op_sel_hi:[0,1,1]
	v_pk_fma_f32 v[2:3], v[36:37], v[38:39], v[58:59] op_sel_hi:[0,1,1]
	v_pk_fma_f32 v[58:59], v[40:41], v[2:3], v[62:63] op_sel_hi:[0,1,1]
	v_lshlrev_b32_e32 v6, 16, v8
	v_and_b32_e32 v7, 0xffff0000, v8
	v_pk_fma_f32 v[62:63], v[42:43], v[58:59], v[6:7] op_sel_hi:[0,1,1]
	v_lshlrev_b32_e32 v6, 16, v12
	v_and_b32_e32 v7, 0xffff0000, v12
	v_pk_fma_f32 v[74:75], v[44:45], v[62:63], v[6:7] op_sel_hi:[0,1,1]
	v_lshlrev_b32_e32 v6, 16, v16
	v_and_b32_e32 v7, 0xffff0000, v16
	v_pk_fma_f32 v[76:77], v[46:47], v[74:75], v[6:7] op_sel_hi:[0,1,1]
	v_cvt_pk_bf16_f32 v50, v2, v3
	v_lshlrev_b32_e32 v2, 16, v4
	v_and_b32_e32 v3, 0xffff0000, v4
	v_lshlrev_b32_e32 v64, 16, v65
	v_and_b32_e32 v65, 0xffff0000, v65
	v_pk_fma_f32 v[38:39], v[34:35], v[76:77], v[2:3] op_sel_hi:[0,1,1]
	v_pk_fma_f32 v[2:3], v[36:37], v[52:53], v[56:57] op_sel_hi:[0,1,1]
	v_pk_fma_f32 v[40:41], v[40:41], v[2:3], v[64:65] op_sel_hi:[0,1,1]
	v_lshlrev_b32_e32 v6, 16, v9
	v_and_b32_e32 v7, 0xffff0000, v9
	v_pk_fma_f32 v[42:43], v[42:43], v[40:41], v[6:7] op_sel_hi:[0,1,1]
	v_lshlrev_b32_e32 v6, 16, v13
	v_and_b32_e32 v7, 0xffff0000, v13
	v_pk_fma_f32 v[12:13], v[44:45], v[42:43], v[6:7] op_sel_hi:[0,1,1]
	v_lshlrev_b32_e32 v6, 16, v17
	v_and_b32_e32 v7, 0xffff0000, v17
	v_pk_fma_f32 v[16:17], v[46:47], v[12:13], v[6:7] op_sel_hi:[0,1,1]
	v_cvt_pk_bf16_f32 v51, v2, v3
	global_store_dwordx4 v[24:25], v[48:51], off sc1
	v_cvt_pk_bf16_f32 v6, v66, v67
	v_cvt_pk_bf16_f32 v7, v54, v55
	v_cvt_pk_bf16_f32 v8, v58, v59
	v_cvt_pk_bf16_f32 v9, v40, v41
	global_store_dwordx4 v[26:27], v[6:9], off sc1
	v_lshlrev_b32_e32 v2, 16, v5
	v_and_b32_e32 v3, 0xffff0000, v5
	v_cvt_pk_bf16_f32 v6, v68, v69
	v_cvt_pk_bf16_f32 v7, v60, v61
	v_cvt_pk_bf16_f32 v8, v62, v63
	v_cvt_pk_bf16_f32 v9, v42, v43
	global_store_dwordx4 v[28:29], v[6:9], off sc1
	v_pk_fma_f32 v[48:49], v[34:35], v[16:17], v[2:3] op_sel_hi:[0,1,1]
	v_pk_fma_f32 v[22:23], v[34:35], v[72:73], v[22:23] op_sel_hi:[0,1,1]
	v_cvt_pk_bf16_f32 v6, v70, v71
	v_cvt_pk_bf16_f32 v7, v10, v11
	v_cvt_pk_bf16_f32 v8, v74, v75
	v_cvt_pk_bf16_f32 v9, v12, v13
	global_store_dwordx4 v[30:31], v[6:9], off sc1
	v_mov_b32_e32 v41, v49
	s_nop 0
	v_cvt_pk_bf16_f32 v6, v72, v73
	v_cvt_pk_bf16_f32 v7, v14, v15
	v_cvt_pk_bf16_f32 v8, v76, v77
	v_cvt_pk_bf16_f32 v9, v16, v17
	global_store_dwordx4 v[20:21], v[6:9], off sc1
	v_lshl_add_u64 v[20:21], v[20:21], 0, s[10:11]
	s_cbranch_scc0 .LBB0_484
	v_add_u32_e32 v35, s12, v35
	v_cmp_lt_i32_e32 vcc, s16, v35
	v_add_u32_e32 v37, s13, v37
	s_or_b64 s[8:9], vcc, s[8:9]
	v_add_u32_e32 v1, s14, v1
	s_andn2_b64 exec, exec, s[8:9]
	s_cbranch_execnz .LBB0_483

.LBB0_680:
	v_lshl_add_u32 v186, s46, 8, v220
	v_lshl_or_b32 v184, s47, 8, v222
	v_ashrrev_i32_e32 v187, 31, v186
	v_ashrrev_i32_e32 v185, 31, v184
	v_lshlrev_b64 v[4:5], 11, v[186:187]
	v_lshl_add_u64 v[4:5], v[4:5], 0, v[184:185]
	v_lshlrev_b64 v[4:5], 1, v[4:5]
	v_lshl_add_u64 v[136:137], s[10:11], 0, v[4:5]
	v_lshl_add_u64 v[138:139], s[8:9], 0, v[4:5]
	global_load_dwordx4 v[194:197], v[136:137], off
	global_load_dwordx4 v[212:215], v[138:139], off
	v_or_b32_e32 v192, 16, v186
	v_ashrrev_i32_e32 v193, 31, v192
	v_lshlrev_b64 v[136:137], 11, v[192:193]
	v_lshl_add_u64 v[136:137], v[136:137], 0, v[184:185]
	v_or_b32_e32 v4, 0x100, v4
	v_lshlrev_b64 v[136:137], 1, v[136:137]
	v_lshl_add_u64 v[142:143], s[10:11], 0, v[4:5]
	v_lshl_add_u64 v[4:5], s[8:9], 0, v[4:5]
	v_lshl_add_u64 v[144:145], s[10:11], 0, v[136:137]
	v_lshl_add_u64 v[146:147], s[8:9], 0, v[136:137]
	global_load_dwordx4 v[226:229], v[142:143], off
	global_load_dwordx4 v[230:233], v[4:5], off
	global_load_dwordx4 v[180:183], v[144:145], off
	global_load_dwordx4 v[176:179], v[146:147], off
	v_or_b32_e32 v190, 32, v186
	v_or_b32_e32 v188, 48, v186
	v_ashrrev_i32_e32 v191, 31, v190
	v_ashrrev_i32_e32 v189, 31, v188
	v_lshlrev_b64 v[138:139], 11, v[190:191]
	v_lshlrev_b64 v[140:141], 11, v[188:189]
	v_lshl_add_u64 v[138:139], v[138:139], 0, v[184:185]
	v_lshl_add_u64 v[140:141], v[140:141], 0, v[184:185]
	v_lshlrev_b64 v[138:139], 1, v[138:139]
	v_lshlrev_b64 v[140:141], 1, v[140:141]
	v_or_b32_e32 v136, 0x100, v136
	v_lshl_add_u64 v[148:149], s[10:11], 0, v[138:139]
	v_lshl_add_u64 v[150:151], s[8:9], 0, v[138:139]
	v_or_b32_e32 v138, 0x100, v138
	v_lshl_add_u64 v[152:153], s[10:11], 0, v[140:141]
	v_lshl_add_u64 v[154:155], s[8:9], 0, v[140:141]
	v_or_b32_e32 v140, 0x100, v140
	v_lshl_add_u64 v[4:5], s[10:11], 0, v[136:137]
	v_lshl_add_u64 v[136:137], s[8:9], 0, v[136:137]
	v_lshl_add_u64 v[142:143], s[10:11], 0, v[138:139]
	v_lshl_add_u64 v[138:139], s[8:9], 0, v[138:139]
	global_load_dwordx4 v[164:167], v[148:149], off
	global_load_dwordx4 v[160:163], v[150:151], off
	s_nop 0
	global_load_dwordx4 v[148:151], v[152:153], off
	global_load_dwordx4 v[144:147], v[154:155], off
	v_lshl_add_u64 v[234:235], s[10:11], 0, v[140:141]
	v_lshl_add_u64 v[236:237], s[8:9], 0, v[140:141]
	global_load_dwordx4 v[172:175], v[4:5], off
	global_load_dwordx4 v[168:171], v[136:137], off
	global_load_dwordx4 v[156:159], v[142:143], off
	global_load_dwordx4 v[152:155], v[138:139], off
	s_nop 0
	global_load_dwordx4 v[140:143], v[234:235], off
	global_load_dwordx4 v[136:139], v[236:237], off
	v_lshlrev_b64 v[198:199], 12, v[186:187]
	s_andn2_b64 vcc, exec, s[0:1]
	s_mov_b64 s[0:1], -1
	s_waitcnt vmcnt(0)
	v_lshlrev_b32_e32 v4, 16, v194
	v_and_b32_e32 v7, 0xffff0000, v194
	v_lshlrev_b32_e32 v5, 16, v212
	v_and_b32_e32 v187, 0xffff0000, v212
	v_lshlrev_b32_e32 v212, 16, v196
	v_mul_f32_e32 v4, 0xbfb8aa3b, v4
	v_mul_f32_e32 v7, 0xbfb8aa3b, v7
	v_mul_f32_e32 v212, 0xbfb8aa3b, v212
	v_exp_f32_e32 v4, v4
	v_exp_f32_e32 v7, v7
	v_exp_f32_e32 v212, v212
	v_lshlrev_b32_e32 v194, 16, v195
	v_and_b32_e32 v195, 0xffff0000, v195
	v_and_b32_e32 v196, 0xffff0000, v196
	v_add_f32_e32 v4, 1.0, v4
	v_add_f32_e32 v7, 1.0, v7
	v_mul_f32_e32 v194, 0xbfb8aa3b, v194
	v_mul_f32_e32 v195, 0xbfb8aa3b, v195
	v_mul_f32_e32 v196, 0xbfb8aa3b, v196
	v_add_f32_e32 v212, 1.0, v212
	v_rcp_f32_e32 v4, v4
	v_rcp_f32_e32 v7, v7
	v_exp_f32_e32 v194, v194
	v_exp_f32_e32 v195, v195
	v_exp_f32_e32 v196, v196
	v_rcp_f32_e32 v212, v212
	v_fmac_f32_e32 v5, v132, v4
	v_fmac_f32_e32 v187, v133, v7
	v_lshlrev_b32_e32 v4, 16, v214
	v_lshlrev_b32_e32 v7, 16, v197
	v_add_f32_e32 v194, 1.0, v194
	v_add_f32_e32 v195, 1.0, v195
	v_add_f32_e32 v196, 1.0, v196
	v_fmac_f32_e32 v4, v128, v212
	v_mul_f32_e32 v7, 0xbfb8aa3b, v7
	v_and_b32_e32 v128, 0xffff0000, v197
	v_rcp_f32_e32 v194, v194
	v_rcp_f32_e32 v195, v195
	v_rcp_f32_e32 v196, v196
	v_exp_f32_e32 v7, v7
	v_mul_f32_e32 v128, 0xbfb8aa3b, v128
	v_exp_f32_e32 v128, v128
	v_lshlrev_b32_e32 v205, 16, v213
	v_and_b32_e32 v207, 0xffff0000, v213
	v_cvt_pk_bf16_f32 v132, v5, v187
	v_and_b32_e32 v5, 0xffff0000, v214
	v_fmac_f32_e32 v205, v134, v194
	v_fmac_f32_e32 v207, v135, v195
	v_cvt_pk_bf16_f32 v133, v205, v207
	v_fmac_f32_e32 v5, v129, v196
	v_cvt_pk_bf16_f32 v134, v4, v5
	v_add_f32_e32 v4, 1.0, v7
	v_rcp_f32_e32 v4, v4
	v_add_f32_e32 v5, 1.0, v128
	v_rcp_f32_e32 v5, v5
	v_lshlrev_b32_e32 v7, 16, v215
	v_fmac_f32_e32 v7, v130, v4
	v_and_b32_e32 v4, 0xffff0000, v215
	v_fmac_f32_e32 v4, v131, v5
	v_cvt_pk_bf16_f32 v135, v7, v4
	v_lshlrev_b32_e32 v7, 16, v226
	v_mul_f32_e32 v7, 0xbfb8aa3b, v7
	v_exp_f32_e32 v7, v7
	v_and_b32_e32 v130, 0xffff0000, v226
	v_mul_f32_e32 v130, 0xbfb8aa3b, v130
	v_exp_f32_e32 v130, v130
	v_add_f32_e32 v7, 1.0, v7
	v_rcp_f32_e32 v7, v7
	v_lshlrev_b32_e32 v131, 16, v230
	v_add_f32_e32 v130, 1.0, v130
	v_rcp_f32_e32 v130, v130
	v_fmac_f32_e32 v131, v124, v7
	v_lshlrev_b32_e32 v124, 16, v227
	v_and_b32_e32 v7, 0xffff0000, v230
	v_mul_f32_e32 v124, 0xbfb8aa3b, v124
	v_fmac_f32_e32 v7, v125, v130
	v_exp_f32_e32 v125, v124
	v_and_b32_e32 v124, 0xffff0000, v227
	v_mul_f32_e32 v124, 0xbfb8aa3b, v124
	v_exp_f32_e32 v130, v124
	v_lshl_add_u64 v[128:129], s[8:9], 0, v[198:199]
	v_lshlrev_b64 v[4:5], 1, v[184:185]
	v_lshl_add_u64 v[128:129], v[128:129], 0, v[4:5]
	global_store_dwordx4 v[128:129], v[132:135], off sc1
	v_cvt_pk_bf16_f32 v124, v131, v7
	v_add_f32_e32 v7, 1.0, v125
	v_rcp_f32_e32 v7, v7
	v_add_f32_e32 v125, 1.0, v130
	v_rcp_f32_e32 v125, v125
	v_lshlrev_b32_e32 v130, 16, v231
	v_fmac_f32_e32 v130, v126, v7
	v_and_b32_e32 v7, 0xffff0000, v231
	v_fmac_f32_e32 v7, v127, v125
	v_lshlrev_b32_e32 v125, 16, v228
	v_mul_f32_e32 v125, 0xbfb8aa3b, v125
	v_exp_f32_e32 v126, v125
	v_and_b32_e32 v125, 0xffff0000, v228
	v_mul_f32_e32 v125, 0xbfb8aa3b, v125
	v_exp_f32_e32 v127, v125
	v_cvt_pk_bf16_f32 v125, v130, v7
	v_add_f32_e32 v7, 1.0, v126
	v_rcp_f32_e32 v7, v7
	v_add_f32_e32 v126, 1.0, v127
	v_rcp_f32_e32 v126, v126
	v_lshlrev_b32_e32 v127, 16, v232
	v_fmac_f32_e32 v127, v120, v7
	v_and_b32_e32 v7, 0xffff0000, v232
	v_lshlrev_b32_e32 v120, 16, v229
	v_fmac_f32_e32 v7, v121, v126
	v_mul_f32_e32 v120, 0xbfb8aa3b, v120
	v_and_b32_e32 v121, 0xffff0000, v229
	v_exp_f32_e32 v120, v120
	v_mul_f32_e32 v121, 0xbfb8aa3b, v121
	v_exp_f32_e32 v121, v121
	v_cvt_pk_bf16_f32 v126, v127, v7
	v_add_f32_e32 v7, 1.0, v120
	v_rcp_f32_e32 v7, v7
	v_add_f32_e32 v120, 1.0, v121
	v_rcp_f32_e32 v120, v120
	v_lshlrev_b32_e32 v121, 16, v233
	v_fmac_f32_e32 v121, v122, v7
	v_and_b32_e32 v7, 0xffff0000, v233
	v_fmac_f32_e32 v7, v123, v120
	v_cvt_pk_bf16_f32 v127, v121, v7
	v_lshlrev_b32_e32 v7, 16, v180
	v_mul_f32_e32 v7, 0xbfb8aa3b, v7
	v_exp_f32_e32 v7, v7
	v_and_b32_e32 v120, 0xffff0000, v180
	v_mul_f32_e32 v120, 0xbfb8aa3b, v120
	v_exp_f32_e32 v122, v120
	v_add_f32_e32 v7, 1.0, v7
	v_rcp_f32_e32 v7, v7
	v_lshlrev_b32_e32 v123, 16, v176
	v_add_f32_e32 v122, 1.0, v122
	v_rcp_f32_e32 v122, v122
	v_fmac_f32_e32 v123, v116, v7
	v_lshlrev_b32_e32 v116, 16, v181
	v_and_b32_e32 v7, 0xffff0000, v176
	v_mul_f32_e32 v116, 0xbfb8aa3b, v116
	v_fmac_f32_e32 v7, v117, v122
	v_exp_f32_e32 v117, v116
	v_and_b32_e32 v116, 0xffff0000, v181
	v_mul_f32_e32 v116, 0xbfb8aa3b, v116
	v_exp_f32_e32 v122, v116
	global_store_dwordx4 v[128:129], v[124:127], off offset:256 sc1
	v_cvt_pk_bf16_f32 v116, v123, v7
	v_add_f32_e32 v7, 1.0, v117
	v_rcp_f32_e32 v7, v7
	v_add_f32_e32 v117, 1.0, v122
	v_rcp_f32_e32 v117, v117
	v_lshlrev_b32_e32 v122, 16, v177
	v_fmac_f32_e32 v122, v118, v7
	v_and_b32_e32 v7, 0xffff0000, v177
	v_fmac_f32_e32 v7, v119, v117
	v_lshlrev_b32_e32 v117, 16, v182
	v_mul_f32_e32 v117, 0xbfb8aa3b, v117
	v_exp_f32_e32 v118, v117
	v_and_b32_e32 v117, 0xffff0000, v182
	v_mul_f32_e32 v117, 0xbfb8aa3b, v117
	v_exp_f32_e32 v119, v117
	v_cvt_pk_bf16_f32 v117, v122, v7
	v_add_f32_e32 v7, 1.0, v118
	v_rcp_f32_e32 v7, v7
	v_add_f32_e32 v118, 1.0, v119
	v_rcp_f32_e32 v118, v118
	v_lshlrev_b32_e32 v119, 16, v178
	v_fmac_f32_e32 v119, v112, v7
	v_and_b32_e32 v7, 0xffff0000, v178
	v_lshlrev_b32_e32 v112, 16, v183
	v_fmac_f32_e32 v7, v113, v118
	v_mul_f32_e32 v112, 0xbfb8aa3b, v112
	v_and_b32_e32 v113, 0xffff0000, v183
	v_exp_f32_e32 v112, v112
	v_mul_f32_e32 v113, 0xbfb8aa3b, v113
	v_exp_f32_e32 v113, v113
	v_cvt_pk_bf16_f32 v118, v119, v7
	v_add_f32_e32 v7, 1.0, v112
	v_rcp_f32_e32 v7, v7
	v_add_f32_e32 v112, 1.0, v113
	v_rcp_f32_e32 v112, v112
	v_lshlrev_b32_e32 v113, 16, v179
	v_fmac_f32_e32 v113, v114, v7
	v_and_b32_e32 v7, 0xffff0000, v179
	v_fmac_f32_e32 v7, v115, v112
	v_cvt_pk_bf16_f32 v119, v113, v7
	v_lshlrev_b32_e32 v7, 16, v172
	v_mul_f32_e32 v7, 0xbfb8aa3b, v7
	v_exp_f32_e32 v7, v7
	v_and_b32_e32 v114, 0xffff0000, v172
	v_mul_f32_e32 v114, 0xbfb8aa3b, v114
	v_exp_f32_e32 v114, v114
	v_add_f32_e32 v7, 1.0, v7
	v_rcp_f32_e32 v7, v7
	v_lshlrev_b32_e32 v115, 16, v168
	v_add_f32_e32 v114, 1.0, v114
	v_rcp_f32_e32 v114, v114
	v_fmac_f32_e32 v115, v108, v7
	v_lshlrev_b32_e32 v108, 16, v173
	v_and_b32_e32 v7, 0xffff0000, v168
	v_mul_f32_e32 v108, 0xbfb8aa3b, v108
	v_fmac_f32_e32 v7, v109, v114
	v_exp_f32_e32 v109, v108
	v_and_b32_e32 v108, 0xffff0000, v173
	v_mul_f32_e32 v108, 0xbfb8aa3b, v108
	v_lshlrev_b64 v[120:121], 12, v[192:193]
	v_exp_f32_e32 v114, v108
	v_lshl_add_u64 v[112:113], s[8:9], 0, v[120:121]
	v_lshl_add_u64 v[112:113], v[112:113], 0, v[4:5]
	global_store_dwordx4 v[112:113], v[116:119], off sc1
	v_cvt_pk_bf16_f32 v108, v115, v7
	v_add_f32_e32 v7, 1.0, v109
	v_rcp_f32_e32 v7, v7
	v_add_f32_e32 v109, 1.0, v114
	v_rcp_f32_e32 v109, v109
	v_lshlrev_b32_e32 v114, 16, v169
	v_fmac_f32_e32 v114, v110, v7
	v_and_b32_e32 v7, 0xffff0000, v169
	v_fmac_f32_e32 v7, v111, v109
	v_lshlrev_b32_e32 v109, 16, v174
	v_mul_f32_e32 v109, 0xbfb8aa3b, v109
	v_exp_f32_e32 v110, v109
	v_and_b32_e32 v109, 0xffff0000, v174
	v_mul_f32_e32 v109, 0xbfb8aa3b, v109
	v_exp_f32_e32 v111, v109
	v_cvt_pk_bf16_f32 v109, v114, v7
	v_add_f32_e32 v7, 1.0, v110
	v_rcp_f32_e32 v7, v7
	v_add_f32_e32 v110, 1.0, v111
	v_rcp_f32_e32 v110, v110
	v_lshlrev_b32_e32 v111, 16, v170
	v_fmac_f32_e32 v111, v104, v7
	v_and_b32_e32 v7, 0xffff0000, v170
	v_lshlrev_b32_e32 v104, 16, v175
	v_fmac_f32_e32 v7, v105, v110
	v_mul_f32_e32 v104, 0xbfb8aa3b, v104
	v_and_b32_e32 v105, 0xffff0000, v175
	v_exp_f32_e32 v104, v104
	v_mul_f32_e32 v105, 0xbfb8aa3b, v105
	v_exp_f32_e32 v105, v105
	v_cvt_pk_bf16_f32 v110, v111, v7
	v_add_f32_e32 v7, 1.0, v104
	v_rcp_f32_e32 v7, v7
	v_add_f32_e32 v104, 1.0, v105
	v_rcp_f32_e32 v104, v104
	v_lshlrev_b32_e32 v105, 16, v171
	v_fmac_f32_e32 v105, v106, v7
	v_and_b32_e32 v7, 0xffff0000, v171
	v_fmac_f32_e32 v7, v107, v104
	v_cvt_pk_bf16_f32 v111, v105, v7
	v_lshlrev_b32_e32 v7, 16, v164
	v_mul_f32_e32 v7, 0xbfb8aa3b, v7
	v_exp_f32_e32 v7, v7
	v_and_b32_e32 v104, 0xffff0000, v164
	v_mul_f32_e32 v104, 0xbfb8aa3b, v104
	v_exp_f32_e32 v106, v104
	v_add_f32_e32 v7, 1.0, v7
	v_rcp_f32_e32 v7, v7
	v_lshlrev_b32_e32 v107, 16, v160
	v_add_f32_e32 v106, 1.0, v106
	v_rcp_f32_e32 v106, v106
	v_fmac_f32_e32 v107, v100, v7
	v_lshlrev_b32_e32 v100, 16, v165
	v_and_b32_e32 v7, 0xffff0000, v160
	v_mul_f32_e32 v100, 0xbfb8aa3b, v100
	v_fmac_f32_e32 v7, v101, v106
	v_exp_f32_e32 v101, v100
	v_and_b32_e32 v100, 0xffff0000, v165
	v_mul_f32_e32 v100, 0xbfb8aa3b, v100
	v_exp_f32_e32 v106, v100
	global_store_dwordx4 v[112:113], v[108:111], off offset:256 sc1
	v_cvt_pk_bf16_f32 v100, v107, v7
	v_add_f32_e32 v7, 1.0, v101
	v_rcp_f32_e32 v7, v7
	v_add_f32_e32 v101, 1.0, v106
	v_rcp_f32_e32 v101, v101
	v_lshlrev_b32_e32 v106, 16, v161
	v_fmac_f32_e32 v106, v102, v7
	v_and_b32_e32 v7, 0xffff0000, v161
	v_fmac_f32_e32 v7, v103, v101
	v_lshlrev_b32_e32 v101, 16, v166
	v_mul_f32_e32 v101, 0xbfb8aa3b, v101
	v_exp_f32_e32 v102, v101
	v_and_b32_e32 v101, 0xffff0000, v166
	v_mul_f32_e32 v101, 0xbfb8aa3b, v101
	v_exp_f32_e32 v103, v101
	v_cvt_pk_bf16_f32 v101, v106, v7
	v_add_f32_e32 v7, 1.0, v102
	v_rcp_f32_e32 v7, v7
	v_add_f32_e32 v102, 1.0, v103
	v_rcp_f32_e32 v102, v102
	v_lshlrev_b32_e32 v103, 16, v162
	v_fmac_f32_e32 v103, v96, v7
	v_and_b32_e32 v7, 0xffff0000, v162
	v_lshlrev_b32_e32 v96, 16, v167
	v_fmac_f32_e32 v7, v97, v102
	v_mul_f32_e32 v96, 0xbfb8aa3b, v96
	v_and_b32_e32 v97, 0xffff0000, v167
	v_exp_f32_e32 v96, v96
	v_mul_f32_e32 v97, 0xbfb8aa3b, v97
	v_exp_f32_e32 v97, v97
	v_cvt_pk_bf16_f32 v102, v103, v7
	v_add_f32_e32 v7, 1.0, v96
	v_rcp_f32_e32 v7, v7
	v_add_f32_e32 v96, 1.0, v97
	v_rcp_f32_e32 v96, v96
	v_lshlrev_b32_e32 v97, 16, v163
	v_fmac_f32_e32 v97, v98, v7
	v_and_b32_e32 v7, 0xffff0000, v163
	v_fmac_f32_e32 v7, v99, v96
	v_cvt_pk_bf16_f32 v103, v97, v7
	v_lshlrev_b32_e32 v7, 16, v156
	v_mul_f32_e32 v7, 0xbfb8aa3b, v7
	v_exp_f32_e32 v7, v7
	v_and_b32_e32 v98, 0xffff0000, v156
	v_mul_f32_e32 v98, 0xbfb8aa3b, v98
	v_exp_f32_e32 v98, v98
	v_add_f32_e32 v7, 1.0, v7
	v_rcp_f32_e32 v7, v7
	v_lshlrev_b32_e32 v99, 16, v152
	v_add_f32_e32 v98, 1.0, v98
	v_rcp_f32_e32 v98, v98
	v_fmac_f32_e32 v99, v92, v7
	v_lshlrev_b32_e32 v92, 16, v157
	v_and_b32_e32 v7, 0xffff0000, v152
	v_mul_f32_e32 v92, 0xbfb8aa3b, v92
	v_fmac_f32_e32 v7, v93, v98
	v_exp_f32_e32 v93, v92
	v_and_b32_e32 v92, 0xffff0000, v157
	v_mul_f32_e32 v92, 0xbfb8aa3b, v92
	v_lshlrev_b64 v[104:105], 12, v[190:191]
	v_exp_f32_e32 v98, v92
	v_lshl_add_u64 v[96:97], s[8:9], 0, v[104:105]
	v_lshl_add_u64 v[96:97], v[96:97], 0, v[4:5]
	global_store_dwordx4 v[96:97], v[100:103], off sc1
	v_cvt_pk_bf16_f32 v92, v99, v7
	v_add_f32_e32 v7, 1.0, v93
	v_rcp_f32_e32 v7, v7
	v_add_f32_e32 v93, 1.0, v98
	v_rcp_f32_e32 v93, v93
	v_lshlrev_b32_e32 v98, 16, v153
	v_fmac_f32_e32 v98, v94, v7
	v_and_b32_e32 v7, 0xffff0000, v153
	v_fmac_f32_e32 v7, v95, v93
	v_lshlrev_b32_e32 v93, 16, v158
	v_mul_f32_e32 v93, 0xbfb8aa3b, v93
	v_exp_f32_e32 v94, v93
	v_and_b32_e32 v93, 0xffff0000, v158
	v_mul_f32_e32 v93, 0xbfb8aa3b, v93
	v_exp_f32_e32 v95, v93
	v_cvt_pk_bf16_f32 v93, v98, v7
	v_add_f32_e32 v7, 1.0, v94
	v_rcp_f32_e32 v7, v7
	v_add_f32_e32 v94, 1.0, v95
	v_rcp_f32_e32 v94, v94
	v_lshlrev_b32_e32 v95, 16, v154
	v_fmac_f32_e32 v95, v88, v7
	v_and_b32_e32 v7, 0xffff0000, v154
	v_lshlrev_b32_e32 v88, 16, v159
	v_fmac_f32_e32 v7, v89, v94
	v_mul_f32_e32 v88, 0xbfb8aa3b, v88
	v_and_b32_e32 v89, 0xffff0000, v159
	v_exp_f32_e32 v88, v88
	v_mul_f32_e32 v89, 0xbfb8aa3b, v89
	v_exp_f32_e32 v89, v89
	v_cvt_pk_bf16_f32 v94, v95, v7
	v_add_f32_e32 v7, 1.0, v88
	v_rcp_f32_e32 v7, v7
	v_add_f32_e32 v88, 1.0, v89
	v_rcp_f32_e32 v88, v88
	v_lshlrev_b32_e32 v89, 16, v155
	v_fmac_f32_e32 v89, v90, v7
	v_and_b32_e32 v7, 0xffff0000, v155
	v_fmac_f32_e32 v7, v91, v88
	v_cvt_pk_bf16_f32 v95, v89, v7
	v_lshlrev_b32_e32 v7, 16, v148
	v_mul_f32_e32 v7, 0xbfb8aa3b, v7
	v_exp_f32_e32 v7, v7
	v_and_b32_e32 v88, 0xffff0000, v148
	v_mul_f32_e32 v88, 0xbfb8aa3b, v88
	v_exp_f32_e32 v90, v88
	v_add_f32_e32 v7, 1.0, v7
	v_rcp_f32_e32 v7, v7
	v_lshlrev_b32_e32 v91, 16, v144
	v_add_f32_e32 v90, 1.0, v90
	v_rcp_f32_e32 v90, v90
	v_fmac_f32_e32 v91, v84, v7
	v_lshlrev_b32_e32 v84, 16, v149
	v_and_b32_e32 v7, 0xffff0000, v144
	v_mul_f32_e32 v84, 0xbfb8aa3b, v84
	v_fmac_f32_e32 v7, v85, v90
	v_exp_f32_e32 v85, v84
	v_and_b32_e32 v84, 0xffff0000, v149
	v_mul_f32_e32 v84, 0xbfb8aa3b, v84
	v_exp_f32_e32 v90, v84
	global_store_dwordx4 v[96:97], v[92:95], off offset:256 sc1
	v_cvt_pk_bf16_f32 v84, v91, v7
	v_add_f32_e32 v7, 1.0, v85
	v_rcp_f32_e32 v7, v7
	v_add_f32_e32 v85, 1.0, v90
	v_rcp_f32_e32 v85, v85
	v_lshlrev_b32_e32 v90, 16, v145
	v_fmac_f32_e32 v90, v86, v7
	v_and_b32_e32 v7, 0xffff0000, v145
	v_fmac_f32_e32 v7, v87, v85
	v_lshlrev_b32_e32 v85, 16, v150
	v_mul_f32_e32 v85, 0xbfb8aa3b, v85
	v_exp_f32_e32 v86, v85
	v_and_b32_e32 v85, 0xffff0000, v150
	v_mul_f32_e32 v85, 0xbfb8aa3b, v85
	v_exp_f32_e32 v87, v85
	v_cvt_pk_bf16_f32 v85, v90, v7
	v_add_f32_e32 v7, 1.0, v86
	v_rcp_f32_e32 v7, v7
	v_add_f32_e32 v86, 1.0, v87
	v_rcp_f32_e32 v86, v86
	v_lshlrev_b32_e32 v87, 16, v146
	v_fmac_f32_e32 v87, v80, v7
	v_and_b32_e32 v7, 0xffff0000, v146
	v_lshlrev_b32_e32 v80, 16, v151
	v_fmac_f32_e32 v7, v81, v86
	v_mul_f32_e32 v80, 0xbfb8aa3b, v80
	v_and_b32_e32 v81, 0xffff0000, v151
	v_exp_f32_e32 v80, v80
	v_mul_f32_e32 v81, 0xbfb8aa3b, v81
	v_exp_f32_e32 v81, v81
	v_cvt_pk_bf16_f32 v86, v87, v7
	v_add_f32_e32 v7, 1.0, v80
	v_rcp_f32_e32 v7, v7
	v_add_f32_e32 v80, 1.0, v81
	v_rcp_f32_e32 v80, v80
	v_lshlrev_b32_e32 v81, 16, v147
	v_fmac_f32_e32 v81, v82, v7
	v_and_b32_e32 v7, 0xffff0000, v147
	v_fmac_f32_e32 v7, v83, v80
	v_cvt_pk_bf16_f32 v87, v81, v7
	v_lshlrev_b32_e32 v7, 16, v140
	v_mul_f32_e32 v7, 0xbfb8aa3b, v7
	v_exp_f32_e32 v7, v7
	v_and_b32_e32 v82, 0xffff0000, v140
	v_mul_f32_e32 v82, 0xbfb8aa3b, v82
	v_exp_f32_e32 v82, v82
	v_add_f32_e32 v7, 1.0, v7
	v_rcp_f32_e32 v7, v7
	v_lshlrev_b32_e32 v83, 16, v136
	v_add_f32_e32 v82, 1.0, v82
	v_rcp_f32_e32 v82, v82
	v_fmac_f32_e32 v83, v76, v7
	v_lshlrev_b32_e32 v76, 16, v141
	v_and_b32_e32 v7, 0xffff0000, v136
	v_mul_f32_e32 v76, 0xbfb8aa3b, v76
	v_fmac_f32_e32 v7, v77, v82
	v_exp_f32_e32 v77, v76
	v_and_b32_e32 v76, 0xffff0000, v141
	v_mul_f32_e32 v76, 0xbfb8aa3b, v76
	v_lshlrev_b64 v[88:89], 12, v[188:189]
	v_exp_f32_e32 v82, v76
	v_lshl_add_u64 v[80:81], s[8:9], 0, v[88:89]
	v_lshl_add_u64 v[80:81], v[80:81], 0, v[4:5]
	global_store_dwordx4 v[80:81], v[84:87], off sc1
	v_cvt_pk_bf16_f32 v76, v83, v7
	v_add_f32_e32 v7, 1.0, v77
	v_rcp_f32_e32 v7, v7
	v_add_f32_e32 v77, 1.0, v82
	v_rcp_f32_e32 v77, v77
	v_lshlrev_b32_e32 v82, 16, v137
	v_fmac_f32_e32 v82, v78, v7
	v_and_b32_e32 v7, 0xffff0000, v137
	v_fmac_f32_e32 v7, v79, v77
	v_lshlrev_b32_e32 v77, 16, v142
	v_mul_f32_e32 v77, 0xbfb8aa3b, v77
	v_exp_f32_e32 v78, v77
	v_and_b32_e32 v77, 0xffff0000, v142
	v_mul_f32_e32 v77, 0xbfb8aa3b, v77
	v_exp_f32_e32 v79, v77
	v_cvt_pk_bf16_f32 v77, v82, v7
	v_add_f32_e32 v7, 1.0, v78
	v_rcp_f32_e32 v7, v7
	v_add_f32_e32 v78, 1.0, v79
	v_rcp_f32_e32 v78, v78
	v_lshlrev_b32_e32 v79, 16, v138
	v_fmac_f32_e32 v79, v72, v7
	v_and_b32_e32 v7, 0xffff0000, v138
	v_lshlrev_b32_e32 v72, 16, v143
	v_fmac_f32_e32 v7, v73, v78
	v_mul_f32_e32 v72, 0xbfb8aa3b, v72
	v_and_b32_e32 v73, 0xffff0000, v143
	v_exp_f32_e32 v72, v72
	v_mul_f32_e32 v73, 0xbfb8aa3b, v73
	v_exp_f32_e32 v73, v73
	v_cvt_pk_bf16_f32 v78, v79, v7
	v_add_f32_e32 v7, 1.0, v72
	v_rcp_f32_e32 v7, v7
	v_add_f32_e32 v72, 1.0, v73
	v_rcp_f32_e32 v72, v72
	v_lshlrev_b32_e32 v73, 16, v139
	v_add_u32_e32 v142, 0x80, v186
	v_fmac_f32_e32 v73, v74, v7
	v_and_b32_e32 v7, 0xffff0000, v139
	v_ashrrev_i32_e32 v143, 31, v142
	v_fmac_f32_e32 v7, v75, v72
	v_cvt_pk_bf16_f32 v79, v73, v7
	v_lshlrev_b64 v[72:73], 11, v[142:143]
	v_lshl_add_u64 v[72:73], v[72:73], 0, v[184:185]
	v_lshlrev_b64 v[72:73], 1, v[72:73]
	global_store_dwordx4 v[80:81], v[76:79], off offset:256 sc1
	v_lshl_add_u64 v[74:75], s[10:11], 0, v[72:73]
	global_load_dwordx4 v[126:129], v[74:75], off
	v_lshl_add_u64 v[74:75], s[8:9], 0, v[72:73]
	global_load_dwordx4 v[130:133], v[74:75], off
	v_or_b32_e32 v72, 0x100, v72
	v_lshl_add_u64 v[74:75], s[10:11], 0, v[72:73]
	v_lshl_add_u64 v[72:73], s[8:9], 0, v[72:73]
	global_load_dwordx4 v[134:137], v[74:75], off
	global_load_dwordx4 v[138:141], v[72:73], off
	v_add_u32_e32 v124, 0x90, v186
	v_ashrrev_i32_e32 v125, 31, v124
	v_lshlrev_b64 v[72:73], 11, v[124:125]
	v_lshl_add_u64 v[72:73], v[72:73], 0, v[184:185]
	v_lshlrev_b64 v[72:73], 1, v[72:73]
	v_lshl_add_u64 v[74:75], s[10:11], 0, v[72:73]
	v_lshl_add_u64 v[76:77], s[8:9], 0, v[72:73]
	v_or_b32_e32 v72, 0x100, v72
	v_add_u32_e32 v122, 0xa0, v186
	global_load_dwordx4 v[116:119], v[74:75], off
	global_load_dwordx4 v[112:115], v[76:77], off
	v_lshl_add_u64 v[74:75], s[10:11], 0, v[72:73]
	v_lshl_add_u64 v[72:73], s[8:9], 0, v[72:73]
	v_ashrrev_i32_e32 v123, 31, v122
	global_load_dwordx4 v[108:111], v[74:75], off
	global_load_dwordx4 v[104:107], v[72:73], off
	v_lshlrev_b64 v[72:73], 11, v[122:123]
	v_lshl_add_u64 v[72:73], v[72:73], 0, v[184:185]
	v_lshlrev_b64 v[72:73], 1, v[72:73]
	v_lshl_add_u64 v[74:75], s[10:11], 0, v[72:73]
	v_lshl_add_u64 v[76:77], s[8:9], 0, v[72:73]
	v_or_b32_e32 v72, 0x100, v72
	v_add_u32_e32 v120, 0xb0, v186
	global_load_dwordx4 v[100:103], v[74:75], off
	global_load_dwordx4 v[96:99], v[76:77], off
	v_lshl_add_u64 v[74:75], s[10:11], 0, v[72:73]
	v_lshl_add_u64 v[72:73], s[8:9], 0, v[72:73]
	v_ashrrev_i32_e32 v121, 31, v120
	global_load_dwordx4 v[92:95], v[74:75], off
	global_load_dwordx4 v[88:91], v[72:73], off
	v_lshlrev_b64 v[72:73], 11, v[120:121]
	v_lshl_add_u64 v[72:73], v[72:73], 0, v[184:185]
	v_lshlrev_b64 v[72:73], 1, v[72:73]
	v_lshl_add_u64 v[74:75], s[10:11], 0, v[72:73]
	v_lshl_add_u64 v[76:77], s[8:9], 0, v[72:73]
	v_or_b32_e32 v72, 0x100, v72
	global_load_dwordx4 v[84:87], v[74:75], off
	global_load_dwordx4 v[80:83], v[76:77], off
	v_lshl_add_u64 v[74:75], s[10:11], 0, v[72:73]
	v_lshl_add_u64 v[72:73], s[8:9], 0, v[72:73]
	global_load_dwordx4 v[76:79], v[74:75], off
	s_nop 0
	global_load_dwordx4 v[72:75], v[72:73], off
	v_lshlrev_b64 v[142:143], 12, v[142:143]
	s_waitcnt vmcnt(15)
	v_lshlrev_b32_e32 v7, 16, v126
	v_mul_f32_e32 v7, 0xbfb8aa3b, v7
	v_exp_f32_e32 v7, v7
	v_and_b32_e32 v126, 0xffff0000, v126
	v_mul_f32_e32 v126, 0xbfb8aa3b, v126
	v_exp_f32_e32 v126, v126
	v_add_f32_e32 v7, 1.0, v7
	v_rcp_f32_e32 v7, v7
	s_waitcnt vmcnt(14)
	v_lshlrev_b32_e32 v144, 16, v130
	v_add_f32_e32 v126, 1.0, v126
	v_rcp_f32_e32 v126, v126
	v_fmac_f32_e32 v144, v68, v7
	v_lshlrev_b32_e32 v68, 16, v127
	v_and_b32_e32 v7, 0xffff0000, v130
	v_mul_f32_e32 v68, 0xbfb8aa3b, v68
	v_fmac_f32_e32 v7, v69, v126
	v_exp_f32_e32 v69, v68
	v_and_b32_e32 v68, 0xffff0000, v127
	v_mul_f32_e32 v68, 0xbfb8aa3b, v68
	v_exp_f32_e32 v126, v68
	v_cvt_pk_bf16_f32 v68, v144, v7
	v_add_f32_e32 v7, 1.0, v69
	v_rcp_f32_e32 v7, v7
	v_add_f32_e32 v69, 1.0, v126
	v_rcp_f32_e32 v69, v69
	v_lshlrev_b32_e32 v126, 16, v131
	v_fmac_f32_e32 v126, v70, v7
	v_and_b32_e32 v7, 0xffff0000, v131
	v_fmac_f32_e32 v7, v71, v69
	v_lshlrev_b32_e32 v69, 16, v128
	v_mul_f32_e32 v69, 0xbfb8aa3b, v69
	v_exp_f32_e32 v70, v69
	v_and_b32_e32 v69, 0xffff0000, v128
	v_mul_f32_e32 v69, 0xbfb8aa3b, v69
	v_exp_f32_e32 v71, v69
	v_cvt_pk_bf16_f32 v69, v126, v7
	v_add_f32_e32 v7, 1.0, v70
	v_rcp_f32_e32 v7, v7
	v_add_f32_e32 v70, 1.0, v71
	v_rcp_f32_e32 v70, v70
	v_lshlrev_b32_e32 v71, 16, v132
	v_fmac_f32_e32 v71, v64, v7
	v_and_b32_e32 v7, 0xffff0000, v132
	v_lshlrev_b32_e32 v64, 16, v129
	v_fmac_f32_e32 v7, v65, v70
	v_mul_f32_e32 v64, 0xbfb8aa3b, v64
	v_and_b32_e32 v65, 0xffff0000, v129
	v_exp_f32_e32 v64, v64
	v_mul_f32_e32 v65, 0xbfb8aa3b, v65
	v_exp_f32_e32 v65, v65
	v_cvt_pk_bf16_f32 v70, v71, v7
	v_add_f32_e32 v7, 1.0, v64
	v_rcp_f32_e32 v7, v7
	v_add_f32_e32 v64, 1.0, v65
	v_rcp_f32_e32 v64, v64
	v_lshlrev_b32_e32 v65, 16, v133
	v_fmac_f32_e32 v65, v66, v7
	v_and_b32_e32 v7, 0xffff0000, v133
	v_fmac_f32_e32 v7, v67, v64
	v_cvt_pk_bf16_f32 v71, v65, v7
	s_waitcnt vmcnt(13)
	v_lshlrev_b32_e32 v7, 16, v134
	v_mul_f32_e32 v7, 0xbfb8aa3b, v7
	v_exp_f32_e32 v7, v7
	v_and_b32_e32 v66, 0xffff0000, v134
	v_mul_f32_e32 v66, 0xbfb8aa3b, v66
	v_exp_f32_e32 v66, v66
	v_add_f32_e32 v7, 1.0, v7
	v_rcp_f32_e32 v7, v7
	s_waitcnt vmcnt(12)
	v_lshlrev_b32_e32 v67, 16, v138
	v_add_f32_e32 v66, 1.0, v66
	v_rcp_f32_e32 v66, v66
	v_fmac_f32_e32 v67, v60, v7
	v_lshlrev_b32_e32 v60, 16, v135
	v_and_b32_e32 v7, 0xffff0000, v138
	v_mul_f32_e32 v60, 0xbfb8aa3b, v60
	v_fmac_f32_e32 v7, v61, v66
	v_exp_f32_e32 v61, v60
	v_and_b32_e32 v60, 0xffff0000, v135
	v_mul_f32_e32 v60, 0xbfb8aa3b, v60
	v_exp_f32_e32 v66, v60
	v_lshl_add_u64 v[64:65], s[8:9], 0, v[142:143]
	v_lshl_add_u64 v[64:65], v[64:65], 0, v[4:5]
	global_store_dwordx4 v[64:65], v[68:71], off sc1
	v_cvt_pk_bf16_f32 v60, v67, v7
	v_add_f32_e32 v7, 1.0, v61
	v_rcp_f32_e32 v7, v7
	v_add_f32_e32 v61, 1.0, v66
	v_rcp_f32_e32 v61, v61
	v_lshlrev_b32_e32 v66, 16, v139
	v_fmac_f32_e32 v66, v62, v7
	v_and_b32_e32 v7, 0xffff0000, v139
	v_fmac_f32_e32 v7, v63, v61
	v_lshlrev_b32_e32 v61, 16, v136
	v_mul_f32_e32 v61, 0xbfb8aa3b, v61
	v_exp_f32_e32 v62, v61
	v_and_b32_e32 v61, 0xffff0000, v136
	v_mul_f32_e32 v61, 0xbfb8aa3b, v61
	v_exp_f32_e32 v63, v61
	v_cvt_pk_bf16_f32 v61, v66, v7
	v_add_f32_e32 v7, 1.0, v62
	v_rcp_f32_e32 v7, v7
	v_add_f32_e32 v62, 1.0, v63
	v_rcp_f32_e32 v62, v62
	v_lshlrev_b32_e32 v63, 16, v140
	v_fmac_f32_e32 v63, v56, v7
	v_and_b32_e32 v7, 0xffff0000, v140
	v_lshlrev_b32_e32 v56, 16, v137
	v_fmac_f32_e32 v7, v57, v62
	v_mul_f32_e32 v56, 0xbfb8aa3b, v56
	v_and_b32_e32 v57, 0xffff0000, v137
	v_exp_f32_e32 v56, v56
	v_mul_f32_e32 v57, 0xbfb8aa3b, v57
	v_exp_f32_e32 v57, v57
	v_cvt_pk_bf16_f32 v62, v63, v7
	v_add_f32_e32 v7, 1.0, v56
	v_rcp_f32_e32 v7, v7
	v_add_f32_e32 v56, 1.0, v57
	v_rcp_f32_e32 v56, v56
	v_lshlrev_b32_e32 v57, 16, v141
	v_fmac_f32_e32 v57, v58, v7
	v_and_b32_e32 v7, 0xffff0000, v141
	v_fmac_f32_e32 v7, v59, v56
	v_cvt_pk_bf16_f32 v63, v57, v7
	s_waitcnt vmcnt(12)
	v_lshlrev_b32_e32 v7, 16, v116
	v_mul_f32_e32 v7, 0xbfb8aa3b, v7
	v_exp_f32_e32 v7, v7
	v_and_b32_e32 v56, 0xffff0000, v116
	v_mul_f32_e32 v56, 0xbfb8aa3b, v56
	v_exp_f32_e32 v58, v56
	v_add_f32_e32 v7, 1.0, v7
	v_rcp_f32_e32 v7, v7
	s_waitcnt vmcnt(11)
	v_lshlrev_b32_e32 v59, 16, v112
	v_add_f32_e32 v58, 1.0, v58
	v_rcp_f32_e32 v58, v58
	v_fmac_f32_e32 v59, v52, v7
	v_lshlrev_b32_e32 v52, 16, v117
	v_and_b32_e32 v7, 0xffff0000, v112
	v_mul_f32_e32 v52, 0xbfb8aa3b, v52
	v_fmac_f32_e32 v7, v53, v58
	v_exp_f32_e32 v53, v52
	v_and_b32_e32 v52, 0xffff0000, v117
	v_mul_f32_e32 v52, 0xbfb8aa3b, v52
	v_exp_f32_e32 v58, v52
	global_store_dwordx4 v[64:65], v[60:63], off offset:256 sc1
	v_cvt_pk_bf16_f32 v52, v59, v7
	v_add_f32_e32 v7, 1.0, v53
	v_rcp_f32_e32 v7, v7
	v_add_f32_e32 v53, 1.0, v58
	v_rcp_f32_e32 v53, v53
	v_lshlrev_b32_e32 v58, 16, v113
	v_fmac_f32_e32 v58, v54, v7
	v_and_b32_e32 v7, 0xffff0000, v113
	v_fmac_f32_e32 v7, v55, v53
	v_lshlrev_b32_e32 v53, 16, v118
	v_mul_f32_e32 v53, 0xbfb8aa3b, v53
	v_exp_f32_e32 v54, v53
	v_and_b32_e32 v53, 0xffff0000, v118
	v_mul_f32_e32 v53, 0xbfb8aa3b, v53
	v_exp_f32_e32 v55, v53
	v_cvt_pk_bf16_f32 v53, v58, v7
	v_add_f32_e32 v7, 1.0, v54
	v_rcp_f32_e32 v7, v7
	v_add_f32_e32 v54, 1.0, v55
	v_rcp_f32_e32 v54, v54
	v_lshlrev_b32_e32 v55, 16, v114
	v_fmac_f32_e32 v55, v48, v7
	v_and_b32_e32 v7, 0xffff0000, v114
	v_lshlrev_b32_e32 v48, 16, v119
	v_fmac_f32_e32 v7, v49, v54
	v_mul_f32_e32 v48, 0xbfb8aa3b, v48
	v_and_b32_e32 v49, 0xffff0000, v119
	v_exp_f32_e32 v48, v48
	v_mul_f32_e32 v49, 0xbfb8aa3b, v49
	v_exp_f32_e32 v49, v49
	v_cvt_pk_bf16_f32 v54, v55, v7
	v_add_f32_e32 v7, 1.0, v48
	v_rcp_f32_e32 v7, v7
	v_add_f32_e32 v48, 1.0, v49
	v_rcp_f32_e32 v48, v48
	v_lshlrev_b32_e32 v49, 16, v115
	v_fmac_f32_e32 v49, v50, v7
	v_and_b32_e32 v7, 0xffff0000, v115
	v_fmac_f32_e32 v7, v51, v48
	v_cvt_pk_bf16_f32 v55, v49, v7
	s_waitcnt vmcnt(11)
	v_lshlrev_b32_e32 v7, 16, v108
	v_mul_f32_e32 v7, 0xbfb8aa3b, v7
	v_exp_f32_e32 v7, v7
	v_and_b32_e32 v50, 0xffff0000, v108
	v_mul_f32_e32 v50, 0xbfb8aa3b, v50
	v_exp_f32_e32 v50, v50
	v_add_f32_e32 v7, 1.0, v7
	v_rcp_f32_e32 v7, v7
	s_waitcnt vmcnt(10)
	v_lshlrev_b32_e32 v51, 16, v104
	v_add_f32_e32 v50, 1.0, v50
	v_rcp_f32_e32 v50, v50
	v_fmac_f32_e32 v51, v44, v7
	v_lshlrev_b32_e32 v44, 16, v109
	v_and_b32_e32 v7, 0xffff0000, v104
	v_mul_f32_e32 v44, 0xbfb8aa3b, v44
	v_fmac_f32_e32 v7, v45, v50
	v_exp_f32_e32 v45, v44
	v_and_b32_e32 v44, 0xffff0000, v109
	v_mul_f32_e32 v44, 0xbfb8aa3b, v44
	v_lshlrev_b64 v[56:57], 12, v[124:125]
	v_exp_f32_e32 v50, v44
	v_lshl_add_u64 v[48:49], s[8:9], 0, v[56:57]
	v_lshl_add_u64 v[48:49], v[48:49], 0, v[4:5]
	global_store_dwordx4 v[48:49], v[52:55], off sc1
	v_cvt_pk_bf16_f32 v44, v51, v7
	v_add_f32_e32 v7, 1.0, v45
	v_rcp_f32_e32 v7, v7
	v_add_f32_e32 v45, 1.0, v50
	v_rcp_f32_e32 v45, v45
	v_lshlrev_b32_e32 v50, 16, v105
	v_fmac_f32_e32 v50, v46, v7
	v_and_b32_e32 v7, 0xffff0000, v105
	v_fmac_f32_e32 v7, v47, v45
	v_lshlrev_b32_e32 v45, 16, v110
	v_mul_f32_e32 v45, 0xbfb8aa3b, v45
	v_exp_f32_e32 v46, v45
	v_and_b32_e32 v45, 0xffff0000, v110
	v_mul_f32_e32 v45, 0xbfb8aa3b, v45
	v_exp_f32_e32 v47, v45
	v_cvt_pk_bf16_f32 v45, v50, v7
	v_add_f32_e32 v7, 1.0, v46
	v_rcp_f32_e32 v7, v7
	v_add_f32_e32 v46, 1.0, v47
	v_rcp_f32_e32 v46, v46
	v_lshlrev_b32_e32 v47, 16, v106
	v_fmac_f32_e32 v47, v40, v7
	v_and_b32_e32 v7, 0xffff0000, v106
	v_lshlrev_b32_e32 v40, 16, v111
	v_fmac_f32_e32 v7, v41, v46
	v_mul_f32_e32 v40, 0xbfb8aa3b, v40
	v_and_b32_e32 v41, 0xffff0000, v111
	v_exp_f32_e32 v40, v40
	v_mul_f32_e32 v41, 0xbfb8aa3b, v41
	v_exp_f32_e32 v41, v41
	v_cvt_pk_bf16_f32 v46, v47, v7
	v_add_f32_e32 v7, 1.0, v40
	v_rcp_f32_e32 v7, v7
	v_add_f32_e32 v40, 1.0, v41
	v_rcp_f32_e32 v40, v40
	v_lshlrev_b32_e32 v41, 16, v107
	v_fmac_f32_e32 v41, v42, v7
	v_and_b32_e32 v7, 0xffff0000, v107
	v_fmac_f32_e32 v7, v43, v40
	v_cvt_pk_bf16_f32 v47, v41, v7
	s_waitcnt vmcnt(10)
	v_lshlrev_b32_e32 v7, 16, v100
	v_mul_f32_e32 v7, 0xbfb8aa3b, v7
	v_exp_f32_e32 v7, v7
	v_and_b32_e32 v40, 0xffff0000, v100
	v_mul_f32_e32 v40, 0xbfb8aa3b, v40
	v_exp_f32_e32 v42, v40
	v_add_f32_e32 v7, 1.0, v7
	v_rcp_f32_e32 v7, v7
	s_waitcnt vmcnt(9)
	v_lshlrev_b32_e32 v43, 16, v96
	v_add_f32_e32 v42, 1.0, v42
	v_rcp_f32_e32 v42, v42
	v_fmac_f32_e32 v43, v36, v7
	v_lshlrev_b32_e32 v36, 16, v101
	v_and_b32_e32 v7, 0xffff0000, v96
	v_mul_f32_e32 v36, 0xbfb8aa3b, v36
	v_fmac_f32_e32 v7, v37, v42
	v_exp_f32_e32 v37, v36
	v_and_b32_e32 v36, 0xffff0000, v101
	v_mul_f32_e32 v36, 0xbfb8aa3b, v36
	v_exp_f32_e32 v42, v36
	global_store_dwordx4 v[48:49], v[44:47], off offset:256 sc1
	v_cvt_pk_bf16_f32 v36, v43, v7
	v_add_f32_e32 v7, 1.0, v37
	v_rcp_f32_e32 v7, v7
	v_add_f32_e32 v37, 1.0, v42
	v_rcp_f32_e32 v37, v37
	v_lshlrev_b32_e32 v42, 16, v97
	v_fmac_f32_e32 v42, v38, v7
	v_and_b32_e32 v7, 0xffff0000, v97
	v_fmac_f32_e32 v7, v39, v37
	v_lshlrev_b32_e32 v37, 16, v102
	v_mul_f32_e32 v37, 0xbfb8aa3b, v37
	v_exp_f32_e32 v38, v37
	v_and_b32_e32 v37, 0xffff0000, v102
	v_mul_f32_e32 v37, 0xbfb8aa3b, v37
	v_exp_f32_e32 v39, v37
	v_cvt_pk_bf16_f32 v37, v42, v7
	v_add_f32_e32 v7, 1.0, v38
	v_rcp_f32_e32 v7, v7
	v_add_f32_e32 v38, 1.0, v39
	v_rcp_f32_e32 v38, v38
	v_lshlrev_b32_e32 v39, 16, v98
	v_fmac_f32_e32 v39, v28, v7
	v_and_b32_e32 v7, 0xffff0000, v98
	v_lshlrev_b32_e32 v28, 16, v103
	v_fmac_f32_e32 v7, v29, v38
	v_mul_f32_e32 v28, 0xbfb8aa3b, v28
	v_and_b32_e32 v29, 0xffff0000, v103
	v_exp_f32_e32 v28, v28
	v_mul_f32_e32 v29, 0xbfb8aa3b, v29
	v_exp_f32_e32 v29, v29
	v_cvt_pk_bf16_f32 v38, v39, v7
	v_add_f32_e32 v7, 1.0, v28
	v_rcp_f32_e32 v7, v7
	v_add_f32_e32 v28, 1.0, v29
	v_rcp_f32_e32 v28, v28
	v_lshlrev_b32_e32 v29, 16, v99
	v_fmac_f32_e32 v29, v30, v7
	v_and_b32_e32 v7, 0xffff0000, v99
	v_lshlrev_b64 v[40:41], 12, v[122:123]
	v_fmac_f32_e32 v7, v31, v28
	v_cvt_pk_bf16_f32 v39, v29, v7
	v_lshl_add_u64 v[28:29], s[8:9], 0, v[40:41]
	s_waitcnt vmcnt(9)
	v_lshlrev_b32_e32 v7, 16, v92
	v_lshl_add_u64 v[40:41], v[28:29], 0, v[4:5]
	v_mul_f32_e32 v7, 0xbfb8aa3b, v7
	v_and_b32_e32 v28, 0xffff0000, v92
	v_exp_f32_e32 v7, v7
	v_mul_f32_e32 v28, 0xbfb8aa3b, v28
	v_exp_f32_e32 v28, v28
	s_waitcnt vmcnt(8)
	v_lshlrev_b32_e32 v29, 16, v88
	v_add_f32_e32 v7, 1.0, v7
	v_rcp_f32_e32 v7, v7
	v_add_f32_e32 v28, 1.0, v28
	v_rcp_f32_e32 v28, v28
	global_store_dwordx4 v[40:41], v[36:39], off sc1
	v_fmac_f32_e32 v29, v32, v7
	v_and_b32_e32 v7, 0xffff0000, v88
	v_fmac_f32_e32 v7, v33, v28
	v_lshlrev_b32_e32 v28, 16, v93
	v_mul_f32_e32 v28, 0xbfb8aa3b, v28
	v_exp_f32_e32 v30, v28
	v_and_b32_e32 v28, 0xffff0000, v93
	v_mul_f32_e32 v28, 0xbfb8aa3b, v28
	v_exp_f32_e32 v31, v28
	v_cvt_pk_bf16_f32 v28, v29, v7
	v_add_f32_e32 v7, 1.0, v30
	v_rcp_f32_e32 v7, v7
	v_add_f32_e32 v29, 1.0, v31
	v_rcp_f32_e32 v29, v29
	v_lshlrev_b32_e32 v30, 16, v89
	v_fmac_f32_e32 v30, v34, v7
	v_and_b32_e32 v7, 0xffff0000, v89
	v_fmac_f32_e32 v7, v35, v29
	v_lshlrev_b32_e32 v29, 16, v94
	v_mul_f32_e32 v29, 0xbfb8aa3b, v29
	v_exp_f32_e32 v31, v29
	v_and_b32_e32 v29, 0xffff0000, v94
	v_mul_f32_e32 v29, 0xbfb8aa3b, v29
	v_exp_f32_e32 v32, v29
	v_cvt_pk_bf16_f32 v29, v30, v7
	v_add_f32_e32 v7, 1.0, v31
	v_rcp_f32_e32 v7, v7
	v_add_f32_e32 v30, 1.0, v32
	v_rcp_f32_e32 v30, v30
	v_lshlrev_b32_e32 v31, 16, v90
	v_fmac_f32_e32 v31, v24, v7
	v_and_b32_e32 v7, 0xffff0000, v90
	v_lshlrev_b32_e32 v24, 16, v95
	v_fmac_f32_e32 v7, v25, v30
	v_mul_f32_e32 v24, 0xbfb8aa3b, v24
	v_and_b32_e32 v25, 0xffff0000, v95
	v_exp_f32_e32 v24, v24
	v_mul_f32_e32 v25, 0xbfb8aa3b, v25
	v_exp_f32_e32 v25, v25
	v_cvt_pk_bf16_f32 v30, v31, v7
	v_add_f32_e32 v7, 1.0, v24
	v_rcp_f32_e32 v7, v7
	v_add_f32_e32 v24, 1.0, v25
	v_rcp_f32_e32 v24, v24
	v_lshlrev_b32_e32 v25, 16, v91
	v_fmac_f32_e32 v25, v26, v7
	v_and_b32_e32 v7, 0xffff0000, v91
	v_fmac_f32_e32 v7, v27, v24
	v_cvt_pk_bf16_f32 v31, v25, v7
	s_waitcnt vmcnt(8)
	v_lshlrev_b32_e32 v7, 16, v84
	v_mul_f32_e32 v7, 0xbfb8aa3b, v7
	v_exp_f32_e32 v7, v7
	v_and_b32_e32 v24, 0xffff0000, v84
	v_mul_f32_e32 v24, 0xbfb8aa3b, v24
	v_exp_f32_e32 v26, v24
	v_add_f32_e32 v7, 1.0, v7
	v_rcp_f32_e32 v7, v7
	s_waitcnt vmcnt(7)
	v_lshlrev_b32_e32 v27, 16, v80
	v_add_f32_e32 v26, 1.0, v26
	v_rcp_f32_e32 v26, v26
	v_fmac_f32_e32 v27, v16, v7
	v_lshlrev_b32_e32 v16, 16, v85
	v_and_b32_e32 v7, 0xffff0000, v80
	v_mul_f32_e32 v16, 0xbfb8aa3b, v16
	v_fmac_f32_e32 v7, v17, v26
	v_exp_f32_e32 v17, v16
	v_and_b32_e32 v16, 0xffff0000, v85
	v_mul_f32_e32 v16, 0xbfb8aa3b, v16
	v_exp_f32_e32 v26, v16
	global_store_dwordx4 v[40:41], v[28:31], off offset:256 sc1
	v_cvt_pk_bf16_f32 v16, v27, v7
	v_add_f32_e32 v7, 1.0, v17
	v_rcp_f32_e32 v7, v7
	v_add_f32_e32 v17, 1.0, v26
	v_rcp_f32_e32 v17, v17
	v_lshlrev_b32_e32 v26, 16, v81
	v_fmac_f32_e32 v26, v18, v7
	v_and_b32_e32 v7, 0xffff0000, v81
	v_fmac_f32_e32 v7, v19, v17
	v_lshlrev_b32_e32 v17, 16, v86
	v_mul_f32_e32 v17, 0xbfb8aa3b, v17
	v_exp_f32_e32 v18, v17
	v_and_b32_e32 v17, 0xffff0000, v86
	v_mul_f32_e32 v17, 0xbfb8aa3b, v17
	v_exp_f32_e32 v19, v17
	v_cvt_pk_bf16_f32 v17, v26, v7
	v_add_f32_e32 v7, 1.0, v18
	v_rcp_f32_e32 v7, v7
	v_add_f32_e32 v18, 1.0, v19
	v_rcp_f32_e32 v18, v18
	v_lshlrev_b32_e32 v19, 16, v82
	v_fmac_f32_e32 v19, v8, v7
	v_and_b32_e32 v7, 0xffff0000, v82
	v_lshlrev_b32_e32 v8, 16, v87
	v_fmac_f32_e32 v7, v9, v18
	v_mul_f32_e32 v8, 0xbfb8aa3b, v8
	v_and_b32_e32 v9, 0xffff0000, v87
	v_exp_f32_e32 v8, v8
	v_mul_f32_e32 v9, 0xbfb8aa3b, v9
	v_exp_f32_e32 v9, v9
	v_cvt_pk_bf16_f32 v18, v19, v7
	v_add_f32_e32 v7, 1.0, v8
	v_rcp_f32_e32 v7, v7
	v_add_f32_e32 v8, 1.0, v9
	v_rcp_f32_e32 v8, v8
	v_lshlrev_b32_e32 v9, 16, v83
	v_fmac_f32_e32 v9, v10, v7
	v_and_b32_e32 v7, 0xffff0000, v83
	v_lshlrev_b64 v[24:25], 12, v[120:121]
	v_fmac_f32_e32 v7, v11, v8
	v_cvt_pk_bf16_f32 v19, v9, v7
	v_lshl_add_u64 v[8:9], s[8:9], 0, v[24:25]
	s_waitcnt vmcnt(7)
	v_lshlrev_b32_e32 v7, 16, v76
	v_lshl_add_u64 v[4:5], v[8:9], 0, v[4:5]
	v_mul_f32_e32 v7, 0xbfb8aa3b, v7
	v_and_b32_e32 v8, 0xffff0000, v76
	v_exp_f32_e32 v7, v7
	v_mul_f32_e32 v8, 0xbfb8aa3b, v8
	v_exp_f32_e32 v8, v8
	s_waitcnt vmcnt(6)
	v_lshlrev_b32_e32 v9, 16, v72
	v_add_f32_e32 v7, 1.0, v7
	v_rcp_f32_e32 v7, v7
	v_add_f32_e32 v8, 1.0, v8
	v_rcp_f32_e32 v8, v8
	global_store_dwordx4 v[4:5], v[16:19], off sc1
	v_fmac_f32_e32 v9, v20, v7
	v_and_b32_e32 v7, 0xffff0000, v72
	v_fmac_f32_e32 v7, v21, v8
	v_lshlrev_b32_e32 v8, 16, v77
	v_mul_f32_e32 v8, 0xbfb8aa3b, v8
	v_exp_f32_e32 v10, v8
	v_and_b32_e32 v8, 0xffff0000, v77
	v_mul_f32_e32 v8, 0xbfb8aa3b, v8
	v_exp_f32_e32 v11, v8
	v_cvt_pk_bf16_f32 v8, v9, v7
	v_add_f32_e32 v7, 1.0, v10
	v_rcp_f32_e32 v7, v7
	v_add_f32_e32 v9, 1.0, v11
	v_rcp_f32_e32 v9, v9
	v_lshlrev_b32_e32 v10, 16, v73
	v_fmac_f32_e32 v10, v22, v7
	v_and_b32_e32 v7, 0xffff0000, v73
	v_fmac_f32_e32 v7, v23, v9
	v_lshlrev_b32_e32 v9, 16, v78
	v_mul_f32_e32 v9, 0xbfb8aa3b, v9
	v_exp_f32_e32 v11, v9
	v_and_b32_e32 v9, 0xffff0000, v78
	v_mul_f32_e32 v9, 0xbfb8aa3b, v9
	v_exp_f32_e32 v16, v9
	v_cvt_pk_bf16_f32 v9, v10, v7
	v_add_f32_e32 v7, 1.0, v11
	v_rcp_f32_e32 v7, v7
	v_add_f32_e32 v10, 1.0, v16
	v_rcp_f32_e32 v10, v10
	v_lshlrev_b32_e32 v11, 16, v74
	v_fmac_f32_e32 v11, v12, v7
	v_and_b32_e32 v7, 0xffff0000, v74
	v_fmac_f32_e32 v7, v13, v10
	v_lshlrev_b32_e32 v10, 16, v79
	v_mul_f32_e32 v10, 0xbfb8aa3b, v10
	v_exp_f32_e32 v12, v10
	v_and_b32_e32 v10, 0xffff0000, v79
	v_mul_f32_e32 v10, 0xbfb8aa3b, v10
	v_exp_f32_e32 v13, v10
	v_cvt_pk_bf16_f32 v10, v11, v7
	v_add_f32_e32 v7, 1.0, v12
	v_rcp_f32_e32 v7, v7
	v_add_f32_e32 v11, 1.0, v13
	v_rcp_f32_e32 v11, v11
	v_lshlrev_b32_e32 v12, 16, v75
	v_fmac_f32_e32 v12, v14, v7
	v_and_b32_e32 v7, 0xffff0000, v75
	v_fmac_f32_e32 v7, v15, v11
	v_cvt_pk_bf16_f32 v11, v12, v7
	global_store_dwordx4 v[4:5], v[8:11], off offset:256 sc1
	s_cbranch_vccnz .LBB0_664
	s_andn2_b64 vcc, exec, s[6:7]
	s_cbranch_vccnz .LBB0_663
	s_barrier
	s_branch .LBB0_663

.LBB0_764:
	v_lshl_add_u32 v144, s44, 8, v220
	v_lshl_or_b32 v4, s45, 8, v222
	v_readlane_b32 s44, v253, 18
	v_ashrrev_i32_e32 v5, 31, v4
	v_readlane_b32 s45, v253, 19
	v_ashrrev_i32_e32 v145, 31, v144
	v_lshlrev_b64 v[136:137], 13, v[144:145]
	v_lshl_add_u64 v[146:147], v[4:5], 2, s[44:45]
	v_or_b32_e32 v226, 16, v144
	v_lshl_add_u64 v[136:137], v[146:147], 0, v[136:137]
	v_ashrrev_i32_e32 v227, 31, v226
	global_load_dwordx4 v[148:151], v[136:137], off
	global_load_dwordx4 v[152:155], v[136:137], off offset:16
	global_load_dwordx4 v[156:159], v[136:137], off offset:512
	global_load_dwordx4 v[160:163], v[136:137], off offset:528
	v_lshlrev_b64 v[136:137], 13, v[226:227]
	v_or_b32_e32 v228, 32, v144
	v_lshl_add_u64 v[136:137], v[146:147], 0, v[136:137]
	v_ashrrev_i32_e32 v229, 31, v228
	global_load_dwordx4 v[164:167], v[136:137], off
	global_load_dwordx4 v[168:171], v[136:137], off offset:16
	global_load_dwordx4 v[172:175], v[136:137], off offset:528
	global_load_dwordx4 v[176:179], v[136:137], off offset:512
	v_lshlrev_b64 v[136:137], 13, v[228:229]
	v_lshl_add_u64 v[136:137], v[146:147], 0, v[136:137]
	global_load_dwordx4 v[180:183], v[136:137], off
	global_load_dwordx4 v[184:187], v[136:137], off offset:16
	global_load_dwordx4 v[188:191], v[136:137], off offset:512
	global_load_dwordx4 v[192:195], v[136:137], off offset:528
	v_or_b32_e32 v230, 48, v144
	v_ashrrev_i32_e32 v231, 31, v230
	v_lshlrev_b64 v[136:137], 13, v[230:231]
	v_lshl_add_u64 v[136:137], v[146:147], 0, v[136:137]
	global_load_dwordx4 v[196:199], v[136:137], off
	global_load_dwordx4 v[212:215], v[136:137], off offset:16
	global_load_dwordx4 v[140:143], v[136:137], off offset:512
	s_nop 0
	global_load_dwordx4 v[136:139], v[136:137], off offset:528
	v_lshlrev_b64 v[232:233], 12, v[144:145]
	v_lshlrev_b64 v[4:5], 1, v[4:5]
	v_lshl_add_u64 v[232:233], s[8:9], 0, v[232:233]
	v_lshlrev_b64 v[226:227], 12, v[226:227]
	v_lshl_add_u64 v[232:233], v[232:233], 0, v[4:5]
	v_lshl_add_u64 v[226:227], s[8:9], 0, v[226:227]
	v_lshlrev_b64 v[228:229], 12, v[228:229]
	v_lshl_add_u64 v[226:227], v[226:227], 0, v[4:5]
	v_lshl_add_u64 v[228:229], s[8:9], 0, v[228:229]
	v_lshl_add_u64 v[228:229], v[228:229], 0, v[4:5]
	s_andn2_b64 vcc, exec, s[0:1]
	s_mov_b64 s[0:1], -1
	v_readlane_b32 s46, v253, 20
	v_readlane_b32 s47, v253, 21
	v_readlane_b32 s48, v253, 22
	v_readlane_b32 s49, v253, 23
	v_readlane_b32 s50, v253, 24
	v_readlane_b32 s51, v253, 25
	v_readlane_b32 s52, v253, 26
	v_readlane_b32 s53, v253, 27
	v_readlane_b32 s54, v253, 28
	v_readlane_b32 s55, v253, 29
	v_readlane_b32 s56, v253, 30
	v_readlane_b32 s57, v253, 31
	v_readlane_b32 s58, v253, 32
	v_readlane_b32 s59, v253, 33
	s_waitcnt vmcnt(0)
	v_pk_add_f32 v[134:135], v[134:135], v[150:151]
	v_pk_add_f32 v[130:131], v[130:131], v[154:155]
	v_pk_add_f32 v[132:133], v[132:133], v[148:149]
	v_pk_add_f32 v[128:129], v[128:129], v[152:153]
	v_pk_add_f32 v[114:115], v[114:115], v[158:159]
	v_pk_add_f32 v[112:113], v[112:113], v[156:157]
	v_pk_add_f32 v[148:149], v[106:107], v[162:163]
	v_pk_add_f32 v[150:151], v[104:105], v[160:161]
	v_cvt_pk_bf16_f32 v104, v132, v133
	v_cvt_pk_bf16_f32 v105, v134, v135
	v_cvt_pk_bf16_f32 v106, v128, v129
	v_cvt_pk_bf16_f32 v107, v130, v131
	v_pk_add_f32 v[130:131], v[94:95], v[190:191]
	global_store_dwordx4 v[232:233], v[104:107], off sc1
	v_cvt_pk_bf16_f32 v94, v112, v113
	v_cvt_pk_bf16_f32 v95, v114, v115
	v_pk_add_f32 v[126:127], v[126:127], v[166:167]
	v_pk_add_f32 v[124:125], v[124:125], v[164:165]
	v_pk_add_f32 v[128:129], v[96:97], v[172:173]
	v_cvt_pk_bf16_f32 v96, v150, v151
	v_cvt_pk_bf16_f32 v97, v148, v149
	global_store_dwordx4 v[232:233], v[94:97], off offset:256 sc1
	v_pk_add_f32 v[122:123], v[122:123], v[170:171]
	v_pk_add_f32 v[120:121], v[120:121], v[168:169]
	v_cvt_pk_bf16_f32 v94, v124, v125
	v_cvt_pk_bf16_f32 v95, v126, v127
	v_pk_add_f32 v[102:103], v[102:103], v[178:179]
	v_pk_add_f32 v[100:101], v[100:101], v[176:177]
	v_cvt_pk_bf16_f32 v96, v120, v121
	v_cvt_pk_bf16_f32 v97, v122, v123
	global_store_dwordx4 v[226:227], v[94:97], off sc1
	v_pk_add_f32 v[98:99], v[98:99], v[174:175]
	v_pk_add_f32 v[118:119], v[118:119], v[182:183]
	v_cvt_pk_bf16_f32 v94, v100, v101
	v_cvt_pk_bf16_f32 v95, v102, v103
	v_pk_add_f32 v[116:117], v[116:117], v[180:181]
	v_cvt_pk_bf16_f32 v96, v128, v129
	v_cvt_pk_bf16_f32 v97, v98, v99
	global_store_dwordx4 v[226:227], v[94:97], off offset:256 sc1
	v_pk_add_f32 v[110:111], v[110:111], v[186:187]
	v_pk_add_f32 v[108:109], v[108:109], v[184:185]
	v_cvt_pk_bf16_f32 v94, v116, v117
	v_cvt_pk_bf16_f32 v95, v118, v119
	v_pk_add_f32 v[92:93], v[92:93], v[188:189]
	v_cvt_pk_bf16_f32 v96, v108, v109
	v_cvt_pk_bf16_f32 v97, v110, v111
	global_store_dwordx4 v[228:229], v[94:97], off sc1
	v_pk_add_f32 v[88:89], v[88:89], v[196:197]
	v_pk_add_f32 v[78:79], v[78:79], v[142:143]
	v_pk_add_f32 v[94:95], v[86:87], v[194:195]
	v_pk_add_f32 v[86:87], v[84:85], v[192:193]
	v_cvt_pk_bf16_f32 v84, v92, v93
	v_cvt_pk_bf16_f32 v85, v130, v131
	v_pk_add_f32 v[76:77], v[76:77], v[140:141]
	v_cvt_pk_bf16_f32 v86, v86, v87
	v_cvt_pk_bf16_f32 v87, v94, v95
	global_store_dwordx4 v[228:229], v[84:87], off offset:256 sc1
	v_add_u32_e32 v140, 0xa0, v144
	v_ashrrev_i32_e32 v141, 31, v140
	v_lshlrev_b64 v[84:85], 12, v[230:231]
	v_lshl_add_u64 v[84:85], s[8:9], 0, v[84:85]
	v_pk_add_f32 v[86:87], v[90:91], v[198:199]
	v_pk_add_f32 v[90:91], v[82:83], v[214:215]
	v_pk_add_f32 v[82:83], v[80:81], v[212:213]
	v_cvt_pk_bf16_f32 v80, v88, v89
	v_cvt_pk_bf16_f32 v81, v86, v87
	v_lshl_add_u64 v[84:85], v[84:85], 0, v[4:5]
	v_cvt_pk_bf16_f32 v82, v82, v83
	v_cvt_pk_bf16_f32 v83, v90, v91
	global_store_dwordx4 v[84:85], v[80:83], off sc1
	v_lshlrev_b64 v[104:105], 13, v[140:141]
	v_lshl_add_u64 v[116:117], v[146:147], 0, v[104:105]
	v_pk_add_f32 v[80:81], v[74:75], v[138:139]
	v_pk_add_f32 v[74:75], v[72:73], v[136:137]
	v_add_u32_e32 v136, 0x80, v144
	v_cvt_pk_bf16_f32 v72, v76, v77
	v_cvt_pk_bf16_f32 v73, v78, v79
	v_ashrrev_i32_e32 v137, 31, v136
	v_cvt_pk_bf16_f32 v74, v74, v75
	v_cvt_pk_bf16_f32 v75, v80, v81
	global_store_dwordx4 v[84:85], v[72:75], off offset:256 sc1
	v_add_u32_e32 v138, 0x90, v144
	v_ashrrev_i32_e32 v139, 31, v138
	v_lshlrev_b64 v[72:73], 13, v[136:137]
	v_lshl_add_u64 v[84:85], v[146:147], 0, v[72:73]
	global_load_dwordx4 v[72:75], v[84:85], off
	global_load_dwordx4 v[76:79], v[84:85], off offset:16
	global_load_dwordx4 v[80:83], v[84:85], off offset:528
	s_nop 0
	global_load_dwordx4 v[84:87], v[84:85], off offset:512
	v_lshlrev_b64 v[88:89], 13, v[138:139]
	v_lshl_add_u64 v[100:101], v[146:147], 0, v[88:89]
	global_load_dwordx4 v[88:91], v[100:101], off
	global_load_dwordx4 v[92:95], v[100:101], off offset:16
	global_load_dwordx4 v[96:99], v[100:101], off offset:512
	s_nop 0
	global_load_dwordx4 v[100:103], v[100:101], off offset:528
	s_nop 0
	global_load_dwordx4 v[104:107], v[116:117], off
	global_load_dwordx4 v[108:111], v[116:117], off offset:16
	global_load_dwordx4 v[112:115], v[116:117], off offset:512
	s_nop 0
	global_load_dwordx4 v[116:119], v[116:117], off offset:528
	v_add_u32_e32 v142, 0xb0, v144
	v_ashrrev_i32_e32 v143, 31, v142
	v_lshlrev_b64 v[120:121], 13, v[142:143]
	v_lshl_add_u64 v[132:133], v[146:147], 0, v[120:121]
	global_load_dwordx4 v[120:123], v[132:133], off
	global_load_dwordx4 v[124:127], v[132:133], off offset:16
	global_load_dwordx4 v[128:131], v[132:133], off offset:512
	s_nop 0
	global_load_dwordx4 v[132:135], v[132:133], off offset:528
	v_lshlrev_b64 v[136:137], 12, v[136:137]
	v_lshl_add_u64 v[136:137], s[8:9], 0, v[136:137]
	v_lshlrev_b64 v[138:139], 12, v[138:139]
	v_lshl_add_u64 v[136:137], v[136:137], 0, v[4:5]
	s_waitcnt vmcnt(15)
	v_pk_add_f32 v[70:71], v[70:71], v[74:75]
	v_pk_add_f32 v[68:69], v[68:69], v[72:73]
	s_waitcnt vmcnt(13)
	v_pk_add_f32 v[74:75], v[48:49], v[80:81]
	s_waitcnt vmcnt(12)
	v_pk_add_f32 v[52:53], v[52:53], v[84:85]
	v_cvt_pk_bf16_f32 v48, v68, v69
	v_cvt_pk_bf16_f32 v49, v70, v71
	v_pk_add_f32 v[66:67], v[66:67], v[78:79]
	v_pk_add_f32 v[64:65], v[64:65], v[76:77]
	v_pk_add_f32 v[54:55], v[54:55], v[86:87]
	v_pk_add_f32 v[72:73], v[50:51], v[82:83]
	v_cvt_pk_bf16_f32 v50, v64, v65
	v_cvt_pk_bf16_f32 v51, v66, v67
	global_store_dwordx4 v[136:137], v[48:51], off sc1
	s_waitcnt vmcnt(12)
	v_pk_add_f32 v[62:63], v[62:63], v[90:91]
	v_pk_add_f32 v[60:61], v[60:61], v[88:89]
	v_cvt_pk_bf16_f32 v48, v52, v53
	v_cvt_pk_bf16_f32 v49, v54, v55
	v_lshl_add_u64 v[52:53], s[8:9], 0, v[138:139]
	v_cvt_pk_bf16_f32 v50, v74, v75
	v_cvt_pk_bf16_f32 v51, v72, v73
	global_store_dwordx4 v[136:137], v[48:51], off offset:256 sc1
	v_lshl_add_u64 v[52:53], v[52:53], 0, v[4:5]
	s_waitcnt vmcnt(12)
	v_pk_add_f32 v[58:59], v[58:59], v[94:95]
	v_cvt_pk_bf16_f32 v48, v60, v61
	v_cvt_pk_bf16_f32 v49, v62, v63
	v_pk_add_f32 v[56:57], v[56:57], v[92:93]
	s_waitcnt vmcnt(11)
	v_pk_add_f32 v[38:39], v[38:39], v[98:99]
	v_cvt_pk_bf16_f32 v50, v56, v57
	v_cvt_pk_bf16_f32 v51, v58, v59
	global_store_dwordx4 v[52:53], v[48:51], off sc1
	v_pk_add_f32 v[36:37], v[36:37], v[96:97]
	s_waitcnt vmcnt(9)
	v_pk_add_f32 v[20:21], v[20:21], v[108:109]
	v_pk_add_f32 v[48:49], v[18:19], v[102:103]
	v_pk_add_f32 v[18:19], v[16:17], v[100:101]
	v_cvt_pk_bf16_f32 v16, v36, v37
	v_cvt_pk_bf16_f32 v17, v38, v39
	v_lshlrev_b64 v[36:37], 12, v[140:141]
	v_cvt_pk_bf16_f32 v18, v18, v19
	v_cvt_pk_bf16_f32 v19, v48, v49
	global_store_dwordx4 v[52:53], v[16:19], off offset:256 sc1
	v_pk_add_f32 v[22:23], v[22:23], v[110:111]
	s_waitcnt vmcnt(7)
	v_pk_add_f32 v[12:13], v[12:13], v[120:121]
	v_pk_add_f32 v[18:19], v[30:31], v[106:107]
	v_pk_add_f32 v[16:17], v[28:29], v[104:105]
	v_pk_add_f32 v[28:29], v[40:41], v[116:117]
	v_cvt_pk_bf16_f32 v16, v16, v17
	v_cvt_pk_bf16_f32 v17, v18, v19
	v_cvt_pk_bf16_f32 v18, v20, v21
	v_lshl_add_u64 v[20:21], s[8:9], 0, v[36:37]
	v_lshl_add_u64 v[20:21], v[20:21], 0, v[4:5]
	v_cvt_pk_bf16_f32 v19, v22, v23
	global_store_dwordx4 v[20:21], v[16:19], off sc1
	v_pk_add_f32 v[22:23], v[42:43], v[118:119]
	v_pk_add_f32 v[14:15], v[14:15], v[122:123]
	v_pk_add_f32 v[16:17], v[44:45], v[112:113]
	v_pk_add_f32 v[18:19], v[46:47], v[114:115]
	v_cvt_pk_bf16_f32 v16, v16, v17
	s_nop 0
	v_cvt_pk_bf16_f32 v17, v18, v19
	v_cvt_pk_bf16_f32 v18, v28, v29
	v_cvt_pk_bf16_f32 v19, v22, v23
	global_store_dwordx4 v[20:21], v[16:19], off offset:256 sc1
	s_nop 1
	v_lshlrev_b64 v[16:17], 12, v[142:143]
	s_waitcnt vmcnt(8)
	v_pk_add_f32 v[18:19], v[10:11], v[126:127]
	v_pk_add_f32 v[10:11], v[8:9], v[124:125]
	v_cvt_pk_bf16_f32 v8, v12, v13
	v_lshl_add_u64 v[12:13], s[8:9], 0, v[16:17]
	v_cvt_pk_bf16_f32 v9, v14, v15
	v_cvt_pk_bf16_f32 v10, v10, v11
	v_cvt_pk_bf16_f32 v11, v18, v19
	v_lshl_add_u64 v[4:5], v[12:13], 0, v[4:5]
	global_store_dwordx4 v[4:5], v[8:11], off sc1
	s_waitcnt vmcnt(7)
	v_pk_add_f32 v[12:13], v[26:27], v[134:135]
	v_pk_add_f32 v[14:15], v[24:25], v[132:133]
	v_pk_add_f32 v[10:11], v[34:35], v[130:131]
	v_pk_add_f32 v[8:9], v[32:33], v[128:129]
	s_nop 0
	v_cvt_pk_bf16_f32 v8, v8, v9
	v_cvt_pk_bf16_f32 v9, v10, v11
	v_cvt_pk_bf16_f32 v10, v14, v15
	v_cvt_pk_bf16_f32 v11, v12, v13
	global_store_dwordx4 v[4:5], v[8:11], off offset:256 sc1
	s_cbranch_vccnz .LBB0_748
	s_andn2_b64 vcc, exec, s[6:7]
	s_cbranch_vccnz .LBB0_747
	s_barrier
	s_branch .LBB0_747

.LBB0_935:
	s_add_i32 s51, s51, 1
	s_mul_i32 s0, s51, s59
	s_mul_hi_u32 s1, s51, s83
	s_add_i32 s1, s1, s0
	s_mul_i32 s0, s51, s83
	s_add_u32 s0, s0, s82
	s_addc_u32 s1, s1, s33
	v_cmp_ge_i64_e32 vcc, s[0:1], v[200:201]
	v_cmp_lt_i64_e64 s[4:5], s[0:1], v[200:201]
	s_cbranch_vccnz .LBB0_939
	s_ashr_i32 s1, s0, 31
	s_lshr_b32 s1, s1, 29
	s_add_i32 s1, s0, s1
	s_ashr_i32 s6, s1, 3
	s_and_b32 s1, s1, -8
	s_sub_i32 s0, s0, s1
	v_mov_b32_e32 v2, s0
	v_alignbit_b32 v2, s27, v2, 31
	s_nop 0
	v_readfirstlane_b32 s1, v2
	s_mul_i32 s0, s1, s0
	s_add_i32 s1, s0, s6
	s_ashr_i32 s0, s1, 31
	s_lshr_b32 s0, s0, 25
	s_add_i32 s6, s1, s0
	s_ashr_i32 s0, s6, 7
	s_lshl_b32 s7, s0, 3
	s_sub_i32 s0, s27, s7
	s_min_i32 s8, s0, 8
	s_abs_i32 s9, s8
	v_cvt_f32_u32_e32 v2, s9
	s_sub_i32 s29, 0, s9
	s_and_b32 s6, s6, 0xffffff80
	s_sub_i32 s1, s1, s6
	v_rcp_iflag_f32_e32 v2, v2
	s_abs_i32 s6, s1
	s_xor_b32 s28, s1, s8
	s_ashr_i32 s28, s28, 31
	v_mul_f32_e32 v2, 0x4f7ffffe, v2
	v_cvt_u32_f32_e32 v2, v2
	s_mov_b32 s0, 0
	v_readfirstlane_b32 s30, v2
	s_mul_i32 s29, s29, s30
	s_mul_hi_u32 s29, s30, s29
	s_add_i32 s30, s30, s29
	s_mul_hi_u32 s29, s6, s30
	s_mul_i32 s30, s29, s9
	s_sub_i32 s6, s6, s30
	s_add_i32 s31, s29, 1
	s_sub_i32 s30, s6, s9
	s_cmp_ge_u32 s6, s9
	s_cselect_b32 s29, s31, s29
	s_cselect_b32 s6, s30, s6
	s_add_i32 s30, s29, 1
	s_cmp_ge_u32 s6, s9
	s_cselect_b32 s6, s30, s29
	s_xor_b32 s6, s6, s28
	s_sub_i32 s28, s6, s28
	s_mul_i32 s6, s28, s8
	s_sub_i32 s1, s1, s6
	s_add_i32 s64, s1, s7
	v_and_b32_e32 v2, 31, v248
	v_lshlrev_b32_e32 v2, 2, v2
	v_add_u32_e32 v2, 0x23c44, v2
	ds_read_b32 v3, v2
	s_waitcnt lgkmcnt(0)
	v_cmp_ge_i32_e32 vcc, s64, v3
	s_nop 1
	s_bcnt1_i32_b32 s30, vcc_lo

.LBB0_948:
	v_readlane_b32 s68, v253, 4
	s_ashr_i32 s39, s38, 31
	v_readlane_b32 s70, v253, 6
	v_readlane_b32 s71, v253, 7
	s_lshl_b64 s[4:5], s[38:39], 14
	s_mov_b64 s[66:67], s[70:71]
	v_lshl_or_b32 v20, s36, 7, v237
	s_add_u32 s4, s66, s4
	s_addc_u32 s5, s67, s5
	v_ashrrev_i32_e32 v21, 31, v20
	v_lshl_add_u64 v[2:3], v[20:21], 2, s[4:5]
	global_load_dwordx4 v[10:13], v[2:3], off
	global_load_dwordx4 v[6:9], v[2:3], off offset:16
	v_add_co_u32_e32 v4, vcc, s52, v2
	v_mov_b32_e32 v24, v67
	s_nop 0
	v_addc_co_u32_e32 v5, vcc, 0, v3, vcc
	global_load_dwordx4 v[14:17], v[4:5], off
	v_lshl_add_u64 v[2:3], v[2:3], 0, s[24:25]
	global_load_dwordx4 v[2:5], v[2:3], off offset:16
	s_and_b64 vcc, exec, s[22:23]
	s_cbranch_vccz .LBB0_950
	s_barrier
.LBB0_950:
	s_nop 15
	s_nop 15
	v_lshl_add_u32 v22, s65, 8, v220
	v_readlane_b32 s69, v253, 5
	v_readlane_b32 s72, v253, 8
	v_readlane_b32 s73, v253, 9
	v_readlane_b32 s74, v253, 10
	v_readlane_b32 s75, v253, 11
	s_waitcnt vmcnt(0)
	v_pk_fma_f32 v[26:27], v[196:197], s[26:27], v[10:11] op_sel_hi:[1,0,1]
	s_nop 0
	v_min_f32_e32 v23, 0x40e00000, v26
	v_min_f32_e32 v25, 0x40e00000, v27
	v_mul_f32_e32 v38, 0x3fd9db23, v23
	v_mul_f32_e32 v39, 0x3fd9db23, v25
	v_mul_f32_e32 v38, 0xbfb8aa3b, v38
	v_mul_f32_e32 v39, 0xbfb8aa3b, v39
	v_pk_fma_f32 v[18:19], v[198:199], s[26:27], v[12:13] op_sel_hi:[1,0,1]
	v_exp_f32_e32 v38, v38
	v_exp_f32_e32 v39, v39
	v_min_f32_e32 v32, 0x40e00000, v18
	v_min_f32_e32 v33, 0x40e00000, v19
	v_pk_fma_f32 v[30:31], v[192:193], s[26:27], v[6:7] op_sel_hi:[1,0,1]
	v_mul_f32_e32 v40, 0x3fd9db23, v32
	v_mul_f32_e32 v41, 0x3fd9db23, v33
	v_min_f32_e32 v34, 0x40e00000, v30
	v_min_f32_e32 v35, 0x40e00000, v31
	v_mul_f32_e32 v40, 0xbfb8aa3b, v40
	v_mul_f32_e32 v41, 0xbfb8aa3b, v41
	v_mul_f32_e32 v42, 0x3fd9db23, v34
	v_mul_f32_e32 v43, 0x3fd9db23, v35
	v_exp_f32_e32 v40, v40
	v_exp_f32_e32 v41, v41
	v_add_f32_e32 v38, 1.0, v38
	v_add_f32_e32 v39, 1.0, v39
	v_mul_f32_e32 v42, 0xbfb8aa3b, v42
	v_mul_f32_e32 v43, 0xbfb8aa3b, v43
	v_rcp_f32_e32 v38, v38
	v_rcp_f32_e32 v39, v39
	v_pk_fma_f32 v[28:29], v[194:195], s[26:27], v[8:9] op_sel_hi:[1,0,1]
	v_exp_f32_e32 v42, v42
	v_exp_f32_e32 v43, v43
	v_min_f32_e32 v36, 0x40e00000, v28
	v_min_f32_e32 v37, 0x40e00000, v29
	v_pk_fma_f32 v[26:27], v[188:189], s[26:27], v[14:15] op_sel_hi:[1,0,1]
	v_mul_f32_e32 v44, 0x3fd9db23, v36
	v_mul_f32_e32 v45, 0x3fd9db23, v37
	v_med3_f32 v26, v26, s60, v239
	v_med3_f32 v27, v27, s60, v239
	v_add_f32_e32 v40, 1.0, v40
	v_add_f32_e32 v41, 1.0, v41
	v_mul_f32_e32 v44, 0xbfb8aa3b, v44
	v_mul_f32_e32 v45, 0xbfb8aa3b, v45
	v_add_f32_e32 v26, 1.0, v26
	v_add_f32_e32 v27, 1.0, v27
	v_rcp_f32_e32 v40, v40
	v_rcp_f32_e32 v41, v41
	v_mul_f32_e32 v23, v23, v38
	v_mul_f32_e32 v25, v25, v39
	v_exp_f32_e32 v44, v44
	v_exp_f32_e32 v45, v45
	v_add_f32_e32 v42, 1.0, v42
	v_add_f32_e32 v43, 1.0, v43
	v_mul_f32_e32 v23, v26, v23
	v_mul_f32_e32 v25, v27, v25
	v_pk_fma_f32 v[18:19], v[190:191], s[26:27], v[16:17] op_sel_hi:[1,0,1]
	v_rcp_f32_e32 v42, v42
	v_rcp_f32_e32 v43, v43
	v_cvt_pk_fp8_f32 v24, v23, v25
	v_med3_f32 v18, v18, s60, v239
	v_med3_f32 v19, v19, s60, v239
	v_pk_fma_f32 v[30:31], v[184:185], s[26:27], v[2:3] op_sel_hi:[1,0,1]
	v_add_f32_e32 v18, 1.0, v18
	v_add_f32_e32 v19, 1.0, v19
	v_mul_f32_e32 v32, v32, v40
	v_mul_f32_e32 v33, v33, v41
	v_med3_f32 v30, v30, s60, v239
	v_med3_f32 v31, v31, s60, v239
	v_add_f32_e32 v44, 1.0, v44
	v_add_f32_e32 v45, 1.0, v45
	v_mul_f32_e32 v18, v18, v32
	v_mul_f32_e32 v19, v19, v33
	v_add_f32_e32 v30, 1.0, v30
	v_add_f32_e32 v31, 1.0, v31
	v_rcp_f32_e32 v44, v44
	v_mul_f32_e32 v34, v34, v42
	v_mul_f32_e32 v35, v35, v43
	v_cvt_pk_fp8_f32 v24, v18, v19 op_sel:[0,0,1]
	v_rcp_f32_e32 v18, v45
	v_mul_f32_e32 v23, v30, v34
	v_mul_f32_e32 v26, v31, v35
	v_mov_b32_e32 v25, v67
	v_pk_fma_f32 v[28:29], v[186:187], s[26:27], v[4:5] op_sel_hi:[1,0,1]
	v_cvt_pk_fp8_f32 v25, v23, v26
	v_med3_f32 v28, v28, s60, v239
	v_med3_f32 v19, v29, s60, v239
	v_add_f32_e32 v28, 1.0, v28
	v_mul_f32_e32 v36, v36, v44
	v_mul_f32_e32 v18, v37, v18
	v_add_f32_e32 v19, 1.0, v19
	v_mul_f32_e32 v27, v28, v36
	v_mul_f32_e32 v18, v19, v18
	v_cvt_pk_fp8_f32 v25, v27, v18 op_sel:[0,0,1]
	v_ashrrev_i32_e32 v23, 31, v22
	v_pk_fma_f32 v[26:27], v[180:181], s[26:27], v[10:11] op_sel_hi:[1,0,1]
	v_lshlrev_b64 v[18:19], 11, v[22:23]
	v_min_f32_e32 v23, 0x40e00000, v26
	v_mul_f32_e32 v26, 0x3fd9db23, v23
	v_mul_f32_e32 v26, 0xbfb8aa3b, v26
	v_exp_f32_e32 v26, v26
	v_min_f32_e32 v27, 0x40e00000, v27
	v_mul_f32_e32 v40, 0x3fd9db23, v27
	v_mul_f32_e32 v40, 0xbfb8aa3b, v40
	v_add_f32_e32 v26, 1.0, v26
	v_rcp_f32_e32 v26, v26
	v_exp_f32_e32 v40, v40
	v_pk_fma_f32 v[34:35], v[172:173], s[26:27], v[14:15] op_sel_hi:[1,0,1]
	v_lshl_add_u64 v[18:19], s[16:17], 0, v[18:19]
	v_med3_f32 v34, v34, s60, v239
	v_mul_f32_e32 v23, v23, v26
	v_add_f32_e32 v26, 1.0, v34
	v_lshl_add_u64 v[18:19], v[18:19], 0, v[20:21]
	v_mul_f32_e32 v23, v26, v23
	v_add_f32_e32 v26, 1.0, v40
	global_store_dwordx2 v[18:19], v[24:25], off
	v_pk_fma_f32 v[24:25], v[182:183], s[26:27], v[12:13] op_sel_hi:[1,0,1]
	v_rcp_f32_e32 v26, v26
	v_min_f32_e32 v24, 0x40e00000, v24
	v_mul_f32_e32 v34, 0x3fd9db23, v24
	v_mul_f32_e32 v34, 0xbfb8aa3b, v34
	v_med3_f32 v35, v35, s60, v239
	v_min_f32_e32 v25, 0x40e00000, v25
	v_exp_f32_e32 v34, v34
	v_mul_f32_e32 v26, v27, v26
	v_add_f32_e32 v27, 1.0, v35
	v_mul_f32_e32 v35, 0x3fd9db23, v25
	v_mul_f32_e32 v35, 0xbfb8aa3b, v35
	v_exp_f32_e32 v35, v35
	v_add_f32_e32 v34, 1.0, v34
	v_pk_fma_f32 v[32:33], v[174:175], s[26:27], v[16:17] op_sel_hi:[1,0,1]
	v_rcp_f32_e32 v34, v34
	v_mul_f32_e32 v26, v27, v26
	v_med3_f32 v27, v32, s60, v239
	v_add_f32_e32 v32, 1.0, v35
	v_rcp_f32_e32 v32, v32
	v_mul_f32_e32 v24, v24, v34
	v_add_f32_e32 v27, 1.0, v27
	v_mul_f32_e32 v27, v27, v24
	v_med3_f32 v24, v33, s60, v239
	v_mul_f32_e32 v25, v25, v32
	v_add_f32_e32 v24, 1.0, v24
	v_pk_fma_f32 v[30:31], v[176:177], s[26:27], v[6:7] op_sel_hi:[1,0,1]
	v_mul_f32_e32 v25, v24, v25
	v_mov_b32_e32 v24, v67
	v_cvt_pk_fp8_f32 v24, v23, v26
	v_min_f32_e32 v26, 0x40e00000, v31
	v_mul_f32_e32 v31, 0x3fd9db23, v26
	v_mul_f32_e32 v31, 0xbfb8aa3b, v31
	v_exp_f32_e32 v31, v31
	v_min_f32_e32 v30, 0x40e00000, v30
	v_cvt_pk_fp8_f32 v24, v27, v25 op_sel:[0,0,1]
	v_mul_f32_e32 v32, 0x3fd9db23, v30
	v_add_f32_e32 v27, 1.0, v31
	v_rcp_f32_e32 v27, v27
	v_mul_f32_e32 v32, 0xbfb8aa3b, v32
	v_exp_f32_e32 v32, v32
	v_pk_fma_f32 v[28:29], v[178:179], s[26:27], v[8:9] op_sel_hi:[1,0,1]
	v_mul_f32_e32 v26, v26, v27
	v_min_f32_e32 v27, 0x40e00000, v28
	v_mul_f32_e32 v28, 0x3fd9db23, v27
	v_add_f32_e32 v23, 1.0, v32
	v_mul_f32_e32 v28, 0xbfb8aa3b, v28
	v_rcp_f32_e32 v23, v23
	v_exp_f32_e32 v28, v28
	v_pk_fma_f32 v[38:39], v[168:169], s[26:27], v[2:3] op_sel_hi:[1,0,1]
	v_min_f32_e32 v29, 0x40e00000, v29
	v_med3_f32 v25, v38, s60, v239
	v_mul_f32_e32 v23, v30, v23
	v_add_f32_e32 v28, 1.0, v28
	v_mul_f32_e32 v30, 0x3fd9db23, v29
	v_add_f32_e32 v25, 1.0, v25
	v_rcp_f32_e32 v28, v28
	v_mul_f32_e32 v30, 0xbfb8aa3b, v30
	v_mul_f32_e32 v23, v25, v23
	v_med3_f32 v25, v39, s60, v239
	v_exp_f32_e32 v30, v30
	v_pk_fma_f32 v[36:37], v[170:171], s[26:27], v[4:5] op_sel_hi:[1,0,1]
	v_add_f32_e32 v25, 1.0, v25
	v_mul_f32_e32 v26, v25, v26
	v_med3_f32 v25, v36, s60, v239
	v_mul_f32_e32 v27, v27, v28
	v_add_f32_e32 v25, 1.0, v25
	v_mul_f32_e32 v27, v25, v27
	v_add_f32_e32 v25, 1.0, v30
	v_rcp_f32_e32 v28, v25
	v_mov_b32_e32 v25, v67
	v_cvt_pk_fp8_f32 v25, v23, v26
	v_med3_f32 v30, v37, s60, v239
	v_mul_f32_e32 v23, v29, v28
	v_add_f32_e32 v26, 1.0, v30
	v_mul_f32_e32 v23, v26, v23
	v_or_b32_e32 v26, 16, v22
	v_cvt_pk_fp8_f32 v25, v27, v23 op_sel:[0,0,1]
	v_ashrrev_i32_e32 v27, 31, v26
	v_lshlrev_b64 v[26:27], 11, v[26:27]
	v_lshl_add_u64 v[26:27], s[16:17], 0, v[26:27]
	v_lshl_add_u64 v[26:27], v[26:27], 0, v[20:21]
	global_store_dwordx2 v[26:27], v[24:25], off
	v_pk_fma_f32 v[26:27], v[164:165], s[26:27], v[10:11] op_sel_hi:[1,0,1]
	v_pk_fma_f32 v[34:35], v[156:157], s[26:27], v[14:15] op_sel_hi:[1,0,1]
	v_min_f32_e32 v23, 0x40e00000, v26
	v_mul_f32_e32 v26, 0x3fd9db23, v23
	v_mul_f32_e32 v26, 0xbfb8aa3b, v26
	v_exp_f32_e32 v26, v26
	v_min_f32_e32 v27, 0x40e00000, v27
	v_mul_f32_e32 v40, 0x3fd9db23, v27
	v_mul_f32_e32 v40, 0xbfb8aa3b, v40
	v_add_f32_e32 v26, 1.0, v26
	v_rcp_f32_e32 v26, v26
	v_exp_f32_e32 v40, v40
	v_med3_f32 v34, v34, s60, v239
	v_pk_fma_f32 v[24:25], v[166:167], s[26:27], v[12:13] op_sel_hi:[1,0,1]
	v_mul_f32_e32 v23, v23, v26
	v_add_f32_e32 v26, 1.0, v34
	v_mul_f32_e32 v23, v26, v23
	v_add_f32_e32 v26, 1.0, v40
	v_rcp_f32_e32 v26, v26
	v_min_f32_e32 v24, 0x40e00000, v24
	v_mul_f32_e32 v34, 0x3fd9db23, v24
	v_mul_f32_e32 v34, 0xbfb8aa3b, v34
	v_med3_f32 v35, v35, s60, v239
	v_min_f32_e32 v25, 0x40e00000, v25
	v_exp_f32_e32 v34, v34
	v_mul_f32_e32 v26, v27, v26
	v_add_f32_e32 v27, 1.0, v35
	v_mul_f32_e32 v35, 0x3fd9db23, v25
	v_mul_f32_e32 v35, 0xbfb8aa3b, v35
	v_exp_f32_e32 v35, v35
	v_add_f32_e32 v34, 1.0, v34
	v_pk_fma_f32 v[32:33], v[158:159], s[26:27], v[16:17] op_sel_hi:[1,0,1]
	v_rcp_f32_e32 v34, v34
	v_mul_f32_e32 v26, v27, v26
	v_med3_f32 v27, v32, s60, v239
	v_add_f32_e32 v32, 1.0, v35
	v_rcp_f32_e32 v32, v32
	v_mul_f32_e32 v24, v24, v34
	v_add_f32_e32 v27, 1.0, v27
	v_mul_f32_e32 v27, v27, v24
	v_med3_f32 v24, v33, s60, v239
	v_mul_f32_e32 v25, v25, v32
	v_add_f32_e32 v24, 1.0, v24
	v_pk_fma_f32 v[30:31], v[160:161], s[26:27], v[6:7] op_sel_hi:[1,0,1]
	v_mul_f32_e32 v25, v24, v25
	v_mov_b32_e32 v24, v67
	v_cvt_pk_fp8_f32 v24, v23, v26
	v_min_f32_e32 v26, 0x40e00000, v31
	v_mul_f32_e32 v31, 0x3fd9db23, v26
	v_mul_f32_e32 v31, 0xbfb8aa3b, v31
	v_exp_f32_e32 v31, v31
	v_min_f32_e32 v30, 0x40e00000, v30
	v_cvt_pk_fp8_f32 v24, v27, v25 op_sel:[0,0,1]
	v_mul_f32_e32 v32, 0x3fd9db23, v30
	v_add_f32_e32 v27, 1.0, v31
	v_rcp_f32_e32 v27, v27
	v_mul_f32_e32 v32, 0xbfb8aa3b, v32
	v_exp_f32_e32 v32, v32
	v_pk_fma_f32 v[28:29], v[162:163], s[26:27], v[8:9] op_sel_hi:[1,0,1]
	v_mul_f32_e32 v26, v26, v27
	v_min_f32_e32 v27, 0x40e00000, v28
	v_mul_f32_e32 v28, 0x3fd9db23, v27
	v_add_f32_e32 v23, 1.0, v32
	v_mul_f32_e32 v28, 0xbfb8aa3b, v28
	v_rcp_f32_e32 v23, v23
	v_exp_f32_e32 v28, v28
	v_pk_fma_f32 v[38:39], v[152:153], s[26:27], v[2:3] op_sel_hi:[1,0,1]
	v_min_f32_e32 v29, 0x40e00000, v29
	v_med3_f32 v25, v38, s60, v239
	v_mul_f32_e32 v23, v30, v23
	v_add_f32_e32 v28, 1.0, v28
	v_mul_f32_e32 v30, 0x3fd9db23, v29
	v_add_f32_e32 v25, 1.0, v25
	v_rcp_f32_e32 v28, v28
	v_mul_f32_e32 v30, 0xbfb8aa3b, v30
	v_mul_f32_e32 v23, v25, v23
	v_med3_f32 v25, v39, s60, v239
	v_exp_f32_e32 v30, v30
	v_pk_fma_f32 v[36:37], v[154:155], s[26:27], v[4:5] op_sel_hi:[1,0,1]
	v_add_f32_e32 v25, 1.0, v25
	v_mul_f32_e32 v26, v25, v26
	v_med3_f32 v25, v36, s60, v239
	v_mul_f32_e32 v27, v27, v28
	v_add_f32_e32 v25, 1.0, v25
	v_mul_f32_e32 v27, v25, v27
	v_add_f32_e32 v25, 1.0, v30
	v_rcp_f32_e32 v28, v25
	v_mov_b32_e32 v25, v67
	v_cvt_pk_fp8_f32 v25, v23, v26
	v_med3_f32 v30, v37, s60, v239
	v_mul_f32_e32 v23, v29, v28
	v_add_f32_e32 v26, 1.0, v30
	v_mul_f32_e32 v23, v26, v23
	v_or_b32_e32 v26, 32, v22
	v_cvt_pk_fp8_f32 v25, v27, v23 op_sel:[0,0,1]
	v_ashrrev_i32_e32 v27, 31, v26
	v_lshlrev_b64 v[26:27], 11, v[26:27]
	v_lshl_add_u64 v[26:27], s[16:17], 0, v[26:27]
	v_lshl_add_u64 v[26:27], v[26:27], 0, v[20:21]
	global_store_dwordx2 v[26:27], v[24:25], off
	v_pk_fma_f32 v[26:27], v[148:149], s[26:27], v[10:11] op_sel_hi:[1,0,1]
	v_pk_fma_f32 v[34:35], v[140:141], s[26:27], v[14:15] op_sel_hi:[1,0,1]
	v_min_f32_e32 v23, 0x40e00000, v26
	v_mul_f32_e32 v26, 0x3fd9db23, v23
	v_mul_f32_e32 v26, 0xbfb8aa3b, v26
	v_exp_f32_e32 v26, v26
	v_min_f32_e32 v27, 0x40e00000, v27
	v_mul_f32_e32 v40, 0x3fd9db23, v27
	v_mul_f32_e32 v40, 0xbfb8aa3b, v40
	v_add_f32_e32 v26, 1.0, v26
	v_rcp_f32_e32 v26, v26
	v_exp_f32_e32 v40, v40
	v_med3_f32 v34, v34, s60, v239
	v_pk_fma_f32 v[24:25], v[150:151], s[26:27], v[12:13] op_sel_hi:[1,0,1]
	v_mul_f32_e32 v23, v23, v26
	v_add_f32_e32 v26, 1.0, v34
	v_mul_f32_e32 v23, v26, v23
	v_add_f32_e32 v26, 1.0, v40
	v_rcp_f32_e32 v26, v26
	v_min_f32_e32 v24, 0x40e00000, v24
	v_mul_f32_e32 v34, 0x3fd9db23, v24
	v_mul_f32_e32 v34, 0xbfb8aa3b, v34
	v_med3_f32 v35, v35, s60, v239
	v_min_f32_e32 v25, 0x40e00000, v25
	v_exp_f32_e32 v34, v34
	v_mul_f32_e32 v26, v27, v26
	v_add_f32_e32 v27, 1.0, v35
	v_mul_f32_e32 v35, 0x3fd9db23, v25
	v_mul_f32_e32 v35, 0xbfb8aa3b, v35
	v_exp_f32_e32 v35, v35
	v_add_f32_e32 v34, 1.0, v34
	v_pk_fma_f32 v[32:33], v[142:143], s[26:27], v[16:17] op_sel_hi:[1,0,1]
	v_rcp_f32_e32 v34, v34
	v_mul_f32_e32 v26, v27, v26
	v_med3_f32 v27, v32, s60, v239
	v_add_f32_e32 v32, 1.0, v35
	v_rcp_f32_e32 v32, v32
	v_mul_f32_e32 v24, v24, v34
	v_add_f32_e32 v27, 1.0, v27
	v_mul_f32_e32 v27, v27, v24
	v_med3_f32 v24, v33, s60, v239
	v_mul_f32_e32 v25, v25, v32
	v_add_f32_e32 v24, 1.0, v24
	v_pk_fma_f32 v[30:31], v[144:145], s[26:27], v[6:7] op_sel_hi:[1,0,1]
	v_mul_f32_e32 v25, v24, v25
	v_mov_b32_e32 v24, v67
	v_cvt_pk_fp8_f32 v24, v23, v26
	v_min_f32_e32 v26, 0x40e00000, v31
	v_mul_f32_e32 v31, 0x3fd9db23, v26
	v_mul_f32_e32 v31, 0xbfb8aa3b, v31
	v_exp_f32_e32 v31, v31
	v_min_f32_e32 v30, 0x40e00000, v30
	v_cvt_pk_fp8_f32 v24, v27, v25 op_sel:[0,0,1]
	v_mul_f32_e32 v32, 0x3fd9db23, v30
	v_add_f32_e32 v27, 1.0, v31
	v_rcp_f32_e32 v27, v27
	v_mul_f32_e32 v32, 0xbfb8aa3b, v32
	v_exp_f32_e32 v32, v32
	v_pk_fma_f32 v[28:29], v[146:147], s[26:27], v[8:9] op_sel_hi:[1,0,1]
	v_mul_f32_e32 v26, v26, v27
	v_min_f32_e32 v27, 0x40e00000, v28
	v_mul_f32_e32 v28, 0x3fd9db23, v27
	v_add_f32_e32 v23, 1.0, v32
	v_mul_f32_e32 v28, 0xbfb8aa3b, v28
	v_rcp_f32_e32 v23, v23
	v_exp_f32_e32 v28, v28
	v_pk_fma_f32 v[38:39], v[136:137], s[26:27], v[2:3] op_sel_hi:[1,0,1]
	v_min_f32_e32 v29, 0x40e00000, v29
	v_med3_f32 v25, v38, s60, v239
	v_mul_f32_e32 v23, v30, v23
	v_add_f32_e32 v28, 1.0, v28
	v_mul_f32_e32 v30, 0x3fd9db23, v29
	v_add_f32_e32 v25, 1.0, v25
	v_rcp_f32_e32 v28, v28
	v_mul_f32_e32 v30, 0xbfb8aa3b, v30
	v_mul_f32_e32 v23, v25, v23
	v_med3_f32 v25, v39, s60, v239
	v_exp_f32_e32 v30, v30
	v_pk_fma_f32 v[36:37], v[138:139], s[26:27], v[4:5] op_sel_hi:[1,0,1]
	v_add_f32_e32 v25, 1.0, v25
	v_mul_f32_e32 v26, v25, v26
	v_med3_f32 v25, v36, s60, v239
	v_mul_f32_e32 v27, v27, v28
	v_add_f32_e32 v25, 1.0, v25
	v_mul_f32_e32 v27, v25, v27
	v_add_f32_e32 v25, 1.0, v30
	v_rcp_f32_e32 v28, v25
	v_mov_b32_e32 v25, v67
	v_cvt_pk_fp8_f32 v25, v23, v26
	v_med3_f32 v30, v37, s60, v239
	v_mul_f32_e32 v23, v29, v28
	v_add_f32_e32 v26, 1.0, v30
	v_mul_f32_e32 v23, v26, v23
	v_or_b32_e32 v22, 48, v22
	v_cvt_pk_fp8_f32 v25, v27, v23 op_sel:[0,0,1]
	v_ashrrev_i32_e32 v23, 31, v22
	v_lshlrev_b64 v[22:23], 11, v[22:23]
	v_lshl_add_u64 v[22:23], s[16:17], 0, v[22:23]
	v_lshl_add_u64 v[20:21], v[22:23], 0, v[20:21]
	v_pk_fma_f32 v[22:23], v[132:133], s[26:27], v[10:11] op_sel_hi:[1,0,1]
	global_store_dwordx2 v[20:21], v[24:25], off
	v_min_f32_e32 v22, 0x40e00000, v22
	v_mul_f32_e32 v32, 0x3fd9db23, v22
	v_mul_f32_e32 v32, 0xbfb8aa3b, v32
	v_exp_f32_e32 v36, v32
	v_min_f32_e32 v23, 0x40e00000, v23
	v_mul_f32_e32 v37, 0x3fd9db23, v23
	v_mul_f32_e32 v37, 0xbfb8aa3b, v37
	v_add_f32_e32 v36, 1.0, v36
	v_rcp_f32_e32 v36, v36
	v_exp_f32_e32 v37, v37
	v_pk_fma_f32 v[20:21], v[134:135], s[26:27], v[12:13] op_sel_hi:[1,0,1]
	v_pk_fma_f32 v[30:31], v[124:125], s[26:27], v[14:15] op_sel_hi:[1,0,1]
	v_min_f32_e32 v20, 0x40e00000, v20
	v_med3_f32 v30, v30, s60, v239
	v_mul_f32_e32 v22, v22, v36
	v_add_f32_e32 v30, 1.0, v30
	v_mul_f32_e32 v36, 0x3fd9db23, v20
	v_mul_f32_e32 v22, v30, v22
	v_add_f32_e32 v30, 1.0, v37
	v_mul_f32_e32 v36, 0xbfb8aa3b, v36
	v_rcp_f32_e32 v30, v30
	v_exp_f32_e32 v36, v36
	v_med3_f32 v31, v31, s60, v239
	v_min_f32_e32 v21, 0x40e00000, v21
	v_mul_f32_e32 v23, v23, v30
	v_add_f32_e32 v30, 1.0, v31
	v_add_f32_e32 v31, 1.0, v36
	v_mul_f32_e32 v36, 0x3fd9db23, v21
	v_mul_f32_e32 v36, 0xbfb8aa3b, v36
	v_exp_f32_e32 v36, v36
	v_rcp_f32_e32 v31, v31
	v_pk_fma_f32 v[28:29], v[126:127], s[26:27], v[16:17] op_sel_hi:[1,0,1]
	v_mul_f32_e32 v23, v30, v23
	v_add_f32_e32 v30, 1.0, v36
	v_pk_fma_f32 v[26:27], v[128:129], s[26:27], v[6:7] op_sel_hi:[1,0,1]
	v_med3_f32 v28, v28, s60, v239
	v_rcp_f32_e32 v30, v30
	v_mul_f32_e32 v20, v20, v31
	v_add_f32_e32 v28, 1.0, v28
	v_min_f32_e32 v26, 0x40e00000, v26
	v_mul_f32_e32 v28, v28, v20
	v_med3_f32 v20, v29, s60, v239
	v_mul_f32_e32 v29, 0x3fd9db23, v26
	v_mul_f32_e32 v29, 0xbfb8aa3b, v29
	v_mul_f32_e32 v21, v21, v30
	v_add_f32_e32 v20, 1.0, v20
	v_exp_f32_e32 v29, v29
	v_mul_f32_e32 v21, v20, v21
	v_mov_b32_e32 v20, v67
	v_cvt_pk_fp8_f32 v20, v22, v23
	v_min_f32_e32 v23, 0x40e00000, v27
	v_mul_f32_e32 v27, 0x3fd9db23, v23
	v_add_f32_e32 v22, 1.0, v29
	v_mul_f32_e32 v27, 0xbfb8aa3b, v27
	v_rcp_f32_e32 v22, v22
	v_exp_f32_e32 v27, v27
	v_pk_fma_f32 v[24:25], v[130:131], s[26:27], v[8:9] op_sel_hi:[1,0,1]
	v_pk_fma_f32 v[34:35], v[120:121], s[26:27], v[2:3] op_sel_hi:[1,0,1]
	v_mul_f32_e32 v22, v26, v22
	v_add_f32_e32 v26, 1.0, v27
	v_rcp_f32_e32 v26, v26
	v_min_f32_e32 v24, 0x40e00000, v24
	v_min_f32_e32 v25, 0x40e00000, v25
	v_cvt_pk_fp8_f32 v20, v28, v21 op_sel:[0,0,1]
	v_mul_f32_e32 v23, v23, v26
	v_mul_f32_e32 v26, 0x3fd9db23, v24
	v_mul_f32_e32 v26, 0xbfb8aa3b, v26
	v_exp_f32_e32 v26, v26
	v_med3_f32 v21, v34, s60, v239
	v_mul_f32_e32 v27, 0x3fd9db23, v25
	v_add_f32_e32 v21, 1.0, v21
	v_add_f32_e32 v26, 1.0, v26
	v_rcp_f32_e32 v26, v26
	v_mul_f32_e32 v27, 0xbfb8aa3b, v27
	v_mul_f32_e32 v22, v21, v22
	v_med3_f32 v21, v35, s60, v239
	v_exp_f32_e32 v27, v27
	v_pk_fma_f32 v[32:33], v[122:123], s[26:27], v[4:5] op_sel_hi:[1,0,1]
	v_add_f32_e32 v21, 1.0, v21
	v_mul_f32_e32 v23, v21, v23
	v_med3_f32 v21, v32, s60, v239
	v_mul_f32_e32 v24, v24, v26
	v_add_f32_e32 v21, 1.0, v21
	v_mul_f32_e32 v24, v21, v24
	v_add_f32_e32 v21, 1.0, v27
	v_rcp_f32_e32 v26, v21
	v_mov_b32_e32 v21, v67
	v_cvt_pk_fp8_f32 v21, v22, v23
	v_med3_f32 v27, v33, s60, v239
	v_mul_f32_e32 v22, v25, v26
	v_add_f32_e32 v23, 1.0, v27
	v_mul_f32_e32 v22, v23, v22
	v_cvt_pk_fp8_f32 v21, v24, v22 op_sel:[0,0,1]
	v_add_co_u32_e32 v22, vcc, s61, v18
	v_pk_fma_f32 v[30:31], v[108:109], s[26:27], v[14:15] op_sel_hi:[1,0,1]
	s_nop 0
	v_addc_co_u32_e32 v23, vcc, 0, v19, vcc
	global_store_dwordx2 v[22:23], v[20:21], off
	v_pk_fma_f32 v[22:23], v[116:117], s[26:27], v[10:11] op_sel_hi:[1,0,1]
	v_pk_fma_f32 v[20:21], v[118:119], s[26:27], v[12:13] op_sel_hi:[1,0,1]
	v_min_f32_e32 v22, 0x40e00000, v22
	v_mul_f32_e32 v32, 0x3fd9db23, v22
	v_mul_f32_e32 v32, 0xbfb8aa3b, v32
	v_exp_f32_e32 v36, v32
	v_min_f32_e32 v23, 0x40e00000, v23
	v_mul_f32_e32 v37, 0x3fd9db23, v23
	v_mul_f32_e32 v37, 0xbfb8aa3b, v37
	v_add_f32_e32 v36, 1.0, v36
	v_rcp_f32_e32 v36, v36
	v_exp_f32_e32 v37, v37
	v_med3_f32 v30, v30, s60, v239
	v_min_f32_e32 v20, 0x40e00000, v20
	v_mul_f32_e32 v22, v22, v36
	v_add_f32_e32 v30, 1.0, v30
	v_mul_f32_e32 v36, 0x3fd9db23, v20
	v_mul_f32_e32 v22, v30, v22
	v_add_f32_e32 v30, 1.0, v37
	v_mul_f32_e32 v36, 0xbfb8aa3b, v36
	v_rcp_f32_e32 v30, v30
	v_exp_f32_e32 v36, v36
	v_med3_f32 v31, v31, s60, v239
	v_min_f32_e32 v21, 0x40e00000, v21
	v_mul_f32_e32 v23, v23, v30
	v_add_f32_e32 v30, 1.0, v31
	v_add_f32_e32 v31, 1.0, v36
	v_mul_f32_e32 v36, 0x3fd9db23, v21
	v_mul_f32_e32 v36, 0xbfb8aa3b, v36
	v_exp_f32_e32 v36, v36
	v_rcp_f32_e32 v31, v31
	v_pk_fma_f32 v[28:29], v[110:111], s[26:27], v[16:17] op_sel_hi:[1,0,1]
	v_mul_f32_e32 v23, v30, v23
	v_add_f32_e32 v30, 1.0, v36
	v_pk_fma_f32 v[26:27], v[112:113], s[26:27], v[6:7] op_sel_hi:[1,0,1]
	v_med3_f32 v28, v28, s60, v239
	v_rcp_f32_e32 v30, v30
	v_mul_f32_e32 v20, v20, v31
	v_add_f32_e32 v28, 1.0, v28
	v_min_f32_e32 v26, 0x40e00000, v26
	v_mul_f32_e32 v28, v28, v20
	v_med3_f32 v20, v29, s60, v239
	v_mul_f32_e32 v29, 0x3fd9db23, v26
	v_mul_f32_e32 v29, 0xbfb8aa3b, v29
	v_mul_f32_e32 v21, v21, v30
	v_add_f32_e32 v20, 1.0, v20
	v_exp_f32_e32 v29, v29
	v_mul_f32_e32 v21, v20, v21
	v_mov_b32_e32 v20, v67
	v_cvt_pk_fp8_f32 v20, v22, v23
	v_min_f32_e32 v23, 0x40e00000, v27
	v_mul_f32_e32 v27, 0x3fd9db23, v23
	v_add_f32_e32 v22, 1.0, v29
	v_mul_f32_e32 v27, 0xbfb8aa3b, v27
	v_rcp_f32_e32 v22, v22
	v_exp_f32_e32 v27, v27
	v_pk_fma_f32 v[24:25], v[114:115], s[26:27], v[8:9] op_sel_hi:[1,0,1]
	v_pk_fma_f32 v[34:35], v[104:105], s[26:27], v[2:3] op_sel_hi:[1,0,1]
	v_mul_f32_e32 v22, v26, v22
	v_add_f32_e32 v26, 1.0, v27
	v_rcp_f32_e32 v26, v26
	v_min_f32_e32 v24, 0x40e00000, v24
	v_min_f32_e32 v25, 0x40e00000, v25
	v_cvt_pk_fp8_f32 v20, v28, v21 op_sel:[0,0,1]
	v_mul_f32_e32 v23, v23, v26
	v_mul_f32_e32 v26, 0x3fd9db23, v24
	v_mul_f32_e32 v26, 0xbfb8aa3b, v26
	v_exp_f32_e32 v26, v26
	v_med3_f32 v21, v34, s60, v239
	v_mul_f32_e32 v27, 0x3fd9db23, v25
	v_add_f32_e32 v21, 1.0, v21
	v_add_f32_e32 v26, 1.0, v26
	v_rcp_f32_e32 v26, v26
	v_mul_f32_e32 v27, 0xbfb8aa3b, v27
	v_mul_f32_e32 v22, v21, v22
	v_med3_f32 v21, v35, s60, v239
	v_exp_f32_e32 v27, v27
	v_pk_fma_f32 v[32:33], v[106:107], s[26:27], v[4:5] op_sel_hi:[1,0,1]
	v_add_f32_e32 v21, 1.0, v21
	v_mul_f32_e32 v23, v21, v23
	v_med3_f32 v21, v32, s60, v239
	v_mul_f32_e32 v24, v24, v26
	v_add_f32_e32 v21, 1.0, v21
	v_mul_f32_e32 v24, v21, v24
	v_add_f32_e32 v21, 1.0, v27
	v_rcp_f32_e32 v26, v21
	v_mov_b32_e32 v21, v67
	v_cvt_pk_fp8_f32 v21, v22, v23
	v_med3_f32 v27, v33, s60, v239
	v_mul_f32_e32 v22, v25, v26
	v_add_f32_e32 v23, 1.0, v27
	v_mul_f32_e32 v22, v23, v22
	v_cvt_pk_fp8_f32 v21, v24, v22 op_sel:[0,0,1]
	v_add_co_u32_e32 v22, vcc, s62, v18
	v_pk_fma_f32 v[30:31], v[100:101], s[26:27], v[14:15] op_sel_hi:[1,0,1]
	s_nop 0
	v_addc_co_u32_e32 v23, vcc, 0, v19, vcc
	global_store_dwordx2 v[22:23], v[20:21], off
	v_pk_fma_f32 v[22:23], v[92:93], s[26:27], v[10:11] op_sel_hi:[1,0,1]
	v_pk_fma_f32 v[20:21], v[94:95], s[26:27], v[12:13] op_sel_hi:[1,0,1]
	v_min_f32_e32 v22, 0x40e00000, v22
	v_mul_f32_e32 v32, 0x3fd9db23, v22
	v_mul_f32_e32 v32, 0xbfb8aa3b, v32
	v_exp_f32_e32 v36, v32
	v_min_f32_e32 v23, 0x40e00000, v23
	v_mul_f32_e32 v37, 0x3fd9db23, v23
	v_mul_f32_e32 v37, 0xbfb8aa3b, v37
	v_add_f32_e32 v36, 1.0, v36
	v_rcp_f32_e32 v36, v36
	v_exp_f32_e32 v37, v37
	v_med3_f32 v30, v30, s60, v239
	v_min_f32_e32 v20, 0x40e00000, v20
	v_mul_f32_e32 v22, v22, v36
	v_add_f32_e32 v30, 1.0, v30
	v_mul_f32_e32 v36, 0x3fd9db23, v20
	v_mul_f32_e32 v22, v30, v22
	v_add_f32_e32 v30, 1.0, v37
	v_mul_f32_e32 v36, 0xbfb8aa3b, v36
	v_rcp_f32_e32 v30, v30
	v_exp_f32_e32 v36, v36
	v_med3_f32 v31, v31, s60, v239
	v_min_f32_e32 v21, 0x40e00000, v21
	v_mul_f32_e32 v23, v23, v30
	v_add_f32_e32 v30, 1.0, v31
	v_add_f32_e32 v31, 1.0, v36
	v_mul_f32_e32 v36, 0x3fd9db23, v21
	v_mul_f32_e32 v36, 0xbfb8aa3b, v36
	v_exp_f32_e32 v36, v36
	v_rcp_f32_e32 v31, v31
	v_pk_fma_f32 v[28:29], v[102:103], s[26:27], v[16:17] op_sel_hi:[1,0,1]
	v_mul_f32_e32 v23, v30, v23
	v_add_f32_e32 v30, 1.0, v36
	v_pk_fma_f32 v[26:27], v[88:89], s[26:27], v[6:7] op_sel_hi:[1,0,1]
	v_med3_f32 v28, v28, s60, v239
	v_rcp_f32_e32 v30, v30
	v_mul_f32_e32 v20, v20, v31
	v_add_f32_e32 v28, 1.0, v28
	v_min_f32_e32 v26, 0x40e00000, v26
	v_mul_f32_e32 v28, v28, v20
	v_med3_f32 v20, v29, s60, v239
	v_mul_f32_e32 v29, 0x3fd9db23, v26
	v_mul_f32_e32 v29, 0xbfb8aa3b, v29
	v_mul_f32_e32 v21, v21, v30
	v_add_f32_e32 v20, 1.0, v20
	v_exp_f32_e32 v29, v29
	v_mul_f32_e32 v21, v20, v21
	v_mov_b32_e32 v20, v67
	v_cvt_pk_fp8_f32 v20, v22, v23
	v_min_f32_e32 v23, 0x40e00000, v27
	v_mul_f32_e32 v27, 0x3fd9db23, v23
	v_add_f32_e32 v22, 1.0, v29
	v_mul_f32_e32 v27, 0xbfb8aa3b, v27
	v_rcp_f32_e32 v22, v22
	v_exp_f32_e32 v27, v27
	v_pk_fma_f32 v[24:25], v[90:91], s[26:27], v[8:9] op_sel_hi:[1,0,1]
	v_pk_fma_f32 v[34:35], v[96:97], s[26:27], v[2:3] op_sel_hi:[1,0,1]
	v_mul_f32_e32 v22, v26, v22
	v_add_f32_e32 v26, 1.0, v27
	v_rcp_f32_e32 v26, v26
	v_min_f32_e32 v24, 0x40e00000, v24
	v_min_f32_e32 v25, 0x40e00000, v25
	v_cvt_pk_fp8_f32 v20, v28, v21 op_sel:[0,0,1]
	v_mul_f32_e32 v23, v23, v26
	v_mul_f32_e32 v26, 0x3fd9db23, v24
	v_mul_f32_e32 v26, 0xbfb8aa3b, v26
	v_exp_f32_e32 v26, v26
	v_med3_f32 v21, v34, s60, v239
	v_mul_f32_e32 v27, 0x3fd9db23, v25
	v_add_f32_e32 v21, 1.0, v21
	v_add_f32_e32 v26, 1.0, v26
	v_rcp_f32_e32 v26, v26
	v_mul_f32_e32 v27, 0xbfb8aa3b, v27
	v_mul_f32_e32 v22, v21, v22
	v_med3_f32 v21, v35, s60, v239
	v_exp_f32_e32 v27, v27
	v_pk_fma_f32 v[32:33], v[98:99], s[26:27], v[4:5] op_sel_hi:[1,0,1]
	v_add_f32_e32 v21, 1.0, v21
	v_mul_f32_e32 v23, v21, v23
	v_med3_f32 v21, v32, s60, v239
	v_mul_f32_e32 v24, v24, v26
	v_add_f32_e32 v21, 1.0, v21
	v_mul_f32_e32 v24, v21, v24
	v_add_f32_e32 v21, 1.0, v27
	v_rcp_f32_e32 v26, v21
	v_mov_b32_e32 v21, v67
	v_cvt_pk_fp8_f32 v21, v22, v23
	v_med3_f32 v27, v33, s60, v239
	v_mul_f32_e32 v22, v25, v26
	v_add_f32_e32 v23, 1.0, v27
	v_mul_f32_e32 v22, v23, v22
	v_cvt_pk_fp8_f32 v21, v24, v22 op_sel:[0,0,1]
	v_add_co_u32_e32 v22, vcc, s63, v18
	v_pk_fma_f32 v[10:11], v[76:77], s[26:27], v[10:11] op_sel_hi:[1,0,1]
	s_nop 0
	v_addc_co_u32_e32 v23, vcc, 0, v19, vcc
	v_min_f32_e32 v10, 0x40e00000, v10
	global_store_dwordx2 v[22:23], v[20:21], off
	v_mul_f32_e32 v20, 0x3fd9db23, v10
	v_mul_f32_e32 v20, 0xbfb8aa3b, v20
	v_exp_f32_e32 v20, v20
	v_min_f32_e32 v11, 0x40e00000, v11
	v_mul_f32_e32 v21, 0x3fd9db23, v11
	v_mul_f32_e32 v21, 0xbfb8aa3b, v21
	v_add_f32_e32 v20, 1.0, v20
	v_rcp_f32_e32 v20, v20
	v_exp_f32_e32 v21, v21
	v_pk_fma_f32 v[12:13], v[78:79], s[26:27], v[12:13] op_sel_hi:[1,0,1]
	v_pk_fma_f32 v[14:15], v[84:85], s[26:27], v[14:15] op_sel_hi:[1,0,1]
	v_min_f32_e32 v12, 0x40e00000, v12
	v_med3_f32 v14, v14, s60, v239
	v_mul_f32_e32 v10, v10, v20
	v_add_f32_e32 v14, 1.0, v14
	v_mul_f32_e32 v20, 0x3fd9db23, v12
	v_mul_f32_e32 v10, v14, v10
	v_add_f32_e32 v14, 1.0, v21
	v_mul_f32_e32 v20, 0xbfb8aa3b, v20
	v_rcp_f32_e32 v14, v14
	v_exp_f32_e32 v20, v20
	v_med3_f32 v15, v15, s60, v239
	v_min_f32_e32 v13, 0x40e00000, v13
	v_mul_f32_e32 v11, v11, v14
	v_add_f32_e32 v14, 1.0, v15
	v_add_f32_e32 v15, 1.0, v20
	v_mul_f32_e32 v20, 0x3fd9db23, v13
	v_mul_f32_e32 v20, 0xbfb8aa3b, v20
	v_rcp_f32_e32 v15, v15
	v_exp_f32_e32 v20, v20
	v_pk_fma_f32 v[6:7], v[72:73], s[26:27], v[6:7] op_sel_hi:[1,0,1]
	v_pk_fma_f32 v[16:17], v[86:87], s[26:27], v[16:17] op_sel_hi:[1,0,1]
	v_mul_f32_e32 v12, v12, v15
	v_add_f32_e32 v15, 1.0, v20
	v_rcp_f32_e32 v15, v15
	v_mul_f32_e32 v11, v14, v11
	v_med3_f32 v14, v16, s60, v239
	v_min_f32_e32 v7, 0x40e00000, v7
	v_mul_f32_e32 v13, v13, v15
	v_min_f32_e32 v15, 0x40e00000, v6
	v_mul_f32_e32 v6, 0x3fd9db23, v15
	v_mul_f32_e32 v6, 0xbfb8aa3b, v6
	v_exp_f32_e32 v16, v6
	v_mov_b32_e32 v6, v67
	v_cvt_pk_fp8_f32 v6, v10, v11
	v_mul_f32_e32 v11, 0x3fd9db23, v7
	v_add_f32_e32 v10, 1.0, v16
	v_rcp_f32_e32 v10, v10
	v_mul_f32_e32 v11, 0xbfb8aa3b, v11
	v_exp_f32_e32 v11, v11
	v_pk_fma_f32 v[2:3], v[80:81], s[26:27], v[2:3] op_sel_hi:[1,0,1]
	v_pk_fma_f32 v[8:9], v[74:75], s[26:27], v[8:9] op_sel_hi:[1,0,1]
	v_med3_f32 v2, v2, s60, v239
	v_mul_f32_e32 v10, v15, v10
	v_add_f32_e32 v2, 1.0, v2
	v_min_f32_e32 v8, 0x40e00000, v8
	v_add_f32_e32 v11, 1.0, v11
	v_mul_f32_e32 v2, v2, v10
	v_mul_f32_e32 v10, 0x3fd9db23, v8
	v_rcp_f32_e32 v11, v11
	v_mul_f32_e32 v10, 0xbfb8aa3b, v10
	v_exp_f32_e32 v10, v10
	v_med3_f32 v3, v3, s60, v239
	v_mul_f32_e32 v7, v7, v11
	v_add_f32_e32 v3, 1.0, v3
	v_min_f32_e32 v9, 0x40e00000, v9
	v_mul_f32_e32 v3, v3, v7
	v_add_f32_e32 v7, 1.0, v10
	v_mul_f32_e32 v10, 0x3fd9db23, v9
	v_rcp_f32_e32 v7, v7
	v_mul_f32_e32 v10, 0xbfb8aa3b, v10
	v_exp_f32_e32 v10, v10
	v_pk_fma_f32 v[4:5], v[82:83], s[26:27], v[4:5] op_sel_hi:[1,0,1]
	v_mul_f32_e32 v7, v8, v7
	v_med3_f32 v4, v4, s60, v239
	v_add_f32_e32 v4, 1.0, v4
	v_mul_f32_e32 v4, v4, v7
	v_add_f32_e32 v7, 1.0, v10
	v_rcp_f32_e32 v8, v7
	v_mov_b32_e32 v7, v67
	v_add_f32_e32 v14, 1.0, v14
	v_cvt_pk_fp8_f32 v7, v2, v3
	v_mul_f32_e32 v12, v14, v12
	v_med3_f32 v14, v17, s60, v239
	v_med3_f32 v5, v5, s60, v239
	v_add_f32_e32 v14, 1.0, v14
	v_mul_f32_e32 v2, v9, v8
	v_add_f32_e32 v3, 1.0, v5
	v_mul_f32_e32 v13, v14, v13
	v_mul_f32_e32 v2, v3, v2
	v_cvt_pk_fp8_f32 v6, v12, v13 op_sel:[0,0,1]
	v_cvt_pk_fp8_f32 v7, v4, v2 op_sel:[0,0,1]
	v_add_co_u32_e32 v2, vcc, 0x58000, v18
	s_nop 1
	v_addc_co_u32_e32 v3, vcc, 0, v19, vcc
	global_store_dwordx2 v[2:3], v[6:7], off
	s_nop 7
	s_and_b64 vcc, exec, s[0:1]
	s_mov_b64 s[0:1], -1
	s_cbranch_vccnz .LBB0_934
	s_andn2_b64 vcc, exec, s[14:15]
	s_cbranch_vccnz .LBB0_933
	s_barrier
	s_branch .LBB0_933

.LBB0_1008:
	v_readlane_b32 s4, v253, 12
	s_cmp_lt_i32 s4, 11
	s_cselect_b64 s[2:3], -1, 0
	s_and_b64 s[2:3], s[2:3], s[0:1]
	s_andn2_b64 vcc, exec, s[2:3]
	v_readlane_b32 s5, v253, 13
	v_readlane_b32 s6, v253, 14
	v_readlane_b32 s7, v253, 15
	s_cbranch_vccnz .LBB0_1040
	s_branch .Lp10_tabs_done
	v_cmp_gt_u32_e32 vcc, 32, v0
	s_waitcnt vmcnt(0) lgkmcnt(0)
	s_barrier
	s_and_saveexec_b64 s[0:1], vcc
	s_cbranch_execz .LBB0_1011
	v_lshlrev_b32_e32 v2, 8, v0
	v_mov_b32_e32 v3, 0
	v_lshl_add_u64 v[2:3], s[92:93], 0, v[2:3]
	v_add_co_u32_e32 v2, vcc, 0x30000, v2
	s_add_i32 s4, 0, 0x23c00
	s_nop 0
	v_addc_co_u32_e32 v3, vcc, 0, v3, vcc
	global_load_dword v1, v[2:3], off sc1
	v_lshl_add_u32 v2, v0, 2, s4
	s_waitcnt vmcnt(0)
	ds_write_b32 v2, v1 offset:256

.Lp10_tabs_done:
	s_add_i32 s0, 0, 0x23cc0
	v_mov_b32_e32 v1, s0
	s_waitcnt lgkmcnt(0)
	s_barrier
	ds_read_b32 v1, v1
	s_mov_b32 s1, 0
	v_readfirstlane_b32 s0, v0
	s_waitcnt lgkmcnt(0)
	v_lshlrev_b32_e32 v200, 3, v1
	v_cmp_ge_i32_e32 vcc, s82, v200
	v_readfirstlane_b32 s21, v1
	s_cbranch_vccnz .LBB0_1040
	s_ashr_i32 s23, s82, 31
	s_lshr_b32 s4, s23, 29
	s_add_i32 s4, s82, s4
	s_ashr_i32 s5, s4, 3
	s_and_b32 s4, s4, -8
	s_sub_i32 s4, s82, s4
	s_lshr_b32 s6, s4, 31
	s_add_i32 s6, s21, s6
	s_mul_i32 s4, s6, s4
	s_add_i32 s4, s4, s5
	s_ashr_i32 s5, s4, 31
	s_lshr_b32 s5, s5, 26
	s_add_i32 s5, s4, s5
	s_ashr_i32 s6, s5, 6
	s_lshl_b32 s6, s6, 3
	s_sub_i32 s7, s21, s6
	s_min_i32 s7, s7, 8
	s_abs_i32 s8, s7
	v_cvt_f32_u32_e32 v1, s8
	s_sub_i32 s10, 0, s8
	s_andn2_b32 s5, s5, 63
	s_sub_i32 s4, s4, s5
	v_rcp_iflag_f32_e32 v1, v1
	s_abs_i32 s5, s4
	s_xor_b32 s9, s4, s7
	s_ashr_i32 s9, s9, 31
	v_mul_f32_e32 v1, 0x4f7ffffe, v1
	v_cvt_u32_f32_e32 v1, v1
	s_nop 0
	v_readfirstlane_b32 s11, v1
	s_mul_i32 s10, s10, s11
	s_mul_hi_u32 s10, s11, s10
	s_add_i32 s11, s11, s10
	s_mul_hi_u32 s10, s5, s11
	s_mul_i32 s11, s10, s8
	s_sub_i32 s5, s5, s11
	s_add_i32 s12, s10, 1
	s_sub_i32 s11, s5, s8
	s_cmp_ge_u32 s5, s8
	s_cselect_b32 s10, s12, s10
	s_cselect_b32 s5, s11, s5
	s_add_i32 s11, s10, 1
	s_cmp_ge_u32 s5, s8
	s_cselect_b32 s5, s11, s10
	s_xor_b32 s5, s5, s9
	s_sub_i32 s36, s5, s9
	s_mul_i32 s5, s36, s7
	s_sub_i32 s4, s4, s5
	s_add_i32 s67, s4, s6
	v_mov_b32_e32 v1, 0

.LBB0_1021:
	s_add_i32 s55, s55, 1
	s_mul_i32 s0, s55, s62
	s_mul_hi_u32 s1, s55, s83
	s_add_i32 s1, s1, s0
	s_mul_i32 s0, s55, s83
	s_add_u32 s0, s0, s82
	s_addc_u32 s1, s1, s23
	v_cmp_ge_i64_e32 vcc, s[0:1], v[200:201]
	v_cmp_lt_i64_e64 s[4:5], s[0:1], v[200:201]
	s_cbranch_vccnz .LBB0_1025
	s_ashr_i32 s1, s0, 31
	s_lshr_b32 s1, s1, 29
	s_add_i32 s1, s0, s1
	s_ashr_i32 s30, s1, 3
	s_and_b32 s1, s1, -8
	s_sub_i32 s0, s0, s1
	s_lshr_b32 s1, s0, 31
	s_add_i32 s1, s21, s1
	s_mul_i32 s0, s1, s0
	s_add_i32 s1, s0, s30
	s_ashr_i32 s0, s1, 31
	s_lshr_b32 s0, s0, 26
	s_add_i32 s30, s1, s0
	s_ashr_i32 s0, s30, 6
	s_lshl_b32 s31, s0, 3
	s_sub_i32 s0, s21, s31
	s_min_i32 s34, s0, 8
	s_abs_i32 s35, s34
	v_cvt_f32_u32_e32 v2, s35
	s_sub_i32 s39, 0, s35
	s_andn2_b32 s30, s30, 63
	s_sub_i32 s1, s1, s30
	v_rcp_iflag_f32_e32 v2, v2
	s_abs_i32 s30, s1
	s_xor_b32 s38, s1, s34
	s_ashr_i32 s38, s38, 31
	v_mul_f32_e32 v2, 0x4f7ffffe, v2
	v_cvt_u32_f32_e32 v2, v2
	s_mov_b32 s0, 0
	v_readfirstlane_b32 s41, v2
	s_mul_i32 s39, s39, s41
	s_mul_hi_u32 s39, s41, s39
	s_add_i32 s41, s41, s39
	s_mul_hi_u32 s39, s30, s41
	s_mul_i32 s41, s39, s35
	s_sub_i32 s30, s30, s41
	s_add_i32 s44, s39, 1
	s_sub_i32 s41, s30, s35
	s_cmp_ge_u32 s30, s35
	s_cselect_b32 s39, s44, s39
	s_cselect_b32 s30, s41, s30
	s_add_i32 s41, s39, 1
	s_cmp_ge_u32 s30, s35
	s_cselect_b32 s30, s41, s39
	s_xor_b32 s30, s30, s38
	s_sub_i32 s30, s30, s38
	s_mul_i32 s34, s30, s34
	s_sub_i32 s1, s1, s34
	s_add_i32 s66, s1, s31
	v_and_b32_e32 v2, 31, v248
	v_lshlrev_b32_e32 v2, 2, v2
	v_add_u32_e32 v2, 0x23c44, v2
	ds_read_b32 v3, v2
	s_waitcnt lgkmcnt(0)
	v_cmp_ge_i32_e32 vcc, s66, v3
	s_nop 1
	s_bcnt1_i32_b32 s34, vcc_lo

.LBB0_1034:
	v_readlane_b32 s68, v253, 4
	s_ashr_i32 s41, s40, 31
	v_readlane_b32 s74, v253, 10
	v_readlane_b32 s75, v253, 11
	s_lshl_b64 s[4:5], s[40:41], 13
	s_mov_b64 s[42:43], s[74:75]
	v_lshl_or_b32 v10, s36, 8, v236
	s_add_u32 s4, s42, s4
	s_addc_u32 s5, s43, s5
	v_ashrrev_i32_e32 v11, 31, v10
	v_lshl_add_u64 v[2:3], v[10:11], 2, s[4:5]
	global_load_dwordx4 v[4:7], v[2:3], off
	global_load_dwordx4 v[22:25], v[2:3], off offset:16
	global_load_dwordx4 v[26:29], v[2:3], off offset:512
	global_load_dwordx4 v[30:33], v[2:3], off offset:528
	s_and_b64 vcc, exec, s[18:19]
	s_cbranch_vccz .LBB0_1036
	s_barrier
.LBB0_1036:
	s_nop 15
	s_nop 15
	v_lshl_add_u32 v34, s67, 8, v215
	v_or_b32_e32 v2, 16, v34
	v_ashrrev_i32_e32 v35, 31, v34
	v_or_b32_e32 v8, 32, v34
	v_ashrrev_i32_e32 v3, 31, v2
	v_mov_b32_e32 v37, v67
	v_lshlrev_b64 v[12:13], 11, v[34:35]
	v_ashrrev_i32_e32 v9, 31, v8
	v_lshlrev_b64 v[14:15], 11, v[2:3]
	v_lshl_add_u64 v[12:13], s[12:13], 0, v[12:13]
	v_lshlrev_b64 v[48:49], 11, v[8:9]
	v_lshl_add_u64 v[8:9], s[12:13], 0, v[14:15]
	v_mov_b32_e32 v36, v67
	v_mov_b32_e32 v44, v67
	v_mov_b32_e32 v45, v67
	v_lshl_add_u64 v[2:3], v[12:13], 0, v[10:11]
	v_lshl_add_u64 v[50:51], v[8:9], 0, v[10:11]
	v_mov_b32_e32 v38, v67
	v_mov_b32_e32 v39, v67
	v_mov_b32_e32 v46, v67
	v_mov_b32_e32 v47, v67
	v_mov_b32_e32 v40, v67
	v_mov_b32_e32 v41, v67
	v_mov_b32_e32 v42, v67
	v_mov_b32_e32 v43, v67
	v_readlane_b32 s69, v253, 5
	v_readlane_b32 s70, v253, 6
	v_readlane_b32 s71, v253, 7
	v_readlane_b32 s72, v253, 8
	v_readlane_b32 s73, v253, 9
	s_waitcnt vmcnt(0)
	v_pk_mul_f32 v[20:21], v[4:5], s[20:21] op_sel_hi:[1,0]
	v_pk_mul_f32 v[18:19], v[22:23], s[20:21] op_sel_hi:[1,0]
	v_pk_mul_f32 v[4:5], v[28:29], s[20:21] op_sel_hi:[1,0]
	v_pk_fma_f32 v[28:29], v[192:193], s[22:23], v[18:19] op_sel_hi:[1,0,1]
	v_pk_mul_f32 v[14:15], v[6:7], s[20:21] op_sel_hi:[1,0]
	v_pk_mul_f32 v[6:7], v[32:33], s[20:21] op_sel_hi:[1,0]
	v_cvt_pk_fp8_f32 v37, v28, v29
	v_pk_mul_f32 v[16:17], v[24:25], s[20:21] op_sel_hi:[1,0]
	v_pk_mul_f32 v[12:13], v[26:27], s[20:21] op_sel_hi:[1,0]
	v_pk_mul_f32 v[8:9], v[30:31], s[20:21] op_sel_hi:[1,0]
	v_pk_fma_f32 v[24:25], v[196:197], s[22:23], v[20:21] op_sel_hi:[1,0,1]
	v_pk_fma_f32 v[52:53], v[170:171], s[22:23], v[6:7] op_sel_hi:[1,0,1]
	v_pk_fma_f32 v[64:65], v[166:167], s[22:23], v[4:5] op_sel_hi:[1,0,1]
	v_pk_fma_f32 v[166:167], v[180:181], s[22:23], v[20:21] op_sel_hi:[1,0,1]
	v_pk_fma_f32 v[170:171], v[172:173], s[22:23], v[18:19] op_sel_hi:[1,0,1]
	v_pk_fma_f32 v[32:33], v[176:177], s[22:23], v[12:13] op_sel_hi:[1,0,1]
	v_pk_fma_f32 v[54:55], v[168:169], s[22:23], v[8:9] op_sel_hi:[1,0,1]
	v_pk_fma_f32 v[156:157], v[156:157], s[22:23], v[12:13] op_sel_hi:[1,0,1]
	v_pk_fma_f32 v[152:153], v[152:153], s[22:23], v[8:9] op_sel_hi:[1,0,1]
	v_cvt_pk_fp8_f32 v36, v24, v25
	v_cvt_pk_fp8_f32 v44, v166, v167
	v_cvt_pk_fp8_f32 v45, v170, v171
	v_pk_fma_f32 v[26:27], v[194:195], s[22:23], v[16:17] op_sel_hi:[1,0,1]
	v_pk_fma_f32 v[58:59], v[188:189], s[22:23], v[20:21] op_sel_hi:[1,0,1]
	v_pk_fma_f32 v[62:63], v[184:185], s[22:23], v[18:19] op_sel_hi:[1,0,1]
	v_cvt_pk_fp8_f32 v38, v32, v33
	v_cvt_pk_fp8_f32 v39, v54, v55
	v_cvt_pk_fp8_f32 v46, v156, v157
	v_cvt_pk_fp8_f32 v47, v152, v153
	v_pk_fma_f32 v[68:69], v[164:165], s[22:23], v[12:13] op_sel_hi:[1,0,1]
	v_pk_fma_f32 v[160:161], v[160:161], s[22:23], v[8:9] op_sel_hi:[1,0,1]
	v_cvt_pk_fp8_f32 v40, v58, v59
	v_cvt_pk_fp8_f32 v41, v62, v63
	v_cvt_pk_fp8_f32 v37, v26, v27 op_sel:[0,0,1]
	v_pk_fma_f32 v[24:25], v[148:149], s[22:23], v[20:21] op_sel_hi:[1,0,1]
	v_pk_fma_f32 v[26:27], v[144:145], s[22:23], v[18:19] op_sel_hi:[1,0,1]
	v_mov_b32_e32 v28, v67
	v_mov_b32_e32 v29, v67
	v_pk_fma_f32 v[22:23], v[198:199], s[22:23], v[14:15] op_sel_hi:[1,0,1]
	v_pk_fma_f32 v[164:165], v[182:183], s[22:23], v[14:15] op_sel_hi:[1,0,1]
	v_pk_fma_f32 v[168:169], v[174:175], s[22:23], v[16:17] op_sel_hi:[1,0,1]
	v_cvt_pk_fp8_f32 v42, v68, v69
	v_cvt_pk_fp8_f32 v43, v160, v161
	v_cvt_pk_fp8_f32 v28, v24, v25
	v_cvt_pk_fp8_f32 v29, v26, v27
	v_pk_fma_f32 v[30:31], v[178:179], s[22:23], v[4:5] op_sel_hi:[1,0,1]
	v_pk_fma_f32 v[158:159], v[158:159], s[22:23], v[4:5] op_sel_hi:[1,0,1]
	v_pk_fma_f32 v[154:155], v[154:155], s[22:23], v[6:7] op_sel_hi:[1,0,1]
	v_cvt_pk_fp8_f32 v36, v22, v23 op_sel:[0,0,1]
	v_cvt_pk_fp8_f32 v44, v164, v165 op_sel:[0,0,1]
	v_cvt_pk_fp8_f32 v45, v168, v169 op_sel:[0,0,1]
	v_pk_fma_f32 v[56:57], v[190:191], s[22:23], v[14:15] op_sel_hi:[1,0,1]
	v_pk_fma_f32 v[60:61], v[186:187], s[22:23], v[16:17] op_sel_hi:[1,0,1]
	v_cvt_pk_fp8_f32 v38, v30, v31 op_sel:[0,0,1]
	v_cvt_pk_fp8_f32 v39, v52, v53 op_sel:[0,0,1]
	v_cvt_pk_fp8_f32 v46, v158, v159 op_sel:[0,0,1]
	v_cvt_pk_fp8_f32 v47, v154, v155 op_sel:[0,0,1]
	v_pk_fma_f32 v[162:163], v[162:163], s[22:23], v[6:7] op_sel_hi:[1,0,1]
	v_cvt_pk_fp8_f32 v40, v56, v57 op_sel:[0,0,1]
	v_cvt_pk_fp8_f32 v41, v60, v61 op_sel:[0,0,1]
	v_lshl_add_u64 v[22:23], s[12:13], 0, v[48:49]
	v_pk_fma_f32 v[24:25], v[150:151], s[22:23], v[14:15] op_sel_hi:[1,0,1]
	v_pk_fma_f32 v[26:27], v[146:147], s[22:23], v[16:17] op_sel_hi:[1,0,1]
	v_cvt_pk_fp8_f32 v42, v64, v65 op_sel:[0,0,1]
	v_cvt_pk_fp8_f32 v43, v162, v163 op_sel:[0,0,1]
	v_lshl_add_u64 v[22:23], v[22:23], 0, v[10:11]
	v_cvt_pk_fp8_f32 v28, v24, v25 op_sel:[0,0,1]
	v_cvt_pk_fp8_f32 v29, v26, v27 op_sel:[0,0,1]
	v_pk_fma_f32 v[24:25], v[140:141], s[22:23], v[12:13] op_sel_hi:[1,0,1]
	v_pk_fma_f32 v[26:27], v[136:137], s[22:23], v[8:9] op_sel_hi:[1,0,1]
	v_mov_b32_e32 v30, v67
	v_mov_b32_e32 v31, v67
	global_store_dwordx2 v[2:3], v[36:37], off
	global_store_dwordx2 v[2:3], v[38:39], off offset:128
	global_store_dwordx2 v[50:51], v[40:41], off
	global_store_dwordx2 v[50:51], v[42:43], off offset:128
	global_store_dwordx2 v[22:23], v[44:45], off
	global_store_dwordx2 v[22:23], v[46:47], off offset:128
	v_or_b32_e32 v22, 48, v34
	v_cvt_pk_fp8_f32 v30, v24, v25
	v_cvt_pk_fp8_f32 v31, v26, v27
	v_ashrrev_i32_e32 v23, 31, v22
	v_lshlrev_b64 v[22:23], 11, v[22:23]
	v_pk_fma_f32 v[24:25], v[142:143], s[22:23], v[4:5] op_sel_hi:[1,0,1]
	v_pk_fma_f32 v[26:27], v[138:139], s[22:23], v[6:7] op_sel_hi:[1,0,1]
	v_lshl_add_u64 v[22:23], s[12:13], 0, v[22:23]
	v_cvt_pk_fp8_f32 v30, v24, v25 op_sel:[0,0,1]
	v_cvt_pk_fp8_f32 v31, v26, v27 op_sel:[0,0,1]
	v_lshl_add_u64 v[10:11], v[22:23], 0, v[10:11]
	v_pk_fma_f32 v[22:23], v[132:133], s[22:23], v[20:21] op_sel_hi:[1,0,1]
	v_pk_fma_f32 v[24:25], v[128:129], s[22:23], v[18:19] op_sel_hi:[1,0,1]
	v_mov_b32_e32 v26, v67
	v_mov_b32_e32 v27, v67
	v_cvt_pk_fp8_f32 v26, v22, v23
	v_cvt_pk_fp8_f32 v27, v24, v25
	v_pk_fma_f32 v[22:23], v[134:135], s[22:23], v[14:15] op_sel_hi:[1,0,1]
	v_pk_fma_f32 v[24:25], v[130:131], s[22:23], v[16:17] op_sel_hi:[1,0,1]
	global_store_dwordx2 v[10:11], v[28:29], off
	global_store_dwordx2 v[10:11], v[30:31], off offset:128
	v_cvt_pk_fp8_f32 v26, v22, v23 op_sel:[0,0,1]
	v_cvt_pk_fp8_f32 v27, v24, v25 op_sel:[0,0,1]
	v_pk_fma_f32 v[22:23], v[124:125], s[22:23], v[12:13] op_sel_hi:[1,0,1]
	v_pk_fma_f32 v[24:25], v[108:109], s[22:23], v[8:9] op_sel_hi:[1,0,1]
	v_mov_b32_e32 v28, v67
	v_mov_b32_e32 v29, v67
	v_cvt_pk_fp8_f32 v28, v22, v23
	v_cvt_pk_fp8_f32 v29, v24, v25
	v_pk_fma_f32 v[22:23], v[126:127], s[22:23], v[4:5] op_sel_hi:[1,0,1]
	v_pk_fma_f32 v[24:25], v[110:111], s[22:23], v[6:7] op_sel_hi:[1,0,1]
	v_cvt_pk_fp8_f32 v28, v22, v23 op_sel:[0,0,1]
	v_cvt_pk_fp8_f32 v29, v24, v25 op_sel:[0,0,1]
	v_add_co_u32_e32 v22, vcc, s54, v2
	v_lshl_add_u64 v[10:11], v[2:3], 0, s[8:9]
	s_nop 0
	v_addc_co_u32_e32 v23, vcc, 0, v3, vcc
	global_store_dwordx2 v[22:23], v[26:27], off
	global_store_dwordx2 v[10:11], v[28:29], off offset:128
	v_pk_fma_f32 v[22:23], v[116:117], s[22:23], v[20:21] op_sel_hi:[1,0,1]
	v_pk_fma_f32 v[24:25], v[104:105], s[22:23], v[18:19] op_sel_hi:[1,0,1]
	v_mov_b32_e32 v26, v67
	v_mov_b32_e32 v27, v67
	v_cvt_pk_fp8_f32 v26, v22, v23
	v_cvt_pk_fp8_f32 v27, v24, v25
	v_pk_fma_f32 v[22:23], v[118:119], s[22:23], v[14:15] op_sel_hi:[1,0,1]
	v_pk_fma_f32 v[24:25], v[106:107], s[22:23], v[16:17] op_sel_hi:[1,0,1]
	v_cvt_pk_fp8_f32 v26, v22, v23 op_sel:[0,0,1]
	v_cvt_pk_fp8_f32 v27, v24, v25 op_sel:[0,0,1]
	v_pk_fma_f32 v[22:23], v[92:93], s[22:23], v[12:13] op_sel_hi:[1,0,1]
	v_pk_fma_f32 v[24:25], v[80:81], s[22:23], v[8:9] op_sel_hi:[1,0,1]
	v_mov_b32_e32 v28, v67
	v_mov_b32_e32 v29, v67
	v_cvt_pk_fp8_f32 v28, v22, v23
	v_cvt_pk_fp8_f32 v29, v24, v25
	v_pk_fma_f32 v[22:23], v[94:95], s[22:23], v[4:5] op_sel_hi:[1,0,1]
	v_pk_fma_f32 v[24:25], v[82:83], s[22:23], v[6:7] op_sel_hi:[1,0,1]
	v_cvt_pk_fp8_f32 v28, v22, v23 op_sel:[0,0,1]
	v_cvt_pk_fp8_f32 v29, v24, v25 op_sel:[0,0,1]
	v_add_co_u32_e32 v22, vcc, s63, v2
	v_lshl_add_u64 v[10:11], v[2:3], 0, s[24:25]
	s_nop 0
	v_addc_co_u32_e32 v23, vcc, 0, v3, vcc
	global_store_dwordx2 v[22:23], v[26:27], off
	global_store_dwordx2 v[10:11], v[28:29], off offset:128
	v_pk_fma_f32 v[22:23], v[88:89], s[22:23], v[20:21] op_sel_hi:[1,0,1]
	v_pk_fma_f32 v[24:25], v[84:85], s[22:23], v[18:19] op_sel_hi:[1,0,1]
	v_mov_b32_e32 v26, v67
	v_mov_b32_e32 v27, v67
	v_cvt_pk_fp8_f32 v26, v22, v23
	v_cvt_pk_fp8_f32 v27, v24, v25
	v_pk_fma_f32 v[22:23], v[90:91], s[22:23], v[14:15] op_sel_hi:[1,0,1]
	v_pk_fma_f32 v[24:25], v[86:87], s[22:23], v[16:17] op_sel_hi:[1,0,1]
	v_cvt_pk_fp8_f32 v26, v22, v23 op_sel:[0,0,1]
	v_cvt_pk_fp8_f32 v27, v24, v25 op_sel:[0,0,1]
	v_pk_fma_f32 v[22:23], v[112:113], s[22:23], v[12:13] op_sel_hi:[1,0,1]
	v_pk_fma_f32 v[24:25], v[120:121], s[22:23], v[8:9] op_sel_hi:[1,0,1]
	v_mov_b32_e32 v28, v67
	v_mov_b32_e32 v29, v67
	v_cvt_pk_fp8_f32 v28, v22, v23
	v_cvt_pk_fp8_f32 v29, v24, v25
	v_pk_fma_f32 v[22:23], v[114:115], s[22:23], v[4:5] op_sel_hi:[1,0,1]
	v_pk_fma_f32 v[24:25], v[122:123], s[22:23], v[6:7] op_sel_hi:[1,0,1]
	v_cvt_pk_fp8_f32 v28, v22, v23 op_sel:[0,0,1]
	v_cvt_pk_fp8_f32 v29, v24, v25 op_sel:[0,0,1]
	v_add_co_u32_e32 v22, vcc, s64, v2
	v_lshl_add_u64 v[10:11], v[2:3], 0, s[26:27]
	s_nop 0
	v_addc_co_u32_e32 v23, vcc, 0, v3, vcc
	global_store_dwordx2 v[22:23], v[26:27], off
	global_store_dwordx2 v[10:11], v[28:29], off offset:128
	v_pk_fma_f32 v[20:21], v[76:77], s[22:23], v[20:21] op_sel_hi:[1,0,1]
	v_mov_b32_e32 v22, v67
	v_cvt_pk_fp8_f32 v22, v20, v21
	v_pk_fma_f32 v[18:19], v[72:73], s[22:23], v[18:19] op_sel_hi:[1,0,1]
	v_mov_b32_e32 v23, v67
	v_pk_fma_f32 v[14:15], v[78:79], s[22:23], v[14:15] op_sel_hi:[1,0,1]
	v_cvt_pk_fp8_f32 v23, v18, v19
	v_cvt_pk_fp8_f32 v22, v14, v15 op_sel:[0,0,1]
	v_pk_fma_f32 v[12:13], v[96:97], s[22:23], v[12:13] op_sel_hi:[1,0,1]
	v_pk_fma_f32 v[8:9], v[100:101], s[22:23], v[8:9] op_sel_hi:[1,0,1]
	v_mov_b32_e32 v14, v67
	v_mov_b32_e32 v15, v67
	v_cvt_pk_fp8_f32 v14, v12, v13
	v_cvt_pk_fp8_f32 v15, v8, v9
	v_pk_fma_f32 v[16:17], v[74:75], s[22:23], v[16:17] op_sel_hi:[1,0,1]
	v_pk_fma_f32 v[4:5], v[98:99], s[22:23], v[4:5] op_sel_hi:[1,0,1]
	v_cvt_pk_fp8_f32 v23, v16, v17 op_sel:[0,0,1]
	v_pk_fma_f32 v[6:7], v[102:103], s[22:23], v[6:7] op_sel_hi:[1,0,1]
	v_cvt_pk_fp8_f32 v14, v4, v5 op_sel:[0,0,1]
	v_cvt_pk_fp8_f32 v15, v6, v7 op_sel:[0,0,1]
	v_lshl_add_u64 v[10:11], v[2:3], 0, s[28:29]
	v_add_co_u32_e32 v2, vcc, s65, v2
	s_nop 1
	v_addc_co_u32_e32 v3, vcc, 0, v3, vcc
	global_store_dwordx2 v[2:3], v[22:23], off
	global_store_dwordx2 v[10:11], v[14:15], off offset:128
	s_nop 7
	s_and_b64 vcc, exec, s[0:1]
	s_mov_b64 s[0:1], -1
	s_cbranch_vccnz .LBB0_1020
	s_andn2_b64 vcc, exec, s[10:11]
	s_cbranch_vccnz .LBB0_1019
	s_barrier
	s_branch .LBB0_1019

.LBB0_1094:
	v_readlane_b32 s4, v253, 12
	s_cmp_lt_i32 s4, 12
	s_cselect_b64 s[2:3], -1, 0
	s_and_b64 s[0:1], s[2:3], s[0:1]
	s_andn2_b64 vcc, exec, s[0:1]
	v_readlane_b32 s5, v253, 13
	v_readlane_b32 s6, v253, 14
	v_readlane_b32 s7, v253, 15
	s_cbranch_vccnz .LBB0_1104
	s_branch .Lp11_tabs_done
	v_cmp_gt_u32_e32 vcc, 32, v0
	s_waitcnt vmcnt(0) lgkmcnt(0)
	s_barrier
	s_and_saveexec_b64 s[0:1], vcc
	s_cbranch_execz .LBB0_1097
	v_lshlrev_b32_e32 v2, 8, v0
	v_mov_b32_e32 v3, 0
	v_lshl_add_u64 v[2:3], s[92:93], 0, v[2:3]
	v_add_co_u32_e32 v2, vcc, 0x30000, v2
	s_add_i32 s2, 0, 0x23c00
	s_nop 0
	v_addc_co_u32_e32 v3, vcc, 0, v3, vcc
	global_load_dword v1, v[2:3], off sc1
	v_lshl_add_u32 v0, v0, 2, s2
	s_waitcnt vmcnt(0)
	ds_write_b32 v0, v1 offset:256

.Lp11_tabs_done:
	s_lshl_b32 s0, s82, 3
	s_add_i32 s8, s84, s0
	s_cmpk_gt_i32 s8, 0x3fff
	s_waitcnt lgkmcnt(0)
	s_barrier
	s_cbranch_scc1 .LBB0_1104
	s_add_u32 s10, s92, 0x8c100000
	s_addc_u32 s11, s93, 0
	s_add_u32 s22, s92, 0x9e400000
	s_addc_u32 s23, s93, 0
	s_lshl_b32 s12, s83, 3
	s_add_u32 s24, s92, 0x9e300000
	s_addc_u32 s25, s93, 0
	s_add_u32 s26, s92, 0x9e500000
	s_addc_u32 s27, s93, 0
	s_lshl_b32 s0, s8, 2
	s_ashr_i32 s1, s0, 31
	s_lshl_b64 s[0:1], s[0:1], 2
	s_add_u32 s2, s24, s0
	s_addc_u32 s3, s25, s1
	v_readlane_b32 s16, v253, 0
	s_add_u32 s4, s22, s0
	v_lshlrev_b32_e32 v64, 5, v248
	v_readlane_b32 s17, v253, 1
	s_addc_u32 s5, s23, s1
	v_mov_b32_e32 v65, 0
	s_nop 2
	global_load_dwordx4 v[0:3], v64, s[16:17] offset:16
	global_load_dwordx4 v[4:7], v64, s[16:17]
	global_load_dwordx4 v[8:11], v64, s[16:17] offset:2064
	global_load_dwordx4 v[12:15], v64, s[16:17] offset:2048
	s_add_u32 s0, s26, s0
	v_or_b32_e32 v24, 0x1000, v64
	global_load_dwordx4 v[48:51], v65, s[2:3]
	global_load_dwordx4 v[32:35], v65, s[4:5]
	global_load_dwordx4 v[16:19], v24, s[16:17] offset:16
	global_load_dwordx4 v[20:23], v24, s[16:17]
	s_addc_u32 s1, s27, s1
	v_or_b32_e32 v36, 0x1800, v64
	global_load_dwordx4 v[44:47], v65, s[0:1]
	global_load_dwordx4 v[24:27], v36, s[16:17] offset:16
	global_load_dwordx4 v[28:31], v36, s[16:17]
	v_mbcnt_lo_u32_b32 v36, -1, 0
	v_mbcnt_hi_u32_b32 v36, -1, v36
	v_and_b32_e32 v37, 64, v36
	v_xor_b32_e32 v38, 1, v36
	v_add_u32_e32 v37, 64, v37
	v_xor_b32_e32 v39, 2, v36
	v_cmp_lt_i32_e32 vcc, v38, v37
	v_xor_b32_e32 v40, 4, v36
	v_xor_b32_e32 v41, 8, v36
	v_cndmask_b32_e32 v38, v36, v38, vcc
	v_cmp_lt_i32_e32 vcc, v39, v37
	v_xor_b32_e32 v42, 16, v36
	s_ashr_i32 s9, s8, 31
	v_cndmask_b32_e32 v39, v36, v39, vcc
	v_cmp_lt_i32_e32 vcc, v40, v37
	v_readlane_b32 s18, v253, 2
	v_xor_b32_e32 v43, 32, v36
	v_cndmask_b32_e32 v40, v36, v40, vcc
	v_cmp_lt_i32_e32 vcc, v41, v37
	s_lshl_b64 s[4:5], s[8:9], 13
	v_readlane_b32 s19, v253, 3
	v_cndmask_b32_e32 v41, v36, v41, vcc
	v_cmp_lt_i32_e32 vcc, v42, v37
	s_add_u32 s4, s18, s4
	s_addc_u32 s5, s19, s5
	v_cndmask_b32_e32 v42, v36, v42, vcc
	v_cmp_lt_i32_e32 vcc, v43, v37
	s_ashr_i32 s13, s12, 31
	s_add_i32 s16, s8, s12
	v_cndmask_b32_e32 v36, v36, v43, vcc
	s_mov_b64 s[0:1], 0x1000
	v_lshlrev_b32_e32 v78, 2, v36
	s_lshl_b32 s29, s83, 5
	s_lshl_b64 s[6:7], s[8:9], 12
	v_lshl_add_u64 v[36:37], s[4:5], 0, v[64:65]
	s_lshl_b64 s[14:15], s[12:13], 13
	s_lshl_b32 s16, s16, 2
	v_lshl_add_u64 v[68:69], v[36:37], 0, s[0:1]
	s_add_u32 s0, s92, s6
	v_lshlrev_b32_e32 v64, 4, v248
	s_addc_u32 s1, s93, s7
	s_mov_b64 s[2:3], 0x72100000
	v_lshl_add_u64 v[36:37], s[0:1], 0, v[64:65]
	v_lshlrev_b32_e32 v73, 2, v38
	v_lshlrev_b32_e32 v74, 2, v39
	v_lshl_add_u64 v[70:71], v[36:37], 0, s[2:3]
	v_lshlrev_b32_e32 v66, 3, v248
	v_mov_b32_e32 v72, 0x3727c5ac
	s_mov_b32 s28, 0x800000
	v_mov_b32_e32 v67, v65
	v_lshlrev_b32_e32 v75, 2, v40
	v_lshlrev_b32_e32 v76, 2, v41
	v_lshlrev_b32_e32 v77, 2, v42
	s_lshl_b64 s[18:19], s[12:13], 12
	s_add_i32 s9, 0, 0x23c00
	s_waitcnt vmcnt(5)
	v_readfirstlane_b32 s4, v32
	v_readfirstlane_b32 s5, v33
	v_readfirstlane_b32 s6, v34
	v_readfirstlane_b32 s7, v35
	s_mov_b64 s[0:1], s[4:5]
	s_waitcnt vmcnt(2)
	v_mov_b64_e32 v[36:37], v[44:45]
	v_mov_b64_e32 v[32:33], v[48:49]
	s_mov_b64 s[2:3], s[6:7]
	v_mov_b64_e32 v[38:39], v[46:47]
	v_mov_b64_e32 v[34:35], v[50:51]
	s_branch .LBB0_1102
